# baseline (speedup 1.0000x reference)
_Z11jacobi_mainPKfS0_S0_PyPf:
	s_lshl_b32 s3, s2, 3
	s_load_dwordx4 s[12:15], s[0:1], 0x0
	s_load_dwordx2 s[4:5], s[0:1], 0x10
	s_and_b32 s3, s3, 56
	s_ashr_i32 s33, s2, 5
	v_readfirstlane_b32 s40, v0
	s_add_i32 s18, s3, s33
	s_bfe_u32 s3, s2, 0x20003
	s_lshl_b32 s7, s3, 8
	s_and_b32 s10, s40, 0xffffffc0
	s_ashr_i32 s19, s18, 31
	s_lshr_b32 s34, s2, 3
	s_add_i32 s11, s10, s7
	s_lshl_b64 s[8:9], s[18:19], 22
	v_and_b32_e32 v206, 63, v0
	s_waitcnt lgkmcnt(0)
	s_add_u32 s8, s12, s8
	s_addc_u32 s9, s13, s9
	v_or_b32_e32 v154, s11, v206
	s_lshl_b32 s6, s18, 10
	v_add_u32_e32 v2, s6, v154
	v_ashrrev_i32_e32 v3, 31, v2
	v_lshlrev_b64 v[2:3], 2, v[2:3]
	v_lshl_add_u64 v[4:5], s[14:15], 0, v[2:3]
	global_load_dword v1, v[4:5], off
	s_movk_i32 s12, 0x1004
	v_mov_b64_e32 v[4:5], s[8:9]
	v_mad_i64_i32 v[4:5], s[12:13], v154, s12, v[4:5]
	v_lshl_add_u64 v[2:3], s[4:5], 0, v[2:3]
	global_load_dword v207, v[4:5], off
	global_load_dword v66, v[2:3], off
	s_lshl_b32 s76, s6, 2
	s_add_u32 s76, s4, s76
	s_addc_u32 s77, s5, 0
	v_lshlrev_b32_e32 v220, 4, v0
	global_load_dwordx4 v[224:227], v220, s[76:77]
	s_load_dwordx2 s[16:17], s[0:1], 0x20
	v_ashrrev_i32_e32 v155, 31, v154
	s_mov_b32 s21, 0
	s_lshr_b32 s35, s40, 6
	v_cmp_eq_u32_e64 s[12:13], 0, v206
	s_load_dwordx2 s[0:1], s[0:1], 0x18
	v_lshrrev_b32_e32 v67, 5, v206
	v_or_b32_e32 v132, s11, v67
	s_lshl_b64 s[14:15], s[18:19], 14
	v_ashrrev_i32_e32 v133, 31, v132
	v_and_b32_e32 v124, 31, v0
	s_waitcnt lgkmcnt(0)
	s_add_u32 s14, s0, s14
	v_lshlrev_b64 v[2:3], 12, v[132:133]
	s_addc_u32 s15, s1, s15
	s_add_i32 s0, s7, 0x100
	v_lshl_add_u64 v[2:3], s[8:9], 0, v[2:3]
	v_lshlrev_b32_e32 v190, 4, v124
	v_mov_b32_e32 v191, 0
	s_and_b32 s26, s0, 0x300
	v_lshl_add_u64 v[130:131], v[2:3], 0, v[190:191]
	s_mov_b64 s[0:1], 0x30000
	v_lshl_add_u64 v[126:127], v[130:131], 0, s[0:1]
	s_mov_b64 s[0:1], 0x32000
	v_lshl_add_u64 v[128:129], v[130:131], 0, s[0:1]
	s_mov_b64 s[0:1], 0x34000
	v_lshl_add_u64 v[134:135], v[130:131], 0, s[0:1]
	s_mov_b64 s[0:1], 0x36000
	v_lshl_add_u64 v[136:137], v[130:131], 0, s[0:1]
	s_mov_b64 s[0:1], 0x38000
	v_lshl_add_u64 v[138:139], v[130:131], 0, s[0:1]
	s_mov_b64 s[0:1], 0x3a000
	v_lshl_add_u64 v[140:141], v[130:131], 0, s[0:1]
	s_mov_b64 s[0:1], 0x3c000
	s_or_b32 s24, s7, 0x80
	v_lshl_add_u64 v[142:143], v[130:131], 0, s[0:1]
	s_mov_b64 s[0:1], 0x3e000
	s_lshl_b32 s20, s7, 2
	v_lshl_add_u64 v[144:145], v[130:131], 0, s[0:1]
	s_lshl_b32 s8, s24, 2
	s_mov_b32 s9, s21
	v_lshl_add_u64 v[2:3], v[126:127], 0, s[20:21]
	v_lshl_add_u64 v[4:5], v[128:129], 0, s[20:21]
	v_lshl_add_u64 v[6:7], v[134:135], 0, s[20:21]
	v_lshl_add_u64 v[8:9], v[136:137], 0, s[20:21]
	v_lshl_add_u64 v[10:11], v[138:139], 0, s[20:21]
	v_lshl_add_u64 v[12:13], v[140:141], 0, s[20:21]
	v_lshl_add_u64 v[14:15], v[142:143], 0, s[20:21]
	v_lshl_add_u64 v[16:17], v[144:145], 0, s[20:21]
	v_lshl_add_u64 v[18:19], v[126:127], 0, s[8:9]
	v_lshl_add_u64 v[20:21], v[128:129], 0, s[8:9]
	v_lshl_add_u64 v[22:23], v[134:135], 0, s[8:9]
	v_lshl_add_u64 v[24:25], v[136:137], 0, s[8:9]
	s_lshl_b32 s0, s26, 2
	s_mov_b32 s1, s21
	v_lshl_add_u64 v[72:73], v[138:139], 0, s[8:9]
	v_lshl_add_u64 v[102:103], v[140:141], 0, s[8:9]
	v_lshl_add_u64 v[104:105], v[142:143], 0, s[8:9]
	v_lshl_add_u64 v[106:107], v[144:145], 0, s[8:9]
	v_lshl_add_u64 v[108:109], v[126:127], 0, s[0:1]
	v_lshl_add_u64 v[110:111], v[128:129], 0, s[0:1]
	v_lshl_add_u64 v[112:113], v[134:135], 0, s[0:1]
	v_lshl_add_u64 v[114:115], v[136:137], 0, s[0:1]
	v_lshl_add_u64 v[116:117], v[138:139], 0, s[0:1]
	v_lshl_add_u64 v[118:119], v[140:141], 0, s[0:1]
	v_lshl_add_u64 v[120:121], v[142:143], 0, s[0:1]
	v_lshl_add_u64 v[122:123], v[144:145], 0, s[0:1]
	global_load_dwordx4 v[68:71], v[2:3], off sc0 sc1 nt
	global_load_dwordx4 v[78:81], v[4:5], off sc0 sc1 nt
	global_load_dwordx4 v[82:85], v[6:7], off sc0 sc1 nt
	global_load_dwordx4 v[90:93], v[8:9], off sc0 sc1 nt
	global_load_dwordx4 v[98:101], v[10:11], off sc0 sc1 nt
	global_load_dwordx4 v[62:65], v[12:13], off sc0 sc1 nt
	global_load_dwordx4 v[54:57], v[14:15], off sc0 sc1 nt
	global_load_dwordx4 v[46:49], v[16:17], off sc0 sc1 nt
	global_load_dwordx4 v[94:97], v[18:19], off sc0 sc1 nt
	global_load_dwordx4 v[86:89], v[20:21], off sc0 sc1 nt
	global_load_dwordx4 v[74:77], v[22:23], off sc0 sc1 nt
	global_load_dwordx4 v[58:61], v[24:25], off sc0 sc1 nt
	global_load_dwordx4 v[50:53], v[72:73], off sc0 sc1 nt
	global_load_dwordx4 v[42:45], v[102:103], off sc0 sc1 nt
	global_load_dwordx4 v[38:41], v[104:105], off sc0 sc1 nt
	global_load_dwordx4 v[34:37], v[106:107], off sc0 sc1 nt
	global_load_dwordx4 v[30:33], v[108:109], off sc0 sc1 nt
	global_load_dwordx4 v[26:29], v[110:111], off sc0 sc1 nt
	s_nop 0
	global_load_dwordx4 v[22:25], v[112:113], off sc0 sc1 nt
	global_load_dwordx4 v[18:21], v[114:115], off sc0 sc1 nt
	global_load_dwordx4 v[14:17], v[116:117], off sc0 sc1 nt
	global_load_dwordx4 v[10:13], v[118:119], off sc0 sc1 nt
	global_load_dwordx4 v[6:9], v[120:121], off sc0 sc1 nt
	global_load_dwordx4 v[2:5], v[122:123], off sc0 sc1 nt
	s_waitcnt vmcnt(25)
	v_div_scale_f32 v72, s[22:23], v207, v207, 1.0
	v_rcp_f32_e32 v73, v72
	s_lshl_b32 s11, s10, 2
	s_mul_i32 s19, s35, 0x1100
	s_add_i32 s22, s11, 0x26600
	v_fma_f32 v103, -v72, v73, 1.0
	v_fmac_f32_e32 v73, v103, v73
	v_div_scale_f32 v103, vcc, 1.0, v207, 1.0
	v_mul_f32_e32 v104, v103, v73
	v_fma_f32 v105, -v72, v104, v103
	v_fmac_f32_e32 v104, v105, v73
	v_fma_f32 v72, -v72, v104, v103
	v_div_fmas_f32 v72, v72, v73, v104
	v_div_fixup_f32 v72, v72, v207, 1.0
	s_waitcnt vmcnt(24)
	v_fma_f32 v208, v72, v1, -v66
	v_mbcnt_lo_u32_b32 v244, -1, 0
	v_mbcnt_hi_u32_b32 v244, -1, v244
	v_and_b32_e32 v245, 64, v244
	v_xor_b32_e32 v246, 32, v244
	v_add_u32_e32 v245, 64, v245
	v_cmp_lt_i32_e32 vcc, v246, v245
	v_xor_b32_e32 v248, 8, v244
	s_nop 0
	v_cndmask_b32_e32 v246, v244, v246, vcc
	v_lshlrev_b32_e32 v246, 2, v246
	v_mul_f32_e32 v247, v1, v1
	ds_bpermute_b32 v246, v246, v247
	v_xor_b32_e32 v247, 16, v244
	v_cmp_lt_i32_e32 vcc, v247, v245
	s_waitcnt lgkmcnt(0)
	v_fmac_f32_e32 v246, v1, v1
	v_cndmask_b32_e32 v247, v244, v247, vcc
	v_lshlrev_b32_e32 v247, 2, v247
	ds_bpermute_b32 v247, v247, v246
	v_cmp_lt_i32_e32 vcc, v248, v245
	s_waitcnt lgkmcnt(0)
	v_add_f32_e32 v246, v246, v247
	v_cndmask_b32_e32 v248, v244, v248, vcc
	v_lshlrev_b32_e32 v248, 2, v248
	ds_bpermute_b32 v247, v248, v246
	v_xor_b32_e32 v248, 4, v244
	v_cmp_lt_i32_e32 vcc, v248, v245
	s_waitcnt lgkmcnt(0)
	v_add_f32_e32 v246, v246, v247
	v_cndmask_b32_e32 v248, v244, v248, vcc
	v_lshlrev_b32_e32 v248, 2, v248
	ds_bpermute_b32 v247, v248, v246
	v_xor_b32_e32 v248, 2, v244
	v_cmp_lt_i32_e32 vcc, v248, v245
	s_waitcnt lgkmcnt(0)
	v_add_f32_e32 v246, v246, v247
	v_cndmask_b32_e32 v248, v244, v248, vcc
	v_lshlrev_b32_e32 v248, 2, v248
	ds_bpermute_b32 v247, v248, v246
	v_xor_b32_e32 v248, 1, v244
	v_cmp_lt_i32_e32 vcc, v248, v245
	s_nop 1
	v_cndmask_b32_e32 v245, v244, v248, vcc
	s_waitcnt lgkmcnt(0)
	v_add_f32_e32 v244, v246, v247
	v_lshlrev_b32_e32 v245, 2, v245
	ds_bpermute_b32 v245, v245, v244
	s_and_saveexec_b64 s[80:81], s[12:13]
	s_cbranch_execz .LBB0_2
	s_lshl_b32 s82, s35, 2
	s_add_i32 s82, s82, 0x26a00
	s_waitcnt lgkmcnt(0)
	v_add_f32_e32 v244, v244, v245
	v_mov_b32_e32 v245, s82
	ds_write_b32 v245, v244
.LBB0_2:
	s_or_b64 exec, exec, s[80:81]
	v_lshl_add_u32 v1, v206, 2, s22
	s_add_i32 s19, s19, 0x22200
	ds_write_b32 v1, v72
	v_lshl_or_b32 v1, v124, 3, s19
	v_lshl_add_u32 v187, v67, 2, s22
	s_movk_i32 s22, 0x110
	v_mad_u32_u24 v186, v67, s22, v1
	s_add_i32 s22, s7, 0x180
	v_and_b32_e32 v102, 15, v0
	s_lshl_b32 s27, s34, 8
	s_and_b32 s25, s22, 0x380
	s_add_i32 s22, s7, 0x280
	v_lshlrev_b32_e32 v66, 2, v124
	v_mul_u32_u24_e32 v1, 0x110, v102
	v_and_b32_e32 v209, 48, v0
	s_and_b32 s23, s22, 0x380
	s_add_i32 s22, s7, 0x300
	v_mov_b32_e32 v67, 0x200
	s_addk_i32 s27, 0x380
	v_or_b32_e32 v133, s7, v66
	v_add3_u32 v1, s19, v1, v209
	s_lshl_b32 s19, s35, 15
	v_lshlrev_b32_e32 v210, 4, v206
	v_or_b32_e32 v189, s24, v66
	s_xor_b32 s24, s7, 0x200
	s_and_b32 s22, s22, 0x300
	v_bitop3_b32 v197, s7, v66, v67 bitop3:0xde
	s_and_b32 s7, s27, 0x380
	v_lshrrev_b32_e32 v185, 4, v206
	s_ashr_i32 s11, s10, 31
	v_or_b32_e32 v184, s19, v210
	v_or_b32_e32 v188, s26, v66
	v_or_b32_e32 v198, s25, v66
	v_or_b32_e32 v196, s23, v66
	v_or_b32_e32 v195, s22, v66
	v_or_b32_e32 v194, s7, v66
	v_mov_b32_e32 v102, v133
	v_and_b32_e32 v248, 2, v206
	v_cmp_ne_u32_e32 vcc, 0, v248
	v_mov_b32_e32 v249, 0x44444444
	v_mov_b32_e32 v250, 0xeeeeeeee
	s_nop 1
	v_cndmask_b32_e32 v223, v249, v250, vcc
	v_lshrrev_b32_e32 v248, 4, v206
	v_lshl_add_u32 v248, v248, 4, 1
	v_add_u32_e32 v249, 0, v248
	v_cvt_f32_u32_e32 v249, v249
	v_add_u32_e32 v250, 1, v248
	v_cvt_f32_u32_e32 v250, v250
	v_cvt_pk_bf16_f32 v232, v249, v250
	v_add_u32_e32 v249, 2, v248
	v_cvt_f32_u32_e32 v249, v249
	v_add_u32_e32 v250, 3, v248
	v_cvt_f32_u32_e32 v250, v250
	v_cvt_pk_bf16_f32 v233, v249, v250
	v_add_u32_e32 v249, 4, v248
	v_cvt_f32_u32_e32 v249, v249
	v_add_u32_e32 v250, 5, v248
	v_cvt_f32_u32_e32 v250, v250
	v_cvt_pk_bf16_f32 v234, v249, v250
	v_add_u32_e32 v249, 6, v248
	v_cvt_f32_u32_e32 v249, v249
	v_add_u32_e32 v250, 7, v248
	v_cvt_f32_u32_e32 v250, v250
	v_cvt_pk_bf16_f32 v235, v249, v250
	v_add_u32_e32 v249, 8, v248
	v_cvt_f32_u32_e32 v249, v249
	v_add_u32_e32 v250, 9, v248
	v_cvt_f32_u32_e32 v250, v250
	v_cvt_pk_bf16_f32 v236, v249, v250
	v_add_u32_e32 v249, 10, v248
	v_cvt_f32_u32_e32 v249, v249
	v_add_u32_e32 v250, 11, v248
	v_cvt_f32_u32_e32 v250, v250
	v_cvt_pk_bf16_f32 v237, v249, v250
	v_add_u32_e32 v249, 12, v248
	v_cvt_f32_u32_e32 v249, v249
	v_add_u32_e32 v250, 13, v248
	v_cvt_f32_u32_e32 v250, v250
	v_cvt_pk_bf16_f32 v238, v249, v250
	v_add_u32_e32 v249, 14, v248
	v_cvt_f32_u32_e32 v249, v249
	v_add_u32_e32 v250, 15, v248
	v_cvt_f32_u32_e32 v250, v250
	v_cvt_pk_bf16_f32 v239, v249, v250
	v_and_b32_e32 v248, 15, v206
	v_lshrrev_b32_e32 v249, 2, v248
	v_and_b32_e32 v250, 1, v248
	v_lshl_add_u32 v249, v249, 1, v250
	v_and_b32_e32 v250, 3, v249
	v_lshrrev_b32_e32 v251, 4, v206
	v_cmp_eq_u32_e32 vcc, v250, v251
	v_lshrrev_b32_e32 v249, 2, v249
	v_cmp_ne_u32_e64 s[78:79], 0, v249
	v_mov_b32_e32 v250, 0x3f80
	v_mov_b32_e32 v251, 0x3f800000
	s_nop 1
	v_cndmask_b32_e64 v250, v250, v251, s[78:79]
	v_cndmask_b32_e32 v252, 0, v250, vcc
	s_lshr_b32 s77, s19, 15
	s_mulk_i32 s77, 0x1100
	s_add_i32 s77, s77, 0x22200
	v_lshrrev_b32_e32 v248, 4, v206
	v_and_b32_e32 v249, 1, v248
	v_lshrrev_b32_e32 v250, 1, v248
	v_lshlrev_b32_e32 v249, 6, v249
	v_lshl_add_u32 v253, v250, 1, v249
	v_and_b32_e32 v248, 15, v206
	v_cmp_eq_u32_e64 s[78:79], 0, v248
	v_mov_b32_e32 v244, v252
	v_mov_b32_e32 v245, 0
	v_mov_b32_e32 v246, 0
	v_mov_b32_e32 v247, 0
	v_mov_b64_e32 v[240:241], 0
	v_mov_b64_e32 v[242:243], 0
	s_nop 1
	v_smfmac_f32_16x16x64_bf16 v[240:243], v[244:247], v[232:239], v223
	s_nop 15
	s_nop 3
	s_and_saveexec_b64 s[80:81], s[78:79]
	v_cvt_u32_f32_e32 v248, v240
	v_add_u32_e32 v248, -1, v248
	v_lshl_add_u32 v248, v248, 2, s77
	v_add_u32_e32 v249, 0, v253
	ds_write_b32 v248, v249
	v_cvt_u32_f32_e32 v248, v241
	v_add_u32_e32 v248, -1, v248
	v_lshl_add_u32 v248, v248, 2, s77
	v_add_u32_e32 v249, 32, v253
	ds_write_b32 v248, v249
	v_cvt_u32_f32_e32 v248, v242
	v_add_u32_e32 v248, -1, v248
	v_lshl_add_u32 v248, v248, 2, s77
	v_add_u32_e32 v249, 16, v253
	ds_write_b32 v248, v249
	v_cvt_u32_f32_e32 v248, v243
	v_add_u32_e32 v248, -1, v248
	v_lshl_add_u32 v248, v248, 2, s77
	v_add_u32_e32 v249, 48, v253
	ds_write_b32 v248, v249
	s_or_b64 exec, exec, s[80:81]
	v_mov_b32_e32 v244, 0
	v_mov_b32_e32 v245, v252
	v_mov_b32_e32 v246, 0
	v_mov_b32_e32 v247, 0
	v_mov_b64_e32 v[240:241], 0
	v_mov_b64_e32 v[242:243], 0
	s_nop 1
	v_smfmac_f32_16x16x64_bf16 v[240:243], v[244:247], v[232:239], v223
	s_nop 15
	s_nop 3
	s_and_saveexec_b64 s[80:81], s[78:79]
	v_cvt_u32_f32_e32 v248, v240
	v_add_u32_e32 v248, -1, v248
	v_lshl_add_u32 v248, v248, 2, s77
	v_add_u32_e32 v249, 4, v253
	ds_write_b32 v248, v249
	v_cvt_u32_f32_e32 v248, v241
	v_add_u32_e32 v248, -1, v248
	v_lshl_add_u32 v248, v248, 2, s77
	v_add_u32_e32 v249, 36, v253
	ds_write_b32 v248, v249
	v_cvt_u32_f32_e32 v248, v242
	v_add_u32_e32 v248, -1, v248
	v_lshl_add_u32 v248, v248, 2, s77
	v_add_u32_e32 v249, 20, v253
	ds_write_b32 v248, v249
	v_cvt_u32_f32_e32 v248, v243
	v_add_u32_e32 v248, -1, v248
	v_lshl_add_u32 v248, v248, 2, s77
	v_add_u32_e32 v249, 52, v253
	ds_write_b32 v248, v249
	s_or_b64 exec, exec, s[80:81]
	v_mov_b32_e32 v244, 0
	v_mov_b32_e32 v245, 0
	v_mov_b32_e32 v246, v252
	v_mov_b32_e32 v247, 0
	v_mov_b64_e32 v[240:241], 0
	v_mov_b64_e32 v[242:243], 0
	s_nop 1
	v_smfmac_f32_16x16x64_bf16 v[240:243], v[244:247], v[232:239], v223
	s_nop 15
	s_nop 3
	s_and_saveexec_b64 s[80:81], s[78:79]
	v_cvt_u32_f32_e32 v248, v240
	v_add_u32_e32 v248, -1, v248
	v_lshl_add_u32 v248, v248, 2, s77
	v_add_u32_e32 v249, 8, v253
	ds_write_b32 v248, v249
	v_cvt_u32_f32_e32 v248, v241
	v_add_u32_e32 v248, -1, v248
	v_lshl_add_u32 v248, v248, 2, s77
	v_add_u32_e32 v249, 40, v253
	ds_write_b32 v248, v249
	v_cvt_u32_f32_e32 v248, v242
	v_add_u32_e32 v248, -1, v248
	v_lshl_add_u32 v248, v248, 2, s77
	v_add_u32_e32 v249, 24, v253
	ds_write_b32 v248, v249
	v_cvt_u32_f32_e32 v248, v243
	v_add_u32_e32 v248, -1, v248
	v_lshl_add_u32 v248, v248, 2, s77
	v_add_u32_e32 v249, 56, v253
	ds_write_b32 v248, v249
	s_or_b64 exec, exec, s[80:81]
	v_mov_b32_e32 v244, 0
	v_mov_b32_e32 v245, 0
	v_mov_b32_e32 v246, 0
	v_mov_b32_e32 v247, v252
	v_mov_b64_e32 v[240:241], 0
	v_mov_b64_e32 v[242:243], 0
	s_nop 1
	v_smfmac_f32_16x16x64_bf16 v[240:243], v[244:247], v[232:239], v223
	s_nop 15
	s_nop 3
	s_and_saveexec_b64 s[80:81], s[78:79]
	v_cvt_u32_f32_e32 v248, v240
	v_add_u32_e32 v248, -1, v248
	v_lshl_add_u32 v248, v248, 2, s77
	v_add_u32_e32 v249, 12, v253
	ds_write_b32 v248, v249
	v_cvt_u32_f32_e32 v248, v241
	v_add_u32_e32 v248, -1, v248
	v_lshl_add_u32 v248, v248, 2, s77
	v_add_u32_e32 v249, 44, v253
	ds_write_b32 v248, v249
	v_cvt_u32_f32_e32 v248, v242
	v_add_u32_e32 v248, -1, v248
	v_lshl_add_u32 v248, v248, 2, s77
	v_add_u32_e32 v249, 28, v253
	ds_write_b32 v248, v249
	v_cvt_u32_f32_e32 v248, v243
	v_add_u32_e32 v248, -1, v248
	v_lshl_add_u32 v248, v248, 2, s77
	v_add_u32_e32 v249, 60, v253
	ds_write_b32 v248, v249
	s_or_b64 exec, exec, s[80:81]
	v_bfe_u32 v248, v206, 3, 2
	v_lshrrev_b32_e32 v249, 5, v206
	v_lshlrev_b32_e32 v248, 4, v248
	v_lshl_or_b32 v248, v249, 3, v248
	v_and_b32_e32 v249, 7, v206
	v_or_b32_e32 v248, v248, v249
	v_lshl_add_u32 v248, v248, 2, s77
	s_waitcnt lgkmcnt(0)
	ds_read_b32 v254, v248
	v_and_b32_e32 v248, 15, v206
	v_bfe_u32 v249, v248, 1, 2
	v_lshrrev_b32_e32 v250, 3, v248
	v_lshlrev_b32_e32 v249, 4, v249
	v_lshl_or_b32 v249, v250, 3, v249
	v_and_b32_e32 v250, 1, v248
	v_lshl_or_b32 v249, v250, 2, v249
	v_lshl_add_u32 v249, v249, 2, s77
	ds_read_b128 v[248:251], v249
	s_lshr_b32 s76, s19, 6
	s_add_i32 s76, s76, 0x20000
	v_lshrrev_b32_e32 v252, 4, v206
	v_lshl_add_u32 v252, v252, 7, s76
	s_waitcnt lgkmcnt(0)
	v_add_u32_e32 v248, v252, v248
	v_add_u32_e32 v249, v252, v249
	v_add_u32_e32 v250, v252, v250
	v_add_u32_e32 v251, v252, v251
	v_cvt_pk_bf16_f32 v236, v224, v225
	v_cvt_pk_bf16_f32 v237, v226, v227
	v_lshlrev_b32_e32 v238, 16, v236
	v_and_b32_e32 v239, 0xffff0000, v236
	v_lshlrev_b32_e32 v240, 16, v237
	v_and_b32_e32 v241, 0xffff0000, v237
	v_sub_f32_e32 v238, v224, v238
	v_sub_f32_e32 v239, v225, v239
	v_sub_f32_e32 v240, v226, v240
	v_sub_f32_e32 v241, v227, v241
	v_cvt_pk_bf16_f32 v238, v238, v239
	v_cvt_pk_bf16_f32 v239, v240, v241
	ds_write_b16 v248, v236
	ds_write_b16_d16_hi v249, v236
	ds_write_b16 v250, v237
	ds_write_b16_d16_hi v251, v237
	ds_write_b16 v248, v238 offset:2176
	ds_write_b16_d16_hi v249, v238 offset:2176
	ds_write_b16 v250, v239 offset:2176
	ds_write_b16_d16_hi v251, v239 offset:2176
	s_waitcnt vmcnt(23)
	s_waitcnt vmcnt(22)
	s_waitcnt vmcnt(21)
	s_waitcnt vmcnt(20)
	s_waitcnt vmcnt(19)
	s_waitcnt vmcnt(18)
	s_waitcnt vmcnt(17)
	s_waitcnt vmcnt(16)
	ds_read_b32 v66, v187 offset:192
	v_or_b32_e32 v103, 48, v132
	v_add_u32_e32 v104, 1, v102
	v_cmp_eq_u32_e32 vcc, v102, v103
	v_add_u32_e32 v105, 3, v102
	v_add_u32_e32 v106, 2, v102
	v_cndmask_b32_e64 v72, 0, 1.0, vcc
	v_cmp_eq_u32_e32 vcc, v104, v103
	v_or_b32_e32 v107, 50, v132
	v_or_b32_e32 v108, 52, v132
	v_cndmask_b32_e64 v73, 0, 1.0, vcc
	v_cmp_eq_u32_e32 vcc, v105, v103
	s_waitcnt lgkmcnt(0)
	v_pk_fma_f32 v[68:69], v[66:67], v[68:69], v[72:73] op_sel_hi:[0,1,1] neg_lo:[1,0,0] neg_hi:[1,0,0]
	v_cvt_pk_bf16_f32 v68, v68, v69
	v_cndmask_b32_e64 v73, 0, 1.0, vcc
	v_cmp_eq_u32_e32 vcc, v106, v103
	v_or_b32_e32 v109, 54, v132
	v_or_b32_e32 v110, 56, v132
	v_cndmask_b32_e64 v72, 0, 1.0, vcc
	v_pk_fma_f32 v[66:67], v[66:67], v[70:71], v[72:73] op_sel_hi:[0,1,1] neg_lo:[1,0,0] neg_hi:[1,0,0]
	v_cvt_pk_bf16_f32 v69, v66, v67
	ds_write_b64 v186, v[68:69]
	ds_read_b32 v66, v187 offset:200
	v_cmp_eq_u32_e32 vcc, v102, v107
	v_or_b32_e32 v111, 58, v132
	v_or_b32_e32 v112, 60, v132
	v_cndmask_b32_e64 v68, 0, 1.0, vcc
	v_cmp_eq_u32_e32 vcc, v104, v107
	v_or_b32_e32 v113, 62, v132
	v_or_b32_e32 v193, 2, v132
	v_cndmask_b32_e64 v69, 0, 1.0, vcc
	v_cmp_eq_u32_e32 vcc, v105, v107
	s_waitcnt lgkmcnt(0)
	v_pk_fma_f32 v[68:69], v[66:67], v[78:79], v[68:69] op_sel_hi:[0,1,1] neg_lo:[1,0,0] neg_hi:[1,0,0]
	v_cvt_pk_bf16_f32 v68, v68, v69
	v_cndmask_b32_e64 v71, 0, 1.0, vcc
	v_cmp_eq_u32_e32 vcc, v106, v107
	v_or_b32_e32 v192, 4, v132
	v_or_b32_e32 v190, 6, v132
	v_cndmask_b32_e64 v70, 0, 1.0, vcc
	v_pk_fma_f32 v[66:67], v[66:67], v[80:81], v[70:71] op_sel_hi:[0,1,1] neg_lo:[1,0,0] neg_hi:[1,0,0]
	v_cvt_pk_bf16_f32 v69, v66, v67
	ds_write_b64 v186, v[68:69] offset:544
	ds_read_b32 v66, v187 offset:208
	v_cmp_eq_u32_e32 vcc, v102, v108
	v_or_b32_e32 v149, 8, v132
	v_or_b32_e32 v148, 10, v132
	v_cndmask_b32_e64 v68, 0, 1.0, vcc
	v_cmp_eq_u32_e32 vcc, v104, v108
	v_or_b32_e32 v147, 12, v132
	v_or_b32_e32 v146, 14, v132
	v_cndmask_b32_e64 v69, 0, 1.0, vcc
	v_cmp_eq_u32_e32 vcc, v105, v108
	s_waitcnt lgkmcnt(0)
	v_pk_fma_f32 v[68:69], v[66:67], v[82:83], v[68:69] op_sel_hi:[0,1,1] neg_lo:[1,0,0] neg_hi:[1,0,0]
	v_cvt_pk_bf16_f32 v68, v68, v69
	v_cndmask_b32_e64 v71, 0, 1.0, vcc
	v_cmp_eq_u32_e32 vcc, v106, v108
	s_nop 1
	v_cndmask_b32_e64 v70, 0, 1.0, vcc
	v_pk_fma_f32 v[66:67], v[66:67], v[84:85], v[70:71] op_sel_hi:[0,1,1] neg_lo:[1,0,0] neg_hi:[1,0,0]
	v_cvt_pk_bf16_f32 v69, v66, v67
	ds_write_b64 v186, v[68:69] offset:1088
	ds_read_b32 v66, v187 offset:216
	v_cmp_eq_u32_e32 vcc, v102, v109
	s_nop 1
	v_cndmask_b32_e64 v68, 0, 1.0, vcc
	v_cmp_eq_u32_e32 vcc, v104, v109
	s_nop 1
	v_cndmask_b32_e64 v69, 0, 1.0, vcc
	v_cmp_eq_u32_e32 vcc, v105, v109
	s_waitcnt lgkmcnt(0)
	v_pk_fma_f32 v[68:69], v[66:67], v[90:91], v[68:69] op_sel_hi:[0,1,1] neg_lo:[1,0,0] neg_hi:[1,0,0]
	v_cvt_pk_bf16_f32 v68, v68, v69
	v_cndmask_b32_e64 v71, 0, 1.0, vcc
	v_cmp_eq_u32_e32 vcc, v106, v109
	s_nop 1
	v_cndmask_b32_e64 v70, 0, 1.0, vcc
	v_pk_fma_f32 v[66:67], v[66:67], v[92:93], v[70:71] op_sel_hi:[0,1,1] neg_lo:[1,0,0] neg_hi:[1,0,0]
	v_cvt_pk_bf16_f32 v69, v66, v67
	ds_write_b64 v186, v[68:69] offset:1632
	ds_read_b32 v66, v187 offset:224
	v_cmp_eq_u32_e32 vcc, v102, v110
	s_nop 1
	v_cndmask_b32_e64 v68, 0, 1.0, vcc
	v_cmp_eq_u32_e32 vcc, v104, v110
	s_nop 1
	v_cndmask_b32_e64 v69, 0, 1.0, vcc
	v_cmp_eq_u32_e32 vcc, v105, v110
	s_waitcnt lgkmcnt(0)
	v_pk_fma_f32 v[68:69], v[66:67], v[98:99], v[68:69] op_sel_hi:[0,1,1] neg_lo:[1,0,0] neg_hi:[1,0,0]
	v_cvt_pk_bf16_f32 v68, v68, v69
	v_cndmask_b32_e64 v71, 0, 1.0, vcc
	v_cmp_eq_u32_e32 vcc, v106, v110
	s_nop 1
	v_cndmask_b32_e64 v70, 0, 1.0, vcc
	v_pk_fma_f32 v[66:67], v[66:67], v[100:101], v[70:71] op_sel_hi:[0,1,1] neg_lo:[1,0,0] neg_hi:[1,0,0]
	v_cvt_pk_bf16_f32 v69, v66, v67
	ds_write_b64 v186, v[68:69] offset:2176
	ds_read_b32 v66, v187 offset:232
	v_cmp_eq_u32_e32 vcc, v102, v111
	s_nop 1
	v_cndmask_b32_e64 v68, 0, 1.0, vcc
	v_cmp_eq_u32_e32 vcc, v104, v111
	s_nop 1
	v_cndmask_b32_e64 v69, 0, 1.0, vcc
	v_cmp_eq_u32_e32 vcc, v105, v111
	s_waitcnt lgkmcnt(0)
	v_pk_fma_f32 v[62:63], v[66:67], v[62:63], v[68:69] op_sel_hi:[0,1,1] neg_lo:[1,0,0] neg_hi:[1,0,0]
	v_cvt_pk_bf16_f32 v62, v62, v63
	v_cndmask_b32_e64 v69, 0, 1.0, vcc
	v_cmp_eq_u32_e32 vcc, v106, v111
	s_nop 1
	v_cndmask_b32_e64 v68, 0, 1.0, vcc
	v_pk_fma_f32 v[64:65], v[66:67], v[64:65], v[68:69] op_sel_hi:[0,1,1] neg_lo:[1,0,0] neg_hi:[1,0,0]
	v_cvt_pk_bf16_f32 v63, v64, v65
	ds_write_b64 v186, v[62:63] offset:2720
	ds_read_b32 v62, v187 offset:240
	v_cmp_eq_u32_e32 vcc, v102, v112
	s_nop 1
	v_cndmask_b32_e64 v64, 0, 1.0, vcc
	v_cmp_eq_u32_e32 vcc, v104, v112
	s_nop 1
	v_cndmask_b32_e64 v65, 0, 1.0, vcc
	v_cmp_eq_u32_e32 vcc, v105, v112
	s_waitcnt lgkmcnt(0)
	v_pk_fma_f32 v[54:55], v[62:63], v[54:55], v[64:65] op_sel_hi:[0,1,1] neg_lo:[1,0,0] neg_hi:[1,0,0]
	v_cvt_pk_bf16_f32 v54, v54, v55
	v_cndmask_b32_e64 v65, 0, 1.0, vcc
	v_cmp_eq_u32_e32 vcc, v106, v112
	s_nop 1
	v_cndmask_b32_e64 v64, 0, 1.0, vcc
	v_pk_fma_f32 v[56:57], v[62:63], v[56:57], v[64:65] op_sel_hi:[0,1,1] neg_lo:[1,0,0] neg_hi:[1,0,0]
	v_cvt_pk_bf16_f32 v55, v56, v57
	ds_write_b64 v186, v[54:55] offset:3264
	ds_read_b32 v54, v187 offset:248
	v_cmp_eq_u32_e32 vcc, v102, v113
	s_nop 1
	v_cndmask_b32_e64 v56, 0, 1.0, vcc
	v_cmp_eq_u32_e32 vcc, v104, v113
	s_nop 1
	v_cndmask_b32_e64 v57, 0, 1.0, vcc
	v_cmp_eq_u32_e32 vcc, v105, v113
	s_waitcnt lgkmcnt(0)
	v_pk_fma_f32 v[46:47], v[54:55], v[46:47], v[56:57] op_sel_hi:[0,1,1] neg_lo:[1,0,0] neg_hi:[1,0,0]
	v_cvt_pk_bf16_f32 v46, v46, v47
	v_cndmask_b32_e64 v57, 0, 1.0, vcc
	v_cmp_eq_u32_e32 vcc, v106, v113
	s_nop 1
	v_cndmask_b32_e64 v56, 0, 1.0, vcc
	v_pk_fma_f32 v[48:49], v[54:55], v[48:49], v[56:57] op_sel_hi:[0,1,1] neg_lo:[1,0,0] neg_hi:[1,0,0]
	v_cvt_pk_bf16_f32 v47, v48, v49
	ds_write_b64 v186, v[46:47] offset:3808
	ds_read_b128 v[46:49], v1
	s_waitcnt lgkmcnt(0)
	ds_write_b128 v184, v[46:49]
	ds_read_b128 v[46:49], v1 offset:64
	s_waitcnt lgkmcnt(0)
	ds_write_b128 v184, v[46:49] offset:1024
	ds_read_b128 v[46:49], v1 offset:128
	s_waitcnt lgkmcnt(0)
	ds_write_b128 v184, v[46:49] offset:2048
	ds_read_b128 v[46:49], v1 offset:192
	s_waitcnt lgkmcnt(0)
	ds_write_b128 v184, v[46:49] offset:3072
	s_lshl_b32 s30, s25, 2
	s_mov_b32 s31, s21
	v_lshl_add_u64 v[46:47], v[126:127], 0, s[30:31]
	v_lshl_add_u64 v[48:49], v[128:129], 0, s[30:31]
	v_lshl_add_u64 v[54:55], v[134:135], 0, s[30:31]
	v_lshl_add_u64 v[56:57], v[136:137], 0, s[30:31]
	v_lshl_add_u64 v[62:63], v[138:139], 0, s[30:31]
	v_lshl_add_u64 v[64:65], v[140:141], 0, s[30:31]
	v_lshl_add_u64 v[98:99], v[142:143], 0, s[30:31]
	v_lshl_add_u64 v[100:101], v[144:145], 0, s[30:31]
	global_load_dwordx4 v[90:93], v[46:47], off sc0 sc1 nt
	global_load_dwordx4 v[82:85], v[48:49], off sc0 sc1 nt
	global_load_dwordx4 v[78:81], v[54:55], off sc0 sc1 nt
	global_load_dwordx4 v[70:73], v[56:57], off sc0 sc1 nt
	global_load_dwordx4 v[66:69], v[62:63], off sc0 sc1 nt
	s_nop 0
	global_load_dwordx4 v[62:65], v[64:65], off sc0 sc1 nt
	s_nop 0
	global_load_dwordx4 v[54:57], v[98:99], off sc0 sc1 nt
	global_load_dwordx4 v[46:49], v[100:101], off sc0 sc1 nt
	v_mov_b32_e32 v99, v189
	s_waitcnt vmcnt(23)
	s_waitcnt vmcnt(22)
	s_waitcnt vmcnt(21)
	s_waitcnt vmcnt(20)
	s_waitcnt vmcnt(19)
	s_waitcnt vmcnt(18)
	s_waitcnt vmcnt(17)
	s_waitcnt vmcnt(16)
	ds_read_b32 v98, v187 offset:192
	v_add_u32_e32 v102, 1, v99
	v_cmp_eq_u32_e32 vcc, v99, v103
	v_add_u32_e32 v104, 3, v99
	v_add_u32_e32 v105, 2, v99
	v_cndmask_b32_e64 v100, 0, 1.0, vcc
	v_cmp_eq_u32_e32 vcc, v102, v103
	s_nop 1
	v_cndmask_b32_e64 v101, 0, 1.0, vcc
	v_cmp_eq_u32_e32 vcc, v104, v103
	s_waitcnt lgkmcnt(0)
	v_pk_fma_f32 v[94:95], v[98:99], v[94:95], v[100:101] op_sel_hi:[0,1,1] neg_lo:[1,0,0] neg_hi:[1,0,0]
	v_cvt_pk_bf16_f32 v94, v94, v95
	v_cndmask_b32_e64 v101, 0, 1.0, vcc
	v_cmp_eq_u32_e32 vcc, v105, v103
	s_nop 1
	v_cndmask_b32_e64 v100, 0, 1.0, vcc
	v_pk_fma_f32 v[96:97], v[98:99], v[96:97], v[100:101] op_sel_hi:[0,1,1] neg_lo:[1,0,0] neg_hi:[1,0,0]
	v_cvt_pk_bf16_f32 v95, v96, v97
	ds_write_b64 v186, v[94:95]
	ds_read_b32 v94, v187 offset:200
	v_cmp_eq_u32_e32 vcc, v99, v107
	s_nop 1
	v_cndmask_b32_e64 v96, 0, 1.0, vcc
	v_cmp_eq_u32_e32 vcc, v102, v107
	s_nop 1
	v_cndmask_b32_e64 v97, 0, 1.0, vcc
	v_cmp_eq_u32_e32 vcc, v104, v107
	s_waitcnt lgkmcnt(0)
	v_pk_fma_f32 v[86:87], v[94:95], v[86:87], v[96:97] op_sel_hi:[0,1,1] neg_lo:[1,0,0] neg_hi:[1,0,0]
	v_cvt_pk_bf16_f32 v86, v86, v87
	v_cndmask_b32_e64 v97, 0, 1.0, vcc
	v_cmp_eq_u32_e32 vcc, v105, v107
	s_nop 1
	v_cndmask_b32_e64 v96, 0, 1.0, vcc
	v_pk_fma_f32 v[88:89], v[94:95], v[88:89], v[96:97] op_sel_hi:[0,1,1] neg_lo:[1,0,0] neg_hi:[1,0,0]
	v_cvt_pk_bf16_f32 v87, v88, v89
	ds_write_b64 v186, v[86:87] offset:544
	ds_read_b32 v86, v187 offset:208
	v_cmp_eq_u32_e32 vcc, v99, v108
	s_nop 1
	v_cndmask_b32_e64 v88, 0, 1.0, vcc
	v_cmp_eq_u32_e32 vcc, v102, v108
	s_nop 1
	v_cndmask_b32_e64 v89, 0, 1.0, vcc
	v_cmp_eq_u32_e32 vcc, v104, v108
	s_waitcnt lgkmcnt(0)
	v_pk_fma_f32 v[74:75], v[86:87], v[74:75], v[88:89] op_sel_hi:[0,1,1] neg_lo:[1,0,0] neg_hi:[1,0,0]
	v_cvt_pk_bf16_f32 v74, v74, v75
	v_cndmask_b32_e64 v89, 0, 1.0, vcc
	v_cmp_eq_u32_e32 vcc, v105, v108
	s_nop 1
	v_cndmask_b32_e64 v88, 0, 1.0, vcc
	v_pk_fma_f32 v[76:77], v[86:87], v[76:77], v[88:89] op_sel_hi:[0,1,1] neg_lo:[1,0,0] neg_hi:[1,0,0]
	v_cvt_pk_bf16_f32 v75, v76, v77
	ds_write_b64 v186, v[74:75] offset:1088
	ds_read_b32 v74, v187 offset:216
	v_cmp_eq_u32_e32 vcc, v99, v109
	s_nop 1
	v_cndmask_b32_e64 v76, 0, 1.0, vcc
	v_cmp_eq_u32_e32 vcc, v102, v109
	s_nop 1
	v_cndmask_b32_e64 v77, 0, 1.0, vcc
	v_cmp_eq_u32_e32 vcc, v104, v109
	s_waitcnt lgkmcnt(0)
	v_pk_fma_f32 v[58:59], v[74:75], v[58:59], v[76:77] op_sel_hi:[0,1,1] neg_lo:[1,0,0] neg_hi:[1,0,0]
	v_cvt_pk_bf16_f32 v58, v58, v59
	v_cndmask_b32_e64 v77, 0, 1.0, vcc
	v_cmp_eq_u32_e32 vcc, v105, v109
	s_nop 1
	v_cndmask_b32_e64 v76, 0, 1.0, vcc
	v_pk_fma_f32 v[60:61], v[74:75], v[60:61], v[76:77] op_sel_hi:[0,1,1] neg_lo:[1,0,0] neg_hi:[1,0,0]
	v_cvt_pk_bf16_f32 v59, v60, v61
	ds_write_b64 v186, v[58:59] offset:1632
	ds_read_b32 v58, v187 offset:224
	v_cmp_eq_u32_e32 vcc, v99, v110
	s_nop 1
	v_cndmask_b32_e64 v60, 0, 1.0, vcc
	v_cmp_eq_u32_e32 vcc, v102, v110
	s_nop 1
	v_cndmask_b32_e64 v61, 0, 1.0, vcc
	v_cmp_eq_u32_e32 vcc, v104, v110
	s_waitcnt lgkmcnt(0)
	v_pk_fma_f32 v[50:51], v[58:59], v[50:51], v[60:61] op_sel_hi:[0,1,1] neg_lo:[1,0,0] neg_hi:[1,0,0]
	v_cvt_pk_bf16_f32 v50, v50, v51
	v_cndmask_b32_e64 v61, 0, 1.0, vcc
	v_cmp_eq_u32_e32 vcc, v105, v110
	s_nop 1
	v_cndmask_b32_e64 v60, 0, 1.0, vcc
	v_pk_fma_f32 v[52:53], v[58:59], v[52:53], v[60:61] op_sel_hi:[0,1,1] neg_lo:[1,0,0] neg_hi:[1,0,0]
	v_cvt_pk_bf16_f32 v51, v52, v53
	ds_write_b64 v186, v[50:51] offset:2176
	ds_read_b32 v50, v187 offset:232
	v_cmp_eq_u32_e32 vcc, v99, v111
	s_nop 1
	v_cndmask_b32_e64 v52, 0, 1.0, vcc
	v_cmp_eq_u32_e32 vcc, v102, v111
	s_nop 1
	v_cndmask_b32_e64 v53, 0, 1.0, vcc
	v_cmp_eq_u32_e32 vcc, v104, v111
	s_waitcnt lgkmcnt(0)
	v_pk_fma_f32 v[42:43], v[50:51], v[42:43], v[52:53] op_sel_hi:[0,1,1] neg_lo:[1,0,0] neg_hi:[1,0,0]
	v_cvt_pk_bf16_f32 v42, v42, v43
	v_cndmask_b32_e64 v53, 0, 1.0, vcc
	v_cmp_eq_u32_e32 vcc, v105, v111
	s_nop 1
	v_cndmask_b32_e64 v52, 0, 1.0, vcc
	v_pk_fma_f32 v[44:45], v[50:51], v[44:45], v[52:53] op_sel_hi:[0,1,1] neg_lo:[1,0,0] neg_hi:[1,0,0]
	v_cvt_pk_bf16_f32 v43, v44, v45
	ds_write_b64 v186, v[42:43] offset:2720
	ds_read_b32 v42, v187 offset:240
	v_cmp_eq_u32_e32 vcc, v99, v112
	s_nop 1
	v_cndmask_b32_e64 v44, 0, 1.0, vcc
	v_cmp_eq_u32_e32 vcc, v102, v112
	s_nop 1
	v_cndmask_b32_e64 v45, 0, 1.0, vcc
	v_cmp_eq_u32_e32 vcc, v104, v112
	s_waitcnt lgkmcnt(0)
	v_pk_fma_f32 v[38:39], v[42:43], v[38:39], v[44:45] op_sel_hi:[0,1,1] neg_lo:[1,0,0] neg_hi:[1,0,0]
	v_cvt_pk_bf16_f32 v38, v38, v39
	v_cndmask_b32_e64 v45, 0, 1.0, vcc
	v_cmp_eq_u32_e32 vcc, v105, v112
	s_nop 1
	v_cndmask_b32_e64 v44, 0, 1.0, vcc
	v_pk_fma_f32 v[40:41], v[42:43], v[40:41], v[44:45] op_sel_hi:[0,1,1] neg_lo:[1,0,0] neg_hi:[1,0,0]
	v_cvt_pk_bf16_f32 v39, v40, v41
	ds_write_b64 v186, v[38:39] offset:3264
	ds_read_b32 v38, v187 offset:248
	v_cmp_eq_u32_e32 vcc, v99, v113
	s_nop 1
	v_cndmask_b32_e64 v40, 0, 1.0, vcc
	v_cmp_eq_u32_e32 vcc, v102, v113
	s_nop 1
	v_cndmask_b32_e64 v41, 0, 1.0, vcc
	v_cmp_eq_u32_e32 vcc, v104, v113
	s_waitcnt lgkmcnt(0)
	v_pk_fma_f32 v[34:35], v[38:39], v[34:35], v[40:41] op_sel_hi:[0,1,1] neg_lo:[1,0,0] neg_hi:[1,0,0]
	v_cvt_pk_bf16_f32 v34, v34, v35
	v_cndmask_b32_e64 v41, 0, 1.0, vcc
	v_cmp_eq_u32_e32 vcc, v105, v113
	s_nop 1
	v_cndmask_b32_e64 v40, 0, 1.0, vcc
	v_pk_fma_f32 v[36:37], v[38:39], v[36:37], v[40:41] op_sel_hi:[0,1,1] neg_lo:[1,0,0] neg_hi:[1,0,0]
	v_cvt_pk_bf16_f32 v35, v36, v37
	ds_write_b64 v186, v[34:35] offset:3808
	ds_read_b128 v[34:37], v1
	s_waitcnt lgkmcnt(0)
	ds_write_b128 v184, v[34:37] offset:4096
	ds_read_b128 v[34:37], v1 offset:64
	s_waitcnt lgkmcnt(0)
	ds_write_b128 v184, v[34:37] offset:5120
	ds_read_b128 v[34:37], v1 offset:128
	s_waitcnt lgkmcnt(0)
	ds_write_b128 v184, v[34:37] offset:6144
	ds_read_b128 v[34:37], v1 offset:192
	s_waitcnt lgkmcnt(0)
	ds_write_b128 v184, v[34:37] offset:7168
	s_lshl_b32 s28, s24, 2
	s_mov_b32 s29, s21
	v_lshl_add_u64 v[34:35], v[126:127], 0, s[28:29]
	v_lshl_add_u64 v[36:37], v[128:129], 0, s[28:29]
	v_lshl_add_u64 v[38:39], v[134:135], 0, s[28:29]
	v_lshl_add_u64 v[40:41], v[136:137], 0, s[28:29]
	v_lshl_add_u64 v[42:43], v[138:139], 0, s[28:29]
	v_lshl_add_u64 v[44:45], v[140:141], 0, s[28:29]
	v_lshl_add_u64 v[50:51], v[142:143], 0, s[28:29]
	v_lshl_add_u64 v[52:53], v[144:145], 0, s[28:29]
	global_load_dwordx4 v[122:125], v[34:35], off sc0 sc1 nt
	global_load_dwordx4 v[114:117], v[36:37], off sc0 sc1 nt
	global_load_dwordx4 v[106:109], v[38:39], off sc0 sc1 nt
	global_load_dwordx4 v[86:89], v[40:41], off sc0 sc1 nt
	global_load_dwordx4 v[74:77], v[42:43], off sc0 sc1 nt
	s_nop 0
	global_load_dwordx4 v[42:45], v[44:45], off sc0 sc1 nt
	s_nop 0
	global_load_dwordx4 v[38:41], v[50:51], off sc0 sc1 nt
	global_load_dwordx4 v[34:37], v[52:53], off sc0 sc1 nt
	v_mov_b32_e32 v50, v188
	s_waitcnt vmcnt(23)
	s_waitcnt vmcnt(22)
	s_waitcnt vmcnt(21)
	s_waitcnt vmcnt(20)
	s_waitcnt vmcnt(19)
	s_waitcnt vmcnt(18)
	s_waitcnt vmcnt(17)
	s_waitcnt vmcnt(16)
	ds_read_b32 v50, v187 offset:192
	s_waitcnt lgkmcnt(0)
	v_pk_fma_f32 v[30:31], v[50:51], v[30:31], 0 op_sel_hi:[0,1,0] neg_lo:[1,0,0] neg_hi:[1,0,0]
	v_pk_fma_f32 v[32:33], v[50:51], v[32:33], 0 op_sel_hi:[0,1,0] neg_lo:[1,0,0] neg_hi:[1,0,0]
	v_cvt_pk_bf16_f32 v30, v30, v31
	v_cvt_pk_bf16_f32 v31, v32, v33
	ds_write_b64 v186, v[30:31]
	ds_read_b32 v30, v187 offset:200
	s_waitcnt lgkmcnt(0)
	v_pk_fma_f32 v[26:27], v[30:31], v[26:27], 0 op_sel_hi:[0,1,0] neg_lo:[1,0,0] neg_hi:[1,0,0]
	v_pk_fma_f32 v[28:29], v[30:31], v[28:29], 0 op_sel_hi:[0,1,0] neg_lo:[1,0,0] neg_hi:[1,0,0]
	v_cvt_pk_bf16_f32 v26, v26, v27
	v_cvt_pk_bf16_f32 v27, v28, v29
	ds_write_b64 v186, v[26:27] offset:544
	ds_read_b32 v26, v187 offset:208
	s_waitcnt lgkmcnt(0)
	v_pk_fma_f32 v[22:23], v[26:27], v[22:23], 0 op_sel_hi:[0,1,0] neg_lo:[1,0,0] neg_hi:[1,0,0]
	v_pk_fma_f32 v[24:25], v[26:27], v[24:25], 0 op_sel_hi:[0,1,0] neg_lo:[1,0,0] neg_hi:[1,0,0]
	v_cvt_pk_bf16_f32 v22, v22, v23
	v_cvt_pk_bf16_f32 v23, v24, v25
	ds_write_b64 v186, v[22:23] offset:1088
	ds_read_b32 v22, v187 offset:216
	s_waitcnt lgkmcnt(0)
	v_pk_fma_f32 v[18:19], v[22:23], v[18:19], 0 op_sel_hi:[0,1,0] neg_lo:[1,0,0] neg_hi:[1,0,0]
	v_pk_fma_f32 v[20:21], v[22:23], v[20:21], 0 op_sel_hi:[0,1,0] neg_lo:[1,0,0] neg_hi:[1,0,0]
	v_cvt_pk_bf16_f32 v18, v18, v19
	v_cvt_pk_bf16_f32 v19, v20, v21
	ds_write_b64 v186, v[18:19] offset:1632
	ds_read_b32 v18, v187 offset:224
	s_waitcnt lgkmcnt(0)
	v_pk_fma_f32 v[14:15], v[18:19], v[14:15], 0 op_sel_hi:[0,1,0] neg_lo:[1,0,0] neg_hi:[1,0,0]
	v_pk_fma_f32 v[16:17], v[18:19], v[16:17], 0 op_sel_hi:[0,1,0] neg_lo:[1,0,0] neg_hi:[1,0,0]
	v_cvt_pk_bf16_f32 v14, v14, v15
	v_cvt_pk_bf16_f32 v15, v16, v17
	ds_write_b64 v186, v[14:15] offset:2176
	ds_read_b32 v14, v187 offset:232
	s_waitcnt lgkmcnt(0)
	v_pk_fma_f32 v[10:11], v[14:15], v[10:11], 0 op_sel_hi:[0,1,0] neg_lo:[1,0,0] neg_hi:[1,0,0]
	v_pk_fma_f32 v[12:13], v[14:15], v[12:13], 0 op_sel_hi:[0,1,0] neg_lo:[1,0,0] neg_hi:[1,0,0]
	v_cvt_pk_bf16_f32 v10, v10, v11
	v_cvt_pk_bf16_f32 v11, v12, v13
	ds_write_b64 v186, v[10:11] offset:2720
	ds_read_b32 v10, v187 offset:240
	s_waitcnt lgkmcnt(0)
	v_pk_fma_f32 v[6:7], v[10:11], v[6:7], 0 op_sel_hi:[0,1,0] neg_lo:[1,0,0] neg_hi:[1,0,0]
	v_pk_fma_f32 v[8:9], v[10:11], v[8:9], 0 op_sel_hi:[0,1,0] neg_lo:[1,0,0] neg_hi:[1,0,0]
	v_cvt_pk_bf16_f32 v6, v6, v7
	v_cvt_pk_bf16_f32 v7, v8, v9
	ds_write_b64 v186, v[6:7] offset:3264
	ds_read_b32 v6, v187 offset:248
	s_waitcnt lgkmcnt(0)
	v_pk_fma_f32 v[2:3], v[6:7], v[2:3], 0 op_sel_hi:[0,1,0] neg_lo:[1,0,0] neg_hi:[1,0,0]
	v_pk_fma_f32 v[4:5], v[6:7], v[4:5], 0 op_sel_hi:[0,1,0] neg_lo:[1,0,0] neg_hi:[1,0,0]
	v_cvt_pk_bf16_f32 v2, v2, v3
	v_cvt_pk_bf16_f32 v3, v4, v5
	ds_write_b64 v186, v[2:3] offset:3808
	ds_read_b128 v[2:5], v1
	s_waitcnt lgkmcnt(0)
	ds_write_b128 v184, v[2:5] offset:8192
	ds_read_b128 v[2:5], v1 offset:64
	s_waitcnt lgkmcnt(0)
	ds_write_b128 v184, v[2:5] offset:9216
	ds_read_b128 v[2:5], v1 offset:128
	s_waitcnt lgkmcnt(0)
	ds_write_b128 v184, v[2:5] offset:10240
	ds_read_b128 v[2:5], v1 offset:192
	s_waitcnt lgkmcnt(0)
	ds_write_b128 v184, v[2:5] offset:11264
	s_lshl_b32 s26, s23, 2
	s_mov_b32 s27, s21
	v_lshl_add_u64 v[2:3], v[126:127], 0, s[26:27]
	v_lshl_add_u64 v[4:5], v[128:129], 0, s[26:27]
	v_lshl_add_u64 v[6:7], v[134:135], 0, s[26:27]
	v_lshl_add_u64 v[8:9], v[136:137], 0, s[26:27]
	v_lshl_add_u64 v[10:11], v[138:139], 0, s[26:27]
	v_lshl_add_u64 v[12:13], v[140:141], 0, s[26:27]
	v_lshl_add_u64 v[14:15], v[142:143], 0, s[26:27]
	v_lshl_add_u64 v[16:17], v[144:145], 0, s[26:27]
	global_load_dwordx4 v[118:121], v[2:3], off sc0 sc1 nt
	global_load_dwordx4 v[110:113], v[4:5], off sc0 sc1 nt
	global_load_dwordx4 v[102:105], v[6:7], off sc0 sc1 nt
	global_load_dwordx4 v[98:101], v[8:9], off sc0 sc1 nt
	global_load_dwordx4 v[58:61], v[10:11], off sc0 sc1 nt
	global_load_dwordx4 v[50:53], v[12:13], off sc0 sc1 nt
	global_load_dwordx4 v[30:33], v[14:15], off sc0 sc1 nt
	global_load_dwordx4 v[22:25], v[16:17], off sc0 sc1 nt
	v_mov_b32_e32 v2, v198
	s_waitcnt vmcnt(23)
	s_waitcnt vmcnt(22)
	s_waitcnt vmcnt(21)
	s_waitcnt vmcnt(20)
	s_waitcnt vmcnt(19)
	s_waitcnt vmcnt(18)
	s_waitcnt vmcnt(17)
	s_waitcnt vmcnt(16)
	ds_read_b32 v2, v187 offset:192
	s_waitcnt lgkmcnt(0)
	v_pk_fma_f32 v[4:5], v[2:3], v[90:91], 0 op_sel_hi:[0,1,0] neg_lo:[1,0,0] neg_hi:[1,0,0]
	v_pk_fma_f32 v[2:3], v[2:3], v[92:93], 0 op_sel_hi:[0,1,0] neg_lo:[1,0,0] neg_hi:[1,0,0]
	v_cvt_pk_bf16_f32 v4, v4, v5
	v_cvt_pk_bf16_f32 v5, v2, v3
	ds_write_b64 v186, v[4:5]
	ds_read_b32 v2, v187 offset:200
	s_waitcnt lgkmcnt(0)
	v_pk_fma_f32 v[4:5], v[2:3], v[82:83], 0 op_sel_hi:[0,1,0] neg_lo:[1,0,0] neg_hi:[1,0,0]
	v_pk_fma_f32 v[2:3], v[2:3], v[84:85], 0 op_sel_hi:[0,1,0] neg_lo:[1,0,0] neg_hi:[1,0,0]
	v_cvt_pk_bf16_f32 v4, v4, v5
	v_cvt_pk_bf16_f32 v5, v2, v3
	ds_write_b64 v186, v[4:5] offset:544
	ds_read_b32 v2, v187 offset:208
	s_waitcnt lgkmcnt(0)
	v_pk_fma_f32 v[4:5], v[2:3], v[78:79], 0 op_sel_hi:[0,1,0] neg_lo:[1,0,0] neg_hi:[1,0,0]
	v_pk_fma_f32 v[2:3], v[2:3], v[80:81], 0 op_sel_hi:[0,1,0] neg_lo:[1,0,0] neg_hi:[1,0,0]
	v_cvt_pk_bf16_f32 v4, v4, v5
	v_cvt_pk_bf16_f32 v5, v2, v3
	ds_write_b64 v186, v[4:5] offset:1088
	ds_read_b32 v2, v187 offset:216
	s_waitcnt lgkmcnt(0)
	v_pk_fma_f32 v[4:5], v[2:3], v[70:71], 0 op_sel_hi:[0,1,0] neg_lo:[1,0,0] neg_hi:[1,0,0]
	v_pk_fma_f32 v[2:3], v[2:3], v[72:73], 0 op_sel_hi:[0,1,0] neg_lo:[1,0,0] neg_hi:[1,0,0]
	v_cvt_pk_bf16_f32 v4, v4, v5
	v_cvt_pk_bf16_f32 v5, v2, v3
	ds_write_b64 v186, v[4:5] offset:1632
	ds_read_b32 v2, v187 offset:224
	s_waitcnt lgkmcnt(0)
	v_pk_fma_f32 v[4:5], v[2:3], v[66:67], 0 op_sel_hi:[0,1,0] neg_lo:[1,0,0] neg_hi:[1,0,0]
	v_pk_fma_f32 v[2:3], v[2:3], v[68:69], 0 op_sel_hi:[0,1,0] neg_lo:[1,0,0] neg_hi:[1,0,0]
	v_cvt_pk_bf16_f32 v4, v4, v5
	v_cvt_pk_bf16_f32 v5, v2, v3
	ds_write_b64 v186, v[4:5] offset:2176
	ds_read_b32 v2, v187 offset:232
	s_waitcnt lgkmcnt(0)
	v_pk_fma_f32 v[4:5], v[2:3], v[62:63], 0 op_sel_hi:[0,1,0] neg_lo:[1,0,0] neg_hi:[1,0,0]
	v_pk_fma_f32 v[2:3], v[2:3], v[64:65], 0 op_sel_hi:[0,1,0] neg_lo:[1,0,0] neg_hi:[1,0,0]
	v_cvt_pk_bf16_f32 v4, v4, v5
	v_cvt_pk_bf16_f32 v5, v2, v3
	ds_write_b64 v186, v[4:5] offset:2720
	ds_read_b32 v2, v187 offset:240
	s_waitcnt lgkmcnt(0)
	v_pk_fma_f32 v[4:5], v[2:3], v[54:55], 0 op_sel_hi:[0,1,0] neg_lo:[1,0,0] neg_hi:[1,0,0]
	v_pk_fma_f32 v[2:3], v[2:3], v[56:57], 0 op_sel_hi:[0,1,0] neg_lo:[1,0,0] neg_hi:[1,0,0]
	v_cvt_pk_bf16_f32 v4, v4, v5
	v_cvt_pk_bf16_f32 v5, v2, v3
	ds_write_b64 v186, v[4:5] offset:3264
	ds_read_b32 v2, v187 offset:248
	s_waitcnt lgkmcnt(0)
	v_pk_fma_f32 v[4:5], v[2:3], v[46:47], 0 op_sel_hi:[0,1,0] neg_lo:[1,0,0] neg_hi:[1,0,0]
	v_pk_fma_f32 v[2:3], v[2:3], v[48:49], 0 op_sel_hi:[0,1,0] neg_lo:[1,0,0] neg_hi:[1,0,0]
	v_cvt_pk_bf16_f32 v4, v4, v5
	v_cvt_pk_bf16_f32 v5, v2, v3
	ds_write_b64 v186, v[4:5] offset:3808
	ds_read_b128 v[2:5], v1
	s_waitcnt lgkmcnt(0)
	ds_write_b128 v184, v[2:5] offset:12288
	ds_read_b128 v[2:5], v1 offset:64
	s_waitcnt lgkmcnt(0)
	ds_write_b128 v184, v[2:5] offset:13312
	ds_read_b128 v[2:5], v1 offset:128
	s_waitcnt lgkmcnt(0)
	ds_write_b128 v184, v[2:5] offset:14336
	ds_read_b128 v[2:5], v1 offset:192
	s_waitcnt lgkmcnt(0)
	ds_write_b128 v184, v[2:5] offset:15360
	s_lshl_b32 s24, s22, 2
	s_mov_b32 s25, s21
	v_lshl_add_u64 v[2:3], v[126:127], 0, s[24:25]
	v_lshl_add_u64 v[6:7], v[134:135], 0, s[24:25]
	v_lshl_add_u64 v[8:9], v[136:137], 0, s[24:25]
	v_lshl_add_u64 v[14:15], v[142:143], 0, s[24:25]
	v_lshl_add_u64 v[4:5], v[128:129], 0, s[24:25]
	v_lshl_add_u64 v[10:11], v[138:139], 0, s[24:25]
	v_lshl_add_u64 v[12:13], v[140:141], 0, s[24:25]
	v_lshl_add_u64 v[18:19], v[144:145], 0, s[24:25]
	global_load_dwordx4 v[94:97], v[2:3], off sc0 sc1 nt
	global_load_dwordx4 v[90:93], v[4:5], off sc0 sc1 nt
	global_load_dwordx4 v[82:85], v[6:7], off sc0 sc1 nt
	global_load_dwordx4 v[70:73], v[8:9], off sc0 sc1 nt
	global_load_dwordx4 v[54:57], v[10:11], off sc0 sc1 nt
	global_load_dwordx4 v[26:29], v[12:13], off sc0 sc1 nt
	s_nop 0
	global_load_dwordx4 v[14:17], v[14:15], off sc0 sc1 nt
	s_nop 0
	global_load_dwordx4 v[6:9], v[18:19], off sc0 sc1 nt
	v_mov_b32_e32 v2, v197
	s_waitcnt vmcnt(23)
	s_waitcnt vmcnt(22)
	s_waitcnt vmcnt(21)
	s_waitcnt vmcnt(20)
	s_waitcnt vmcnt(19)
	s_waitcnt vmcnt(18)
	s_waitcnt vmcnt(17)
	s_waitcnt vmcnt(16)
	ds_read_b32 v2, v187 offset:192
	s_waitcnt lgkmcnt(0)
	v_pk_fma_f32 v[4:5], v[2:3], v[122:123], 0 op_sel_hi:[0,1,0] neg_lo:[1,0,0] neg_hi:[1,0,0]
	v_pk_fma_f32 v[2:3], v[2:3], v[124:125], 0 op_sel_hi:[0,1,0] neg_lo:[1,0,0] neg_hi:[1,0,0]
	v_cvt_pk_bf16_f32 v4, v4, v5
	v_cvt_pk_bf16_f32 v5, v2, v3
	ds_write_b64 v186, v[4:5]
	ds_read_b32 v2, v187 offset:200
	s_waitcnt lgkmcnt(0)
	v_pk_fma_f32 v[4:5], v[2:3], v[114:115], 0 op_sel_hi:[0,1,0] neg_lo:[1,0,0] neg_hi:[1,0,0]
	v_pk_fma_f32 v[2:3], v[2:3], v[116:117], 0 op_sel_hi:[0,1,0] neg_lo:[1,0,0] neg_hi:[1,0,0]
	v_cvt_pk_bf16_f32 v4, v4, v5
	v_cvt_pk_bf16_f32 v5, v2, v3
	ds_write_b64 v186, v[4:5] offset:544
	ds_read_b32 v2, v187 offset:208
	s_waitcnt lgkmcnt(0)
	v_pk_fma_f32 v[4:5], v[2:3], v[106:107], 0 op_sel_hi:[0,1,0] neg_lo:[1,0,0] neg_hi:[1,0,0]
	v_pk_fma_f32 v[2:3], v[2:3], v[108:109], 0 op_sel_hi:[0,1,0] neg_lo:[1,0,0] neg_hi:[1,0,0]
	v_cvt_pk_bf16_f32 v4, v4, v5
	v_cvt_pk_bf16_f32 v5, v2, v3
	ds_write_b64 v186, v[4:5] offset:1088
	ds_read_b32 v2, v187 offset:216
	s_waitcnt lgkmcnt(0)
	v_pk_fma_f32 v[4:5], v[2:3], v[86:87], 0 op_sel_hi:[0,1,0] neg_lo:[1,0,0] neg_hi:[1,0,0]
	v_pk_fma_f32 v[2:3], v[2:3], v[88:89], 0 op_sel_hi:[0,1,0] neg_lo:[1,0,0] neg_hi:[1,0,0]
	v_cvt_pk_bf16_f32 v4, v4, v5
	v_cvt_pk_bf16_f32 v5, v2, v3
	ds_write_b64 v186, v[4:5] offset:1632
	ds_read_b32 v2, v187 offset:224
	s_waitcnt lgkmcnt(0)
	v_pk_fma_f32 v[4:5], v[2:3], v[74:75], 0 op_sel_hi:[0,1,0] neg_lo:[1,0,0] neg_hi:[1,0,0]
	v_pk_fma_f32 v[2:3], v[2:3], v[76:77], 0 op_sel_hi:[0,1,0] neg_lo:[1,0,0] neg_hi:[1,0,0]
	v_cvt_pk_bf16_f32 v4, v4, v5
	v_cvt_pk_bf16_f32 v5, v2, v3
	ds_write_b64 v186, v[4:5] offset:2176
	ds_read_b32 v2, v187 offset:232
	s_waitcnt lgkmcnt(0)
	v_pk_fma_f32 v[4:5], v[2:3], v[42:43], 0 op_sel_hi:[0,1,0] neg_lo:[1,0,0] neg_hi:[1,0,0]
	v_pk_fma_f32 v[2:3], v[2:3], v[44:45], 0 op_sel_hi:[0,1,0] neg_lo:[1,0,0] neg_hi:[1,0,0]
	v_cvt_pk_bf16_f32 v4, v4, v5
	v_cvt_pk_bf16_f32 v5, v2, v3
	ds_write_b64 v186, v[4:5] offset:2720
	ds_read_b32 v2, v187 offset:240
	s_waitcnt lgkmcnt(0)
	v_pk_fma_f32 v[4:5], v[2:3], v[38:39], 0 op_sel_hi:[0,1,0] neg_lo:[1,0,0] neg_hi:[1,0,0]
	v_pk_fma_f32 v[2:3], v[2:3], v[40:41], 0 op_sel_hi:[0,1,0] neg_lo:[1,0,0] neg_hi:[1,0,0]
	v_cvt_pk_bf16_f32 v4, v4, v5
	v_cvt_pk_bf16_f32 v5, v2, v3
	ds_write_b64 v186, v[4:5] offset:3264
	ds_read_b32 v2, v187 offset:248
	s_waitcnt lgkmcnt(0)
	v_pk_fma_f32 v[4:5], v[2:3], v[34:35], 0 op_sel_hi:[0,1,0] neg_lo:[1,0,0] neg_hi:[1,0,0]
	v_pk_fma_f32 v[2:3], v[2:3], v[36:37], 0 op_sel_hi:[0,1,0] neg_lo:[1,0,0] neg_hi:[1,0,0]
	v_cvt_pk_bf16_f32 v4, v4, v5
	v_cvt_pk_bf16_f32 v5, v2, v3
	ds_write_b64 v186, v[4:5] offset:3808
	ds_read_b128 v[2:5], v1
	s_waitcnt lgkmcnt(0)
	ds_write_b128 v184, v[2:5] offset:16384
	ds_read_b128 v[2:5], v1 offset:64
	s_waitcnt lgkmcnt(0)
	ds_write_b128 v184, v[2:5] offset:17408
	ds_read_b128 v[2:5], v1 offset:128
	s_waitcnt lgkmcnt(0)
	ds_write_b128 v184, v[2:5] offset:18432
	ds_read_b128 v[2:5], v1 offset:192
	s_waitcnt lgkmcnt(0)
	ds_write_b128 v184, v[2:5] offset:19456
	s_lshl_b32 s22, s7, 2
	s_mov_b32 s23, s21
	v_lshl_add_u64 v[2:3], v[126:127], 0, s[22:23]
	v_lshl_add_u64 v[4:5], v[128:129], 0, s[22:23]
	v_lshl_add_u64 v[10:11], v[134:135], 0, s[22:23]
	v_lshl_add_u64 v[12:13], v[136:137], 0, s[22:23]
	v_lshl_add_u64 v[34:35], v[138:139], 0, s[22:23]
	v_lshl_add_u64 v[36:37], v[140:141], 0, s[22:23]
	v_lshl_add_u64 v[46:47], v[142:143], 0, s[22:23]
	v_lshl_add_u64 v[48:49], v[144:145], 0, s[22:23]
	global_load_dwordx4 v[86:89], v[2:3], off sc0 sc1 nt
	global_load_dwordx4 v[78:81], v[4:5], off sc0 sc1 nt
	global_load_dwordx4 v[66:69], v[10:11], off sc0 sc1 nt
	global_load_dwordx4 v[42:45], v[12:13], off sc0 sc1 nt
	global_load_dwordx4 v[38:41], v[34:35], off sc0 sc1 nt
	global_load_dwordx4 v[18:21], v[36:37], off sc0 sc1 nt
	s_nop 0
	global_load_dwordx4 v[10:13], v[46:47], off sc0 sc1 nt
	global_load_dwordx4 v[2:5], v[48:49], off sc0 sc1 nt
	v_mov_b32_e32 v34, v196
	s_waitcnt vmcnt(23)
	s_waitcnt vmcnt(22)
	s_waitcnt vmcnt(21)
	s_waitcnt vmcnt(20)
	s_waitcnt vmcnt(19)
	s_waitcnt vmcnt(18)
	s_waitcnt vmcnt(17)
	s_waitcnt vmcnt(16)
	ds_read_b32 v34, v187 offset:192
	s_waitcnt lgkmcnt(0)
	v_pk_fma_f32 v[36:37], v[34:35], v[118:119], 0 op_sel_hi:[0,1,0] neg_lo:[1,0,0] neg_hi:[1,0,0]
	v_pk_fma_f32 v[34:35], v[34:35], v[120:121], 0 op_sel_hi:[0,1,0] neg_lo:[1,0,0] neg_hi:[1,0,0]
	v_cvt_pk_bf16_f32 v36, v36, v37
	v_cvt_pk_bf16_f32 v37, v34, v35
	ds_write_b64 v186, v[36:37]
	ds_read_b32 v34, v187 offset:200
	s_waitcnt lgkmcnt(0)
	v_pk_fma_f32 v[36:37], v[34:35], v[110:111], 0 op_sel_hi:[0,1,0] neg_lo:[1,0,0] neg_hi:[1,0,0]
	v_pk_fma_f32 v[34:35], v[34:35], v[112:113], 0 op_sel_hi:[0,1,0] neg_lo:[1,0,0] neg_hi:[1,0,0]
	v_cvt_pk_bf16_f32 v36, v36, v37
	v_cvt_pk_bf16_f32 v37, v34, v35
	ds_write_b64 v186, v[36:37] offset:544
	ds_read_b32 v34, v187 offset:208
	s_waitcnt lgkmcnt(0)
	v_pk_fma_f32 v[36:37], v[34:35], v[102:103], 0 op_sel_hi:[0,1,0] neg_lo:[1,0,0] neg_hi:[1,0,0]
	v_pk_fma_f32 v[34:35], v[34:35], v[104:105], 0 op_sel_hi:[0,1,0] neg_lo:[1,0,0] neg_hi:[1,0,0]
	v_cvt_pk_bf16_f32 v36, v36, v37
	v_cvt_pk_bf16_f32 v37, v34, v35
	ds_write_b64 v186, v[36:37] offset:1088
	ds_read_b32 v34, v187 offset:216
	s_waitcnt lgkmcnt(0)
	v_pk_fma_f32 v[36:37], v[34:35], v[98:99], 0 op_sel_hi:[0,1,0] neg_lo:[1,0,0] neg_hi:[1,0,0]
	v_pk_fma_f32 v[34:35], v[34:35], v[100:101], 0 op_sel_hi:[0,1,0] neg_lo:[1,0,0] neg_hi:[1,0,0]
	v_cvt_pk_bf16_f32 v36, v36, v37
	v_cvt_pk_bf16_f32 v37, v34, v35
	ds_write_b64 v186, v[36:37] offset:1632
	ds_read_b32 v34, v187 offset:224
	s_waitcnt lgkmcnt(0)
	v_pk_fma_f32 v[36:37], v[34:35], v[58:59], 0 op_sel_hi:[0,1,0] neg_lo:[1,0,0] neg_hi:[1,0,0]
	v_pk_fma_f32 v[34:35], v[34:35], v[60:61], 0 op_sel_hi:[0,1,0] neg_lo:[1,0,0] neg_hi:[1,0,0]
	v_cvt_pk_bf16_f32 v36, v36, v37
	v_cvt_pk_bf16_f32 v37, v34, v35
	ds_write_b64 v186, v[36:37] offset:2176
	ds_read_b32 v34, v187 offset:232
	s_waitcnt lgkmcnt(0)
	v_pk_fma_f32 v[36:37], v[34:35], v[50:51], 0 op_sel_hi:[0,1,0] neg_lo:[1,0,0] neg_hi:[1,0,0]
	v_pk_fma_f32 v[34:35], v[34:35], v[52:53], 0 op_sel_hi:[0,1,0] neg_lo:[1,0,0] neg_hi:[1,0,0]
	v_cvt_pk_bf16_f32 v36, v36, v37
	v_cvt_pk_bf16_f32 v37, v34, v35
	ds_write_b64 v186, v[36:37] offset:2720
	ds_read_b32 v34, v187 offset:240
	s_waitcnt lgkmcnt(0)
	v_pk_fma_f32 v[30:31], v[34:35], v[30:31], 0 op_sel_hi:[0,1,0] neg_lo:[1,0,0] neg_hi:[1,0,0]
	v_pk_fma_f32 v[32:33], v[34:35], v[32:33], 0 op_sel_hi:[0,1,0] neg_lo:[1,0,0] neg_hi:[1,0,0]
	v_cvt_pk_bf16_f32 v30, v30, v31
	v_cvt_pk_bf16_f32 v31, v32, v33
	ds_write_b64 v186, v[30:31] offset:3264
	ds_read_b32 v30, v187 offset:248
	s_waitcnt lgkmcnt(0)
	v_pk_fma_f32 v[22:23], v[30:31], v[22:23], 0 op_sel_hi:[0,1,0] neg_lo:[1,0,0] neg_hi:[1,0,0]
	v_pk_fma_f32 v[24:25], v[30:31], v[24:25], 0 op_sel_hi:[0,1,0] neg_lo:[1,0,0] neg_hi:[1,0,0]
	v_cvt_pk_bf16_f32 v22, v22, v23
	v_cvt_pk_bf16_f32 v23, v24, v25
	ds_write_b64 v186, v[22:23] offset:3808
	ds_read_b128 v[22:25], v1
	s_waitcnt lgkmcnt(0)
	ds_write_b128 v184, v[22:25] offset:20480
	ds_read_b128 v[22:25], v1 offset:64
	s_waitcnt lgkmcnt(0)
	ds_write_b128 v184, v[22:25] offset:21504
	ds_read_b128 v[22:25], v1 offset:128
	s_waitcnt lgkmcnt(0)
	ds_write_b128 v184, v[22:25] offset:22528
	ds_read_b128 v[22:25], v1 offset:192
	s_waitcnt lgkmcnt(0)
	ds_write_b128 v184, v[22:25] offset:23552
	v_lshl_add_u64 v[22:23], v[130:131], 0, s[30:31]
	s_movk_i32 s7, 0x2000
	v_add_co_u32_e32 v24, vcc, s7, v22
	s_movk_i32 s36, 0x4000
	s_nop 0
	v_addc_co_u32_e32 v25, vcc, 0, v23, vcc
	global_load_dwordx4 v[74:77], v[22:23], off sc0 sc1 nt
	global_load_dwordx4 v[62:65], v[24:25], off sc0 sc1 nt
	v_add_co_u32_e32 v24, vcc, s36, v22
	s_movk_i32 s37, 0x6000
	s_nop 0
	v_addc_co_u32_e32 v25, vcc, 0, v23, vcc
	v_add_co_u32_e32 v30, vcc, s37, v22
	s_mov_b32 s38, 0x8000
	s_nop 0
	v_addc_co_u32_e32 v31, vcc, 0, v23, vcc
	global_load_dwordx4 v[58:61], v[24:25], off sc0 sc1 nt
	global_load_dwordx4 v[46:49], v[30:31], off sc0 sc1 nt
	v_add_co_u32_e32 v24, vcc, s38, v22
	s_mov_b32 s39, 0xa000
	s_nop 0
	v_addc_co_u32_e32 v25, vcc, 0, v23, vcc
	v_add_co_u32_e32 v34, vcc, s39, v22
	s_mov_b32 s41, 0xc000
	s_nop 0
	v_addc_co_u32_e32 v35, vcc, 0, v23, vcc
	global_load_dwordx4 v[50:53], v[24:25], off sc0 sc1 nt
	global_load_dwordx4 v[30:33], v[34:35], off sc0 sc1 nt
	v_add_co_u32_e32 v24, vcc, s41, v22
	s_mov_b32 s42, 0xe000
	s_nop 0
	v_addc_co_u32_e32 v25, vcc, 0, v23, vcc
	v_add_co_u32_e32 v22, vcc, s42, v22
	s_nop 1
	v_addc_co_u32_e32 v23, vcc, 0, v23, vcc
	global_load_dwordx4 v[34:37], v[24:25], off sc0 sc1 nt
	s_nop 0
	global_load_dwordx4 v[22:25], v[22:23], off sc0 sc1 nt
	v_mov_b32_e32 v98, v195
	s_waitcnt vmcnt(23)
	s_waitcnt vmcnt(22)
	s_waitcnt vmcnt(21)
	s_waitcnt vmcnt(20)
	s_waitcnt vmcnt(19)
	s_waitcnt vmcnt(18)
	s_waitcnt vmcnt(17)
	s_waitcnt vmcnt(16)
	ds_read_b32 v98, v187 offset:192
	s_waitcnt lgkmcnt(0)
	v_pk_fma_f32 v[94:95], v[98:99], v[94:95], 0 op_sel_hi:[0,1,0] neg_lo:[1,0,0] neg_hi:[1,0,0]
	v_pk_fma_f32 v[96:97], v[98:99], v[96:97], 0 op_sel_hi:[0,1,0] neg_lo:[1,0,0] neg_hi:[1,0,0]
	v_cvt_pk_bf16_f32 v94, v94, v95
	v_cvt_pk_bf16_f32 v95, v96, v97
	ds_write_b64 v186, v[94:95]
	ds_read_b32 v94, v187 offset:200
	s_waitcnt lgkmcnt(0)
	v_pk_fma_f32 v[90:91], v[94:95], v[90:91], 0 op_sel_hi:[0,1,0] neg_lo:[1,0,0] neg_hi:[1,0,0]
	v_pk_fma_f32 v[92:93], v[94:95], v[92:93], 0 op_sel_hi:[0,1,0] neg_lo:[1,0,0] neg_hi:[1,0,0]
	v_cvt_pk_bf16_f32 v90, v90, v91
	v_cvt_pk_bf16_f32 v91, v92, v93
	ds_write_b64 v186, v[90:91] offset:544
	ds_read_b32 v90, v187 offset:208
	s_waitcnt lgkmcnt(0)
	v_pk_fma_f32 v[82:83], v[90:91], v[82:83], 0 op_sel_hi:[0,1,0] neg_lo:[1,0,0] neg_hi:[1,0,0]
	v_pk_fma_f32 v[84:85], v[90:91], v[84:85], 0 op_sel_hi:[0,1,0] neg_lo:[1,0,0] neg_hi:[1,0,0]
	v_cvt_pk_bf16_f32 v82, v82, v83
	v_cvt_pk_bf16_f32 v83, v84, v85
	ds_write_b64 v186, v[82:83] offset:1088
	ds_read_b32 v82, v187 offset:216
	s_waitcnt lgkmcnt(0)
	v_pk_fma_f32 v[70:71], v[82:83], v[70:71], 0 op_sel_hi:[0,1,0] neg_lo:[1,0,0] neg_hi:[1,0,0]
	v_pk_fma_f32 v[72:73], v[82:83], v[72:73], 0 op_sel_hi:[0,1,0] neg_lo:[1,0,0] neg_hi:[1,0,0]
	v_cvt_pk_bf16_f32 v70, v70, v71
	v_cvt_pk_bf16_f32 v71, v72, v73
	ds_write_b64 v186, v[70:71] offset:1632
	ds_read_b32 v70, v187 offset:224
	s_waitcnt lgkmcnt(0)
	v_pk_fma_f32 v[54:55], v[70:71], v[54:55], 0 op_sel_hi:[0,1,0] neg_lo:[1,0,0] neg_hi:[1,0,0]
	v_pk_fma_f32 v[56:57], v[70:71], v[56:57], 0 op_sel_hi:[0,1,0] neg_lo:[1,0,0] neg_hi:[1,0,0]
	v_cvt_pk_bf16_f32 v54, v54, v55
	v_cvt_pk_bf16_f32 v55, v56, v57
	ds_write_b64 v186, v[54:55] offset:2176
	ds_read_b32 v54, v187 offset:232
	s_waitcnt lgkmcnt(0)
	v_pk_fma_f32 v[26:27], v[54:55], v[26:27], 0 op_sel_hi:[0,1,0] neg_lo:[1,0,0] neg_hi:[1,0,0]
	v_pk_fma_f32 v[28:29], v[54:55], v[28:29], 0 op_sel_hi:[0,1,0] neg_lo:[1,0,0] neg_hi:[1,0,0]
	v_cvt_pk_bf16_f32 v26, v26, v27
	v_cvt_pk_bf16_f32 v27, v28, v29
	ds_write_b64 v186, v[26:27] offset:2720
	ds_read_b32 v26, v187 offset:240
	s_waitcnt lgkmcnt(0)
	v_pk_fma_f32 v[14:15], v[26:27], v[14:15], 0 op_sel_hi:[0,1,0] neg_lo:[1,0,0] neg_hi:[1,0,0]
	v_pk_fma_f32 v[16:17], v[26:27], v[16:17], 0 op_sel_hi:[0,1,0] neg_lo:[1,0,0] neg_hi:[1,0,0]
	v_cvt_pk_bf16_f32 v14, v14, v15
	v_cvt_pk_bf16_f32 v15, v16, v17
	ds_write_b64 v186, v[14:15] offset:3264
	ds_read_b32 v14, v187 offset:248
	s_waitcnt lgkmcnt(0)
	v_pk_fma_f32 v[6:7], v[14:15], v[6:7], 0 op_sel_hi:[0,1,0] neg_lo:[1,0,0] neg_hi:[1,0,0]
	v_pk_fma_f32 v[8:9], v[14:15], v[8:9], 0 op_sel_hi:[0,1,0] neg_lo:[1,0,0] neg_hi:[1,0,0]
	v_cvt_pk_bf16_f32 v6, v6, v7
	v_cvt_pk_bf16_f32 v7, v8, v9
	ds_write_b64 v186, v[6:7] offset:3808
	ds_read_b128 v[6:9], v1
	s_waitcnt lgkmcnt(0)
	ds_write_b128 v184, v[6:9] offset:24576
	ds_read_b128 v[6:9], v1 offset:64
	s_waitcnt lgkmcnt(0)
	ds_write_b128 v184, v[6:9] offset:25600
	ds_read_b128 v[6:9], v1 offset:128
	s_waitcnt lgkmcnt(0)
	ds_write_b128 v184, v[6:9] offset:26624
	ds_read_b128 v[6:9], v1 offset:192
	s_waitcnt lgkmcnt(0)
	ds_write_b128 v184, v[6:9] offset:27648
	s_mov_b64 s[44:45], 0x10000
	v_lshl_add_u64 v[150:151], v[130:131], 0, s[44:45]
	s_mov_b64 s[44:45], 0x12000
	v_lshl_add_u64 v[152:153], v[130:131], 0, s[44:45]
	s_mov_b64 s[44:45], 0x14000
	v_lshl_add_u64 v[156:157], v[130:131], 0, s[44:45]
	s_mov_b64 s[44:45], 0x16000
	v_lshl_add_u64 v[158:159], v[130:131], 0, s[44:45]
	s_mov_b64 s[44:45], 0x18000
	v_lshl_add_u64 v[160:161], v[130:131], 0, s[44:45]
	s_mov_b64 s[44:45], 0x1a000
	v_lshl_add_u64 v[162:163], v[130:131], 0, s[44:45]
	s_mov_b64 s[44:45], 0x1c000
	v_lshl_add_u64 v[164:165], v[130:131], 0, s[44:45]
	s_mov_b64 s[44:45], 0x1e000
	v_lshl_add_u64 v[6:7], v[150:151], 0, s[30:31]
	v_lshl_add_u64 v[8:9], v[152:153], 0, s[30:31]
	v_lshl_add_u64 v[14:15], v[156:157], 0, s[30:31]
	v_lshl_add_u64 v[16:17], v[158:159], 0, s[30:31]
	v_lshl_add_u64 v[26:27], v[160:161], 0, s[30:31]
	v_lshl_add_u64 v[28:29], v[162:163], 0, s[30:31]
	v_lshl_add_u64 v[166:167], v[130:131], 0, s[44:45]
	v_lshl_add_u64 v[98:99], v[164:165], 0, s[30:31]
	v_lshl_add_u64 v[100:101], v[166:167], 0, s[30:31]
	global_load_dwordx4 v[94:97], v[6:7], off sc0 sc1 nt
	global_load_dwordx4 v[90:93], v[8:9], off sc0 sc1 nt
	global_load_dwordx4 v[82:85], v[14:15], off sc0 sc1 nt
	global_load_dwordx4 v[70:73], v[16:17], off sc0 sc1 nt
	global_load_dwordx4 v[54:57], v[26:27], off sc0 sc1 nt
	s_nop 0
	global_load_dwordx4 v[26:29], v[28:29], off sc0 sc1 nt
	s_nop 0
	global_load_dwordx4 v[14:17], v[98:99], off sc0 sc1 nt
	global_load_dwordx4 v[6:9], v[100:101], off sc0 sc1 nt
	v_mov_b32_e32 v98, v194
	s_waitcnt vmcnt(23)
	s_waitcnt vmcnt(22)
	s_waitcnt vmcnt(21)
	s_waitcnt vmcnt(20)
	s_waitcnt vmcnt(19)
	s_waitcnt vmcnt(18)
	s_waitcnt vmcnt(17)
	s_waitcnt vmcnt(16)
	ds_read_b32 v98, v187 offset:192
	s_waitcnt lgkmcnt(0)
	v_pk_fma_f32 v[86:87], v[98:99], v[86:87], 0 op_sel_hi:[0,1,0] neg_lo:[1,0,0] neg_hi:[1,0,0]
	v_pk_fma_f32 v[88:89], v[98:99], v[88:89], 0 op_sel_hi:[0,1,0] neg_lo:[1,0,0] neg_hi:[1,0,0]
	v_cvt_pk_bf16_f32 v86, v86, v87
	v_cvt_pk_bf16_f32 v87, v88, v89
	ds_write_b64 v186, v[86:87]
	ds_read_b32 v86, v187 offset:200
	s_waitcnt lgkmcnt(0)
	v_pk_fma_f32 v[78:79], v[86:87], v[78:79], 0 op_sel_hi:[0,1,0] neg_lo:[1,0,0] neg_hi:[1,0,0]
	v_pk_fma_f32 v[80:81], v[86:87], v[80:81], 0 op_sel_hi:[0,1,0] neg_lo:[1,0,0] neg_hi:[1,0,0]
	v_cvt_pk_bf16_f32 v78, v78, v79
	v_cvt_pk_bf16_f32 v79, v80, v81
	ds_write_b64 v186, v[78:79] offset:544
	ds_read_b32 v78, v187 offset:208
	s_waitcnt lgkmcnt(0)
	v_pk_fma_f32 v[66:67], v[78:79], v[66:67], 0 op_sel_hi:[0,1,0] neg_lo:[1,0,0] neg_hi:[1,0,0]
	v_pk_fma_f32 v[68:69], v[78:79], v[68:69], 0 op_sel_hi:[0,1,0] neg_lo:[1,0,0] neg_hi:[1,0,0]
	v_cvt_pk_bf16_f32 v66, v66, v67
	v_cvt_pk_bf16_f32 v67, v68, v69
	ds_write_b64 v186, v[66:67] offset:1088
	ds_read_b32 v66, v187 offset:216
	s_waitcnt lgkmcnt(0)
	v_pk_fma_f32 v[42:43], v[66:67], v[42:43], 0 op_sel_hi:[0,1,0] neg_lo:[1,0,0] neg_hi:[1,0,0]
	v_pk_fma_f32 v[44:45], v[66:67], v[44:45], 0 op_sel_hi:[0,1,0] neg_lo:[1,0,0] neg_hi:[1,0,0]
	v_cvt_pk_bf16_f32 v42, v42, v43
	v_cvt_pk_bf16_f32 v43, v44, v45
	ds_write_b64 v186, v[42:43] offset:1632
	ds_read_b32 v42, v187 offset:224
	s_waitcnt lgkmcnt(0)
	v_pk_fma_f32 v[38:39], v[42:43], v[38:39], 0 op_sel_hi:[0,1,0] neg_lo:[1,0,0] neg_hi:[1,0,0]
	v_pk_fma_f32 v[40:41], v[42:43], v[40:41], 0 op_sel_hi:[0,1,0] neg_lo:[1,0,0] neg_hi:[1,0,0]
	v_cvt_pk_bf16_f32 v38, v38, v39
	v_cvt_pk_bf16_f32 v39, v40, v41
	ds_write_b64 v186, v[38:39] offset:2176
	ds_read_b32 v38, v187 offset:232
	s_waitcnt lgkmcnt(0)
	v_pk_fma_f32 v[18:19], v[38:39], v[18:19], 0 op_sel_hi:[0,1,0] neg_lo:[1,0,0] neg_hi:[1,0,0]
	v_pk_fma_f32 v[20:21], v[38:39], v[20:21], 0 op_sel_hi:[0,1,0] neg_lo:[1,0,0] neg_hi:[1,0,0]
	v_cvt_pk_bf16_f32 v18, v18, v19
	v_cvt_pk_bf16_f32 v19, v20, v21
	ds_write_b64 v186, v[18:19] offset:2720
	ds_read_b32 v18, v187 offset:240
	s_waitcnt lgkmcnt(0)
	v_pk_fma_f32 v[10:11], v[18:19], v[10:11], 0 op_sel_hi:[0,1,0] neg_lo:[1,0,0] neg_hi:[1,0,0]
	v_pk_fma_f32 v[12:13], v[18:19], v[12:13], 0 op_sel_hi:[0,1,0] neg_lo:[1,0,0] neg_hi:[1,0,0]
	v_cvt_pk_bf16_f32 v10, v10, v11
	v_cvt_pk_bf16_f32 v11, v12, v13
	ds_write_b64 v186, v[10:11] offset:3264
	ds_read_b32 v10, v187 offset:248
	s_waitcnt lgkmcnt(0)
	v_pk_fma_f32 v[2:3], v[10:11], v[2:3], 0 op_sel_hi:[0,1,0] neg_lo:[1,0,0] neg_hi:[1,0,0]
	v_pk_fma_f32 v[4:5], v[10:11], v[4:5], 0 op_sel_hi:[0,1,0] neg_lo:[1,0,0] neg_hi:[1,0,0]
	v_cvt_pk_bf16_f32 v2, v2, v3
	v_cvt_pk_bf16_f32 v3, v4, v5
	ds_write_b64 v186, v[2:3] offset:3808
	ds_read_b128 v[2:5], v1
	s_waitcnt lgkmcnt(0)
	ds_write_b128 v184, v[2:5] offset:28672
	ds_read_b128 v[2:5], v1 offset:64
	s_waitcnt lgkmcnt(0)
	ds_write_b128 v184, v[2:5] offset:29696
	ds_read_b128 v[2:5], v1 offset:128
	s_waitcnt lgkmcnt(0)
	ds_write_b128 v184, v[2:5] offset:30720
	ds_read_b128 v[2:5], v1 offset:192
	s_waitcnt lgkmcnt(0)
	ds_write_b128 v184, v[2:5] offset:31744
	s_mov_b64 s[44:45], 0x20000
	v_lshl_add_u64 v[168:169], v[130:131], 0, s[44:45]
	s_mov_b64 s[44:45], 0x22000
	v_lshl_add_u64 v[170:171], v[130:131], 0, s[44:45]
	s_mov_b64 s[44:45], 0x24000
	v_lshl_add_u64 v[172:173], v[130:131], 0, s[44:45]
	s_mov_b64 s[44:45], 0x26000
	v_lshl_add_u64 v[174:175], v[130:131], 0, s[44:45]
	s_mov_b64 s[44:45], 0x28000
	v_lshl_add_u64 v[176:177], v[130:131], 0, s[44:45]
	s_mov_b64 s[44:45], 0x2a000
	v_lshl_add_u64 v[178:179], v[130:131], 0, s[44:45]
	s_mov_b64 s[44:45], 0x2c000
	v_lshl_add_u64 v[180:181], v[130:131], 0, s[44:45]
	s_mov_b64 s[44:45], 0x2e000
	v_lshl_add_u64 v[2:3], v[168:169], 0, s[30:31]
	v_lshl_add_u64 v[4:5], v[170:171], 0, s[30:31]
	v_lshl_add_u64 v[10:11], v[172:173], 0, s[30:31]
	v_lshl_add_u64 v[12:13], v[174:175], 0, s[30:31]
	v_lshl_add_u64 v[18:19], v[176:177], 0, s[30:31]
	v_lshl_add_u64 v[20:21], v[178:179], 0, s[30:31]
	v_lshl_add_u64 v[182:183], v[130:131], 0, s[44:45]
	v_lshl_add_u64 v[42:43], v[180:181], 0, s[30:31]
	v_lshl_add_u64 v[44:45], v[182:183], 0, s[30:31]
	global_load_dwordx4 v[106:109], v[2:3], off sc0 sc1 nt
	global_load_dwordx4 v[98:101], v[4:5], off sc0 sc1 nt
	global_load_dwordx4 v[78:81], v[10:11], off sc0 sc1 nt
	global_load_dwordx4 v[66:69], v[12:13], off sc0 sc1 nt
	global_load_dwordx4 v[38:41], v[18:19], off sc0 sc1 nt
	s_nop 0
	global_load_dwordx4 v[18:21], v[20:21], off sc0 sc1 nt
	s_nop 0
	global_load_dwordx4 v[10:13], v[42:43], off sc0 sc1 nt
	global_load_dwordx4 v[2:5], v[44:45], off sc0 sc1 nt
	v_mov_b32_e32 v42, v198
	s_waitcnt vmcnt(23)
	s_waitcnt vmcnt(22)
	s_waitcnt vmcnt(21)
	s_waitcnt vmcnt(20)
	s_waitcnt vmcnt(19)
	s_waitcnt vmcnt(18)
	s_waitcnt vmcnt(17)
	s_waitcnt vmcnt(16)
	ds_read_b32 v42, v187
	s_waitcnt lgkmcnt(0)
	v_pk_fma_f32 v[44:45], v[42:43], v[74:75], 0 op_sel_hi:[0,1,0] neg_lo:[1,0,0] neg_hi:[1,0,0]
	v_pk_fma_f32 v[42:43], v[42:43], v[76:77], 0 op_sel_hi:[0,1,0] neg_lo:[1,0,0] neg_hi:[1,0,0]
	v_cvt_pk_bf16_f32 v44, v44, v45
	v_cvt_pk_bf16_f32 v45, v42, v43
	ds_write_b64 v186, v[44:45]
	ds_read_b32 v42, v187 offset:8
	s_waitcnt lgkmcnt(0)
	v_pk_fma_f32 v[44:45], v[42:43], v[62:63], 0 op_sel_hi:[0,1,0] neg_lo:[1,0,0] neg_hi:[1,0,0]
	v_pk_fma_f32 v[42:43], v[42:43], v[64:65], 0 op_sel_hi:[0,1,0] neg_lo:[1,0,0] neg_hi:[1,0,0]
	v_cvt_pk_bf16_f32 v44, v44, v45
	v_cvt_pk_bf16_f32 v45, v42, v43
	ds_write_b64 v186, v[44:45] offset:544
	ds_read_b32 v42, v187 offset:16
	s_waitcnt lgkmcnt(0)
	v_pk_fma_f32 v[44:45], v[42:43], v[58:59], 0 op_sel_hi:[0,1,0] neg_lo:[1,0,0] neg_hi:[1,0,0]
	v_pk_fma_f32 v[42:43], v[42:43], v[60:61], 0 op_sel_hi:[0,1,0] neg_lo:[1,0,0] neg_hi:[1,0,0]
	v_cvt_pk_bf16_f32 v44, v44, v45
	v_cvt_pk_bf16_f32 v45, v42, v43
	ds_write_b64 v186, v[44:45] offset:1088
	ds_read_b32 v42, v187 offset:24
	s_waitcnt lgkmcnt(0)
	v_pk_fma_f32 v[44:45], v[42:43], v[46:47], 0 op_sel_hi:[0,1,0] neg_lo:[1,0,0] neg_hi:[1,0,0]
	v_pk_fma_f32 v[42:43], v[42:43], v[48:49], 0 op_sel_hi:[0,1,0] neg_lo:[1,0,0] neg_hi:[1,0,0]
	v_cvt_pk_bf16_f32 v44, v44, v45
	v_cvt_pk_bf16_f32 v45, v42, v43
	ds_write_b64 v186, v[44:45] offset:1632
	ds_read_b32 v42, v187 offset:32
	s_waitcnt lgkmcnt(0)
	v_pk_fma_f32 v[44:45], v[42:43], v[50:51], 0 op_sel_hi:[0,1,0] neg_lo:[1,0,0] neg_hi:[1,0,0]
	v_pk_fma_f32 v[42:43], v[42:43], v[52:53], 0 op_sel_hi:[0,1,0] neg_lo:[1,0,0] neg_hi:[1,0,0]
	v_cvt_pk_bf16_f32 v44, v44, v45
	v_cvt_pk_bf16_f32 v45, v42, v43
	ds_write_b64 v186, v[44:45] offset:2176
	ds_read_b32 v42, v187 offset:40
	s_waitcnt lgkmcnt(0)
	v_pk_fma_f32 v[30:31], v[42:43], v[30:31], 0 op_sel_hi:[0,1,0] neg_lo:[1,0,0] neg_hi:[1,0,0]
	v_pk_fma_f32 v[32:33], v[42:43], v[32:33], 0 op_sel_hi:[0,1,0] neg_lo:[1,0,0] neg_hi:[1,0,0]
	v_cvt_pk_bf16_f32 v30, v30, v31
	v_cvt_pk_bf16_f32 v31, v32, v33
	ds_write_b64 v186, v[30:31] offset:2720
	ds_read_b32 v30, v187 offset:48
	s_waitcnt lgkmcnt(0)
	v_pk_fma_f32 v[32:33], v[30:31], v[34:35], 0 op_sel_hi:[0,1,0] neg_lo:[1,0,0] neg_hi:[1,0,0]
	v_pk_fma_f32 v[30:31], v[30:31], v[36:37], 0 op_sel_hi:[0,1,0] neg_lo:[1,0,0] neg_hi:[1,0,0]
	v_cvt_pk_bf16_f32 v32, v32, v33
	v_cvt_pk_bf16_f32 v33, v30, v31
	ds_write_b64 v186, v[32:33] offset:3264
	ds_read_b32 v30, v187 offset:56
	s_waitcnt lgkmcnt(0)
	v_pk_fma_f32 v[22:23], v[30:31], v[22:23], 0 op_sel_hi:[0,1,0] neg_lo:[1,0,0] neg_hi:[1,0,0]
	v_pk_fma_f32 v[24:25], v[30:31], v[24:25], 0 op_sel_hi:[0,1,0] neg_lo:[1,0,0] neg_hi:[1,0,0]
	v_cvt_pk_bf16_f32 v22, v22, v23
	v_cvt_pk_bf16_f32 v23, v24, v25
	ds_write_b64 v186, v[22:23] offset:3808
	ds_read_b128 a[0:3], v1
	ds_read_b128 a[4:7], v1 offset:64
	ds_read_b128 a[8:11], v1 offset:128
	ds_read_b128 a[12:15], v1 offset:192
	v_lshl_add_u64 v[22:23], v[130:131], 0, s[28:29]
	v_add_co_u32_e32 v24, vcc, s7, v22
	s_nop 1
	v_addc_co_u32_e32 v25, vcc, 0, v23, vcc
	global_load_dwordx4 v[102:105], v[22:23], off sc0 sc1 nt
	global_load_dwordx4 v[86:89], v[24:25], off sc0 sc1 nt
	v_add_co_u32_e32 v24, vcc, s36, v22
	s_nop 1
	v_addc_co_u32_e32 v25, vcc, 0, v23, vcc
	v_add_co_u32_e32 v30, vcc, s37, v22
	s_nop 1
	v_addc_co_u32_e32 v31, vcc, 0, v23, vcc
	global_load_dwordx4 v[74:77], v[24:25], off sc0 sc1 nt
	global_load_dwordx4 v[62:65], v[30:31], off sc0 sc1 nt
	v_add_co_u32_e32 v24, vcc, s38, v22
	s_nop 1
	v_addc_co_u32_e32 v25, vcc, 0, v23, vcc
	v_add_co_u32_e32 v30, vcc, s39, v22
	s_nop 1
	v_addc_co_u32_e32 v31, vcc, 0, v23, vcc
	global_load_dwordx4 v[58:61], v[24:25], off sc0 sc1 nt
	global_load_dwordx4 v[46:49], v[30:31], off sc0 sc1 nt
	v_add_co_u32_e32 v24, vcc, s41, v22
	s_nop 1
	v_addc_co_u32_e32 v25, vcc, 0, v23, vcc
	v_add_co_u32_e32 v22, vcc, s42, v22
	s_nop 1
	v_addc_co_u32_e32 v23, vcc, 0, v23, vcc
	global_load_dwordx4 v[42:45], v[24:25], off sc0 sc1 nt
	global_load_dwordx4 v[30:33], v[22:23], off sc0 sc1 nt
	v_mov_b32_e32 v22, v198
	s_waitcnt vmcnt(23)
	s_waitcnt vmcnt(22)
	s_waitcnt vmcnt(21)
	s_waitcnt vmcnt(20)
	s_waitcnt vmcnt(19)
	s_waitcnt vmcnt(18)
	s_waitcnt vmcnt(17)
	s_waitcnt vmcnt(16)
	ds_read_b32 v22, v187 offset:64
	s_waitcnt lgkmcnt(0)
	v_pk_fma_f32 v[24:25], v[22:23], v[94:95], 0 op_sel_hi:[0,1,0] neg_lo:[1,0,0] neg_hi:[1,0,0]
	v_pk_fma_f32 v[22:23], v[22:23], v[96:97], 0 op_sel_hi:[0,1,0] neg_lo:[1,0,0] neg_hi:[1,0,0]
	v_cvt_pk_bf16_f32 v24, v24, v25
	v_cvt_pk_bf16_f32 v25, v22, v23
	ds_write_b64 v186, v[24:25]
	ds_read_b32 v22, v187 offset:72
	s_waitcnt lgkmcnt(0)
	v_pk_fma_f32 v[24:25], v[22:23], v[90:91], 0 op_sel_hi:[0,1,0] neg_lo:[1,0,0] neg_hi:[1,0,0]
	v_pk_fma_f32 v[22:23], v[22:23], v[92:93], 0 op_sel_hi:[0,1,0] neg_lo:[1,0,0] neg_hi:[1,0,0]
	v_cvt_pk_bf16_f32 v24, v24, v25
	v_cvt_pk_bf16_f32 v25, v22, v23
	ds_write_b64 v186, v[24:25] offset:544
	ds_read_b32 v22, v187 offset:80
	s_waitcnt lgkmcnt(0)
	v_pk_fma_f32 v[24:25], v[22:23], v[82:83], 0 op_sel_hi:[0,1,0] neg_lo:[1,0,0] neg_hi:[1,0,0]
	v_pk_fma_f32 v[22:23], v[22:23], v[84:85], 0 op_sel_hi:[0,1,0] neg_lo:[1,0,0] neg_hi:[1,0,0]
	v_cvt_pk_bf16_f32 v24, v24, v25
	v_cvt_pk_bf16_f32 v25, v22, v23
	ds_write_b64 v186, v[24:25] offset:1088
	ds_read_b32 v22, v187 offset:88
	s_waitcnt lgkmcnt(0)
	v_pk_fma_f32 v[24:25], v[22:23], v[70:71], 0 op_sel_hi:[0,1,0] neg_lo:[1,0,0] neg_hi:[1,0,0]
	v_pk_fma_f32 v[22:23], v[22:23], v[72:73], 0 op_sel_hi:[0,1,0] neg_lo:[1,0,0] neg_hi:[1,0,0]
	v_cvt_pk_bf16_f32 v24, v24, v25
	v_cvt_pk_bf16_f32 v25, v22, v23
	ds_write_b64 v186, v[24:25] offset:1632
	ds_read_b32 v22, v187 offset:96
	s_waitcnt lgkmcnt(0)
	v_pk_fma_f32 v[24:25], v[22:23], v[54:55], 0 op_sel_hi:[0,1,0] neg_lo:[1,0,0] neg_hi:[1,0,0]
	v_pk_fma_f32 v[22:23], v[22:23], v[56:57], 0 op_sel_hi:[0,1,0] neg_lo:[1,0,0] neg_hi:[1,0,0]
	v_cvt_pk_bf16_f32 v24, v24, v25
	v_cvt_pk_bf16_f32 v25, v22, v23
	ds_write_b64 v186, v[24:25] offset:2176
	ds_read_b32 v22, v187 offset:104
	s_waitcnt lgkmcnt(0)
	v_pk_fma_f32 v[24:25], v[22:23], v[26:27], 0 op_sel_hi:[0,1,0] neg_lo:[1,0,0] neg_hi:[1,0,0]
	v_pk_fma_f32 v[22:23], v[22:23], v[28:29], 0 op_sel_hi:[0,1,0] neg_lo:[1,0,0] neg_hi:[1,0,0]
	v_cvt_pk_bf16_f32 v24, v24, v25
	v_cvt_pk_bf16_f32 v25, v22, v23
	ds_write_b64 v186, v[24:25] offset:2720
	ds_read_b32 v22, v187 offset:112
	s_waitcnt lgkmcnt(0)
	v_pk_fma_f32 v[14:15], v[22:23], v[14:15], 0 op_sel_hi:[0,1,0] neg_lo:[1,0,0] neg_hi:[1,0,0]
	v_pk_fma_f32 v[16:17], v[22:23], v[16:17], 0 op_sel_hi:[0,1,0] neg_lo:[1,0,0] neg_hi:[1,0,0]
	v_cvt_pk_bf16_f32 v14, v14, v15
	v_cvt_pk_bf16_f32 v15, v16, v17
	ds_write_b64 v186, v[14:15] offset:3264
	ds_read_b32 v14, v187 offset:120
	s_waitcnt lgkmcnt(0)
	v_pk_fma_f32 v[6:7], v[14:15], v[6:7], 0 op_sel_hi:[0,1,0] neg_lo:[1,0,0] neg_hi:[1,0,0]
	v_pk_fma_f32 v[8:9], v[14:15], v[8:9], 0 op_sel_hi:[0,1,0] neg_lo:[1,0,0] neg_hi:[1,0,0]
	v_cvt_pk_bf16_f32 v6, v6, v7
	v_cvt_pk_bf16_f32 v7, v8, v9
	ds_write_b64 v186, v[6:7] offset:3808
	ds_read_b128 a[16:19], v1
	ds_read_b128 a[20:23], v1 offset:64
	ds_read_b128 a[24:27], v1 offset:128
	ds_read_b128 a[28:31], v1 offset:192
	v_lshl_add_u64 v[6:7], v[150:151], 0, s[28:29]
	v_lshl_add_u64 v[8:9], v[152:153], 0, s[28:29]
	v_lshl_add_u64 v[14:15], v[156:157], 0, s[28:29]
	v_lshl_add_u64 v[16:17], v[158:159], 0, s[28:29]
	v_lshl_add_u64 v[22:23], v[160:161], 0, s[28:29]
	v_lshl_add_u64 v[24:25], v[162:163], 0, s[28:29]
	v_lshl_add_u64 v[26:27], v[164:165], 0, s[28:29]
	v_lshl_add_u64 v[28:29], v[166:167], 0, s[28:29]
	global_load_dwordx4 v[110:113], v[6:7], off sc0 sc1 nt
	global_load_dwordx4 v[90:93], v[8:9], off sc0 sc1 nt
	global_load_dwordx4 v[70:73], v[14:15], off sc0 sc1 nt
	global_load_dwordx4 v[50:53], v[16:17], off sc0 sc1 nt
	global_load_dwordx4 v[34:37], v[22:23], off sc0 sc1 nt
	s_nop 0
	global_load_dwordx4 v[22:25], v[24:25], off sc0 sc1 nt
	s_nop 0
	global_load_dwordx4 v[14:17], v[26:27], off sc0 sc1 nt
	global_load_dwordx4 v[6:9], v[28:29], off sc0 sc1 nt
	s_waitcnt vmcnt(23)
	s_waitcnt vmcnt(22)
	s_waitcnt vmcnt(21)
	s_waitcnt vmcnt(20)
	s_waitcnt vmcnt(19)
	s_waitcnt vmcnt(18)
	s_waitcnt vmcnt(17)
	s_waitcnt vmcnt(16)
	ds_read_b32 v26, v187 offset:128
	s_waitcnt lgkmcnt(0)
	v_pk_fma_f32 v[28:29], v[26:27], v[106:107], 0 op_sel_hi:[0,1,0] neg_lo:[1,0,0] neg_hi:[1,0,0]
	v_pk_fma_f32 v[26:27], v[26:27], v[108:109], 0 op_sel_hi:[0,1,0] neg_lo:[1,0,0] neg_hi:[1,0,0]
	v_cvt_pk_bf16_f32 v28, v28, v29
	v_cvt_pk_bf16_f32 v29, v26, v27
	ds_write_b64 v186, v[28:29]
	ds_read_b32 v26, v187 offset:136
	s_waitcnt lgkmcnt(0)
	v_pk_fma_f32 v[28:29], v[26:27], v[98:99], 0 op_sel_hi:[0,1,0] neg_lo:[1,0,0] neg_hi:[1,0,0]
	v_pk_fma_f32 v[26:27], v[26:27], v[100:101], 0 op_sel_hi:[0,1,0] neg_lo:[1,0,0] neg_hi:[1,0,0]
	v_cvt_pk_bf16_f32 v28, v28, v29
	v_cvt_pk_bf16_f32 v29, v26, v27
	ds_write_b64 v186, v[28:29] offset:544
	ds_read_b32 v26, v187 offset:144
	s_waitcnt lgkmcnt(0)
	v_pk_fma_f32 v[28:29], v[26:27], v[78:79], 0 op_sel_hi:[0,1,0] neg_lo:[1,0,0] neg_hi:[1,0,0]
	v_pk_fma_f32 v[26:27], v[26:27], v[80:81], 0 op_sel_hi:[0,1,0] neg_lo:[1,0,0] neg_hi:[1,0,0]
	v_cvt_pk_bf16_f32 v28, v28, v29
	v_cvt_pk_bf16_f32 v29, v26, v27
	ds_write_b64 v186, v[28:29] offset:1088
	ds_read_b32 v26, v187 offset:152
	s_waitcnt lgkmcnt(0)
	v_pk_fma_f32 v[28:29], v[26:27], v[66:67], 0 op_sel_hi:[0,1,0] neg_lo:[1,0,0] neg_hi:[1,0,0]
	v_pk_fma_f32 v[26:27], v[26:27], v[68:69], 0 op_sel_hi:[0,1,0] neg_lo:[1,0,0] neg_hi:[1,0,0]
	v_cvt_pk_bf16_f32 v28, v28, v29
	v_cvt_pk_bf16_f32 v29, v26, v27
	ds_write_b64 v186, v[28:29] offset:1632
	ds_read_b32 v26, v187 offset:160
	s_waitcnt lgkmcnt(0)
	v_pk_fma_f32 v[28:29], v[26:27], v[38:39], 0 op_sel_hi:[0,1,0] neg_lo:[1,0,0] neg_hi:[1,0,0]
	v_pk_fma_f32 v[26:27], v[26:27], v[40:41], 0 op_sel_hi:[0,1,0] neg_lo:[1,0,0] neg_hi:[1,0,0]
	v_cvt_pk_bf16_f32 v28, v28, v29
	v_cvt_pk_bf16_f32 v29, v26, v27
	ds_write_b64 v186, v[28:29] offset:2176
	ds_read_b32 v26, v187 offset:168
	s_waitcnt lgkmcnt(0)
	v_pk_fma_f32 v[18:19], v[26:27], v[18:19], 0 op_sel_hi:[0,1,0] neg_lo:[1,0,0] neg_hi:[1,0,0]
	v_pk_fma_f32 v[20:21], v[26:27], v[20:21], 0 op_sel_hi:[0,1,0] neg_lo:[1,0,0] neg_hi:[1,0,0]
	v_cvt_pk_bf16_f32 v18, v18, v19
	v_cvt_pk_bf16_f32 v19, v20, v21
	ds_write_b64 v186, v[18:19] offset:2720
	ds_read_b32 v18, v187 offset:176
	s_waitcnt lgkmcnt(0)
	v_pk_fma_f32 v[10:11], v[18:19], v[10:11], 0 op_sel_hi:[0,1,0] neg_lo:[1,0,0] neg_hi:[1,0,0]
	v_pk_fma_f32 v[12:13], v[18:19], v[12:13], 0 op_sel_hi:[0,1,0] neg_lo:[1,0,0] neg_hi:[1,0,0]
	v_cvt_pk_bf16_f32 v10, v10, v11
	v_cvt_pk_bf16_f32 v11, v12, v13
	ds_write_b64 v186, v[10:11] offset:3264
	ds_read_b32 v10, v187 offset:184
	s_waitcnt lgkmcnt(0)
	v_pk_fma_f32 v[2:3], v[10:11], v[2:3], 0 op_sel_hi:[0,1,0] neg_lo:[1,0,0] neg_hi:[1,0,0]
	v_pk_fma_f32 v[4:5], v[10:11], v[4:5], 0 op_sel_hi:[0,1,0] neg_lo:[1,0,0] neg_hi:[1,0,0]
	v_cvt_pk_bf16_f32 v2, v2, v3
	v_cvt_pk_bf16_f32 v3, v4, v5
	ds_write_b64 v186, v[2:3] offset:3808
	ds_read_b128 a[32:35], v1
	ds_read_b128 a[36:39], v1 offset:64
	ds_read_b128 a[40:43], v1 offset:128
	ds_read_b128 a[44:47], v1 offset:192
	v_lshl_add_u64 v[2:3], v[168:169], 0, s[28:29]
	v_lshl_add_u64 v[4:5], v[170:171], 0, s[28:29]
	v_lshl_add_u64 v[10:11], v[172:173], 0, s[28:29]
	v_lshl_add_u64 v[12:13], v[174:175], 0, s[28:29]
	v_lshl_add_u64 v[18:19], v[176:177], 0, s[28:29]
	v_lshl_add_u64 v[20:21], v[178:179], 0, s[28:29]
	v_lshl_add_u64 v[26:27], v[180:181], 0, s[28:29]
	v_lshl_add_u64 v[28:29], v[182:183], 0, s[28:29]
	global_load_dwordx4 v[106:109], v[2:3], off sc0 sc1 nt
	global_load_dwordx4 v[94:97], v[4:5], off sc0 sc1 nt
	global_load_dwordx4 v[66:69], v[10:11], off sc0 sc1 nt
	global_load_dwordx4 v[54:57], v[12:13], off sc0 sc1 nt
	global_load_dwordx4 v[38:41], v[18:19], off sc0 sc1 nt
	s_nop 0
	global_load_dwordx4 v[18:21], v[20:21], off sc0 sc1 nt
	s_nop 0
	global_load_dwordx4 v[10:13], v[26:27], off sc0 sc1 nt
	global_load_dwordx4 v[2:5], v[28:29], off sc0 sc1 nt
	v_mov_b32_e32 v26, v197
	s_waitcnt vmcnt(23)
	s_waitcnt vmcnt(22)
	s_waitcnt vmcnt(21)
	s_waitcnt vmcnt(20)
	s_waitcnt vmcnt(19)
	s_waitcnt vmcnt(18)
	s_waitcnt vmcnt(17)
	s_waitcnt vmcnt(16)
	ds_read_b32 v26, v187
	s_waitcnt lgkmcnt(0)
	v_pk_fma_f32 v[28:29], v[26:27], v[102:103], 0 op_sel_hi:[0,1,0] neg_lo:[1,0,0] neg_hi:[1,0,0]
	v_pk_fma_f32 v[26:27], v[26:27], v[104:105], 0 op_sel_hi:[0,1,0] neg_lo:[1,0,0] neg_hi:[1,0,0]
	v_cvt_pk_bf16_f32 v28, v28, v29
	v_cvt_pk_bf16_f32 v29, v26, v27
	ds_write_b64 v186, v[28:29]
	ds_read_b32 v26, v187 offset:8
	s_waitcnt lgkmcnt(0)
	v_pk_fma_f32 v[28:29], v[26:27], v[86:87], 0 op_sel_hi:[0,1,0] neg_lo:[1,0,0] neg_hi:[1,0,0]
	v_pk_fma_f32 v[26:27], v[26:27], v[88:89], 0 op_sel_hi:[0,1,0] neg_lo:[1,0,0] neg_hi:[1,0,0]
	v_cvt_pk_bf16_f32 v28, v28, v29
	v_cvt_pk_bf16_f32 v29, v26, v27
	ds_write_b64 v186, v[28:29] offset:544
	ds_read_b32 v26, v187 offset:16
	s_waitcnt lgkmcnt(0)
	v_pk_fma_f32 v[28:29], v[26:27], v[74:75], 0 op_sel_hi:[0,1,0] neg_lo:[1,0,0] neg_hi:[1,0,0]
	v_pk_fma_f32 v[26:27], v[26:27], v[76:77], 0 op_sel_hi:[0,1,0] neg_lo:[1,0,0] neg_hi:[1,0,0]
	v_cvt_pk_bf16_f32 v28, v28, v29
	v_cvt_pk_bf16_f32 v29, v26, v27
	ds_write_b64 v186, v[28:29] offset:1088
	ds_read_b32 v26, v187 offset:24
	s_waitcnt lgkmcnt(0)
	v_pk_fma_f32 v[28:29], v[26:27], v[62:63], 0 op_sel_hi:[0,1,0] neg_lo:[1,0,0] neg_hi:[1,0,0]
	v_pk_fma_f32 v[26:27], v[26:27], v[64:65], 0 op_sel_hi:[0,1,0] neg_lo:[1,0,0] neg_hi:[1,0,0]
	v_cvt_pk_bf16_f32 v28, v28, v29
	v_cvt_pk_bf16_f32 v29, v26, v27
	ds_write_b64 v186, v[28:29] offset:1632
	ds_read_b32 v26, v187 offset:32
	s_waitcnt lgkmcnt(0)
	v_pk_fma_f32 v[28:29], v[26:27], v[58:59], 0 op_sel_hi:[0,1,0] neg_lo:[1,0,0] neg_hi:[1,0,0]
	v_pk_fma_f32 v[26:27], v[26:27], v[60:61], 0 op_sel_hi:[0,1,0] neg_lo:[1,0,0] neg_hi:[1,0,0]
	v_cvt_pk_bf16_f32 v28, v28, v29
	v_cvt_pk_bf16_f32 v29, v26, v27
	ds_write_b64 v186, v[28:29] offset:2176
	ds_read_b32 v26, v187 offset:40
	s_waitcnt lgkmcnt(0)
	v_pk_fma_f32 v[28:29], v[26:27], v[46:47], 0 op_sel_hi:[0,1,0] neg_lo:[1,0,0] neg_hi:[1,0,0]
	v_pk_fma_f32 v[26:27], v[26:27], v[48:49], 0 op_sel_hi:[0,1,0] neg_lo:[1,0,0] neg_hi:[1,0,0]
	v_cvt_pk_bf16_f32 v28, v28, v29
	v_cvt_pk_bf16_f32 v29, v26, v27
	ds_write_b64 v186, v[28:29] offset:2720
	ds_read_b32 v26, v187 offset:48
	s_waitcnt lgkmcnt(0)
	v_pk_fma_f32 v[28:29], v[26:27], v[42:43], 0 op_sel_hi:[0,1,0] neg_lo:[1,0,0] neg_hi:[1,0,0]
	v_pk_fma_f32 v[26:27], v[26:27], v[44:45], 0 op_sel_hi:[0,1,0] neg_lo:[1,0,0] neg_hi:[1,0,0]
	v_cvt_pk_bf16_f32 v28, v28, v29
	v_cvt_pk_bf16_f32 v29, v26, v27
	ds_write_b64 v186, v[28:29] offset:3264
	ds_read_b32 v26, v187 offset:56
	s_waitcnt lgkmcnt(0)
	v_pk_fma_f32 v[28:29], v[26:27], v[30:31], 0 op_sel_hi:[0,1,0] neg_lo:[1,0,0] neg_hi:[1,0,0]
	v_pk_fma_f32 v[26:27], v[26:27], v[32:33], 0 op_sel_hi:[0,1,0] neg_lo:[1,0,0] neg_hi:[1,0,0]
	v_cvt_pk_bf16_f32 v28, v28, v29
	v_cvt_pk_bf16_f32 v29, v26, v27
	ds_write_b64 v186, v[28:29] offset:3808
	ds_read_b128 a[48:51], v1
	ds_read_b128 a[52:55], v1 offset:64
	ds_read_b128 a[56:59], v1 offset:128
	ds_read_b128 a[60:63], v1 offset:192
	v_lshl_add_u64 v[26:27], v[130:131], 0, s[26:27]
	v_add_co_u32_e32 v28, vcc, s7, v26
	s_nop 1
	v_addc_co_u32_e32 v29, vcc, 0, v27, vcc
	global_load_dwordx4 v[86:89], v[26:27], off sc0 sc1 nt
	global_load_dwordx4 v[82:85], v[28:29], off sc0 sc1 nt
	v_add_co_u32_e32 v28, vcc, s36, v26
	s_nop 1
	v_addc_co_u32_e32 v29, vcc, 0, v27, vcc
	v_add_co_u32_e32 v30, vcc, s37, v26
	s_nop 1
	v_addc_co_u32_e32 v31, vcc, 0, v27, vcc
	global_load_dwordx4 v[78:81], v[28:29], off sc0 sc1 nt
	global_load_dwordx4 v[58:61], v[30:31], off sc0 sc1 nt
	v_add_co_u32_e32 v28, vcc, s38, v26
	s_nop 1
	v_addc_co_u32_e32 v29, vcc, 0, v27, vcc
	v_add_co_u32_e32 v30, vcc, s39, v26
	s_nop 1
	v_addc_co_u32_e32 v31, vcc, 0, v27, vcc
	global_load_dwordx4 v[46:49], v[28:29], off sc0 sc1 nt
	global_load_dwordx4 v[42:45], v[30:31], off sc0 sc1 nt
	v_add_co_u32_e32 v28, vcc, s41, v26
	s_nop 1
	v_addc_co_u32_e32 v29, vcc, 0, v27, vcc
	v_add_co_u32_e32 v26, vcc, s42, v26
	s_nop 1
	v_addc_co_u32_e32 v27, vcc, 0, v27, vcc
	global_load_dwordx4 v[30:33], v[28:29], off sc0 sc1 nt
	s_nop 0
	global_load_dwordx4 v[26:29], v[26:27], off sc0 sc1 nt
	v_mov_b32_e32 v62, v197
	s_waitcnt vmcnt(23)
	s_waitcnt vmcnt(22)
	s_waitcnt vmcnt(21)
	s_waitcnt vmcnt(20)
	s_waitcnt vmcnt(19)
	s_waitcnt vmcnt(18)
	s_waitcnt vmcnt(17)
	s_waitcnt vmcnt(16)
	ds_read_b32 v62, v187 offset:64
	s_waitcnt lgkmcnt(0)
	v_pk_fma_f32 v[64:65], v[62:63], v[110:111], 0 op_sel_hi:[0,1,0] neg_lo:[1,0,0] neg_hi:[1,0,0]
	v_pk_fma_f32 v[62:63], v[62:63], v[112:113], 0 op_sel_hi:[0,1,0] neg_lo:[1,0,0] neg_hi:[1,0,0]
	v_cvt_pk_bf16_f32 v64, v64, v65
	v_cvt_pk_bf16_f32 v65, v62, v63
	ds_write_b64 v186, v[64:65]
	ds_read_b32 v62, v187 offset:72
	s_waitcnt lgkmcnt(0)
	v_pk_fma_f32 v[64:65], v[62:63], v[90:91], 0 op_sel_hi:[0,1,0] neg_lo:[1,0,0] neg_hi:[1,0,0]
	v_pk_fma_f32 v[62:63], v[62:63], v[92:93], 0 op_sel_hi:[0,1,0] neg_lo:[1,0,0] neg_hi:[1,0,0]
	v_cvt_pk_bf16_f32 v64, v64, v65
	v_cvt_pk_bf16_f32 v65, v62, v63
	ds_write_b64 v186, v[64:65] offset:544
	ds_read_b32 v62, v187 offset:80
	s_waitcnt lgkmcnt(0)
	v_pk_fma_f32 v[64:65], v[62:63], v[70:71], 0 op_sel_hi:[0,1,0] neg_lo:[1,0,0] neg_hi:[1,0,0]
	v_pk_fma_f32 v[62:63], v[62:63], v[72:73], 0 op_sel_hi:[0,1,0] neg_lo:[1,0,0] neg_hi:[1,0,0]
	v_cvt_pk_bf16_f32 v64, v64, v65
	v_cvt_pk_bf16_f32 v65, v62, v63
	ds_write_b64 v186, v[64:65] offset:1088
	ds_read_b32 v62, v187 offset:88
	s_waitcnt lgkmcnt(0)
	v_pk_fma_f32 v[50:51], v[62:63], v[50:51], 0 op_sel_hi:[0,1,0] neg_lo:[1,0,0] neg_hi:[1,0,0]
	v_pk_fma_f32 v[52:53], v[62:63], v[52:53], 0 op_sel_hi:[0,1,0] neg_lo:[1,0,0] neg_hi:[1,0,0]
	v_cvt_pk_bf16_f32 v50, v50, v51
	v_cvt_pk_bf16_f32 v51, v52, v53
	ds_write_b64 v186, v[50:51] offset:1632
	ds_read_b32 v50, v187 offset:96
	s_waitcnt lgkmcnt(0)
	v_pk_fma_f32 v[34:35], v[50:51], v[34:35], 0 op_sel_hi:[0,1,0] neg_lo:[1,0,0] neg_hi:[1,0,0]
	v_pk_fma_f32 v[36:37], v[50:51], v[36:37], 0 op_sel_hi:[0,1,0] neg_lo:[1,0,0] neg_hi:[1,0,0]
	v_cvt_pk_bf16_f32 v34, v34, v35
	v_cvt_pk_bf16_f32 v35, v36, v37
	ds_write_b64 v186, v[34:35] offset:2176
	ds_read_b32 v34, v187 offset:104
	s_waitcnt lgkmcnt(0)
	v_pk_fma_f32 v[22:23], v[34:35], v[22:23], 0 op_sel_hi:[0,1,0] neg_lo:[1,0,0] neg_hi:[1,0,0]
	v_pk_fma_f32 v[24:25], v[34:35], v[24:25], 0 op_sel_hi:[0,1,0] neg_lo:[1,0,0] neg_hi:[1,0,0]
	v_cvt_pk_bf16_f32 v22, v22, v23
	v_cvt_pk_bf16_f32 v23, v24, v25
	ds_write_b64 v186, v[22:23] offset:2720
	ds_read_b32 v22, v187 offset:112
	s_waitcnt lgkmcnt(0)
	v_pk_fma_f32 v[14:15], v[22:23], v[14:15], 0 op_sel_hi:[0,1,0] neg_lo:[1,0,0] neg_hi:[1,0,0]
	v_pk_fma_f32 v[16:17], v[22:23], v[16:17], 0 op_sel_hi:[0,1,0] neg_lo:[1,0,0] neg_hi:[1,0,0]
	v_cvt_pk_bf16_f32 v14, v14, v15
	v_cvt_pk_bf16_f32 v15, v16, v17
	ds_write_b64 v186, v[14:15] offset:3264
	ds_read_b32 v14, v187 offset:120
	s_waitcnt lgkmcnt(0)
	v_pk_fma_f32 v[6:7], v[14:15], v[6:7], 0 op_sel_hi:[0,1,0] neg_lo:[1,0,0] neg_hi:[1,0,0]
	v_pk_fma_f32 v[8:9], v[14:15], v[8:9], 0 op_sel_hi:[0,1,0] neg_lo:[1,0,0] neg_hi:[1,0,0]
	v_cvt_pk_bf16_f32 v6, v6, v7
	v_cvt_pk_bf16_f32 v7, v8, v9
	ds_write_b64 v186, v[6:7] offset:3808
	ds_read_b128 a[64:67], v1
	ds_read_b128 a[68:71], v1 offset:64
	ds_read_b128 a[72:75], v1 offset:128
	ds_read_b128 a[76:79], v1 offset:192
	v_lshl_add_u64 v[6:7], v[150:151], 0, s[26:27]
	v_lshl_add_u64 v[8:9], v[152:153], 0, s[26:27]
	v_lshl_add_u64 v[14:15], v[156:157], 0, s[26:27]
	v_lshl_add_u64 v[16:17], v[158:159], 0, s[26:27]
	v_lshl_add_u64 v[22:23], v[160:161], 0, s[26:27]
	v_lshl_add_u64 v[24:25], v[162:163], 0, s[26:27]
	v_lshl_add_u64 v[70:71], v[164:165], 0, s[26:27]
	v_lshl_add_u64 v[72:73], v[166:167], 0, s[26:27]
	global_load_dwordx4 v[110:113], v[6:7], off sc0 sc1 nt
	global_load_dwordx4 v[98:101], v[8:9], off sc0 sc1 nt
	global_load_dwordx4 v[62:65], v[14:15], off sc0 sc1 nt
	global_load_dwordx4 v[50:53], v[16:17], off sc0 sc1 nt
	global_load_dwordx4 v[34:37], v[22:23], off sc0 sc1 nt
	s_nop 0
	global_load_dwordx4 v[22:25], v[24:25], off sc0 sc1 nt
	s_nop 0
	global_load_dwordx4 v[14:17], v[70:71], off sc0 sc1 nt
	global_load_dwordx4 v[6:9], v[72:73], off sc0 sc1 nt
	s_waitcnt vmcnt(23)
	s_waitcnt vmcnt(22)
	s_waitcnt vmcnt(21)
	s_waitcnt vmcnt(20)
	s_waitcnt vmcnt(19)
	s_waitcnt vmcnt(18)
	s_waitcnt vmcnt(17)
	s_waitcnt vmcnt(16)
	ds_read_b32 v70, v187 offset:128
	s_waitcnt lgkmcnt(0)
	v_pk_fma_f32 v[72:73], v[70:71], v[106:107], 0 op_sel_hi:[0,1,0] neg_lo:[1,0,0] neg_hi:[1,0,0]
	v_pk_fma_f32 v[70:71], v[70:71], v[108:109], 0 op_sel_hi:[0,1,0] neg_lo:[1,0,0] neg_hi:[1,0,0]
	v_cvt_pk_bf16_f32 v72, v72, v73
	v_cvt_pk_bf16_f32 v73, v70, v71
	ds_write_b64 v186, v[72:73]
	ds_read_b32 v70, v187 offset:136
	s_waitcnt lgkmcnt(0)
	v_pk_fma_f32 v[72:73], v[70:71], v[94:95], 0 op_sel_hi:[0,1,0] neg_lo:[1,0,0] neg_hi:[1,0,0]
	v_pk_fma_f32 v[70:71], v[70:71], v[96:97], 0 op_sel_hi:[0,1,0] neg_lo:[1,0,0] neg_hi:[1,0,0]
	v_cvt_pk_bf16_f32 v72, v72, v73
	v_cvt_pk_bf16_f32 v73, v70, v71
	ds_write_b64 v186, v[72:73] offset:544
	ds_read_b32 v70, v187 offset:144
	s_waitcnt lgkmcnt(0)
	v_pk_fma_f32 v[66:67], v[70:71], v[66:67], 0 op_sel_hi:[0,1,0] neg_lo:[1,0,0] neg_hi:[1,0,0]
	v_pk_fma_f32 v[68:69], v[70:71], v[68:69], 0 op_sel_hi:[0,1,0] neg_lo:[1,0,0] neg_hi:[1,0,0]
	v_cvt_pk_bf16_f32 v66, v66, v67
	v_cvt_pk_bf16_f32 v67, v68, v69
	ds_write_b64 v186, v[66:67] offset:1088
	ds_read_b32 v66, v187 offset:152
	s_waitcnt lgkmcnt(0)
	v_pk_fma_f32 v[54:55], v[66:67], v[54:55], 0 op_sel_hi:[0,1,0] neg_lo:[1,0,0] neg_hi:[1,0,0]
	v_pk_fma_f32 v[56:57], v[66:67], v[56:57], 0 op_sel_hi:[0,1,0] neg_lo:[1,0,0] neg_hi:[1,0,0]
	v_cvt_pk_bf16_f32 v54, v54, v55
	v_cvt_pk_bf16_f32 v55, v56, v57
	ds_write_b64 v186, v[54:55] offset:1632
	ds_read_b32 v54, v187 offset:160
	s_waitcnt lgkmcnt(0)
	v_pk_fma_f32 v[38:39], v[54:55], v[38:39], 0 op_sel_hi:[0,1,0] neg_lo:[1,0,0] neg_hi:[1,0,0]
	v_pk_fma_f32 v[40:41], v[54:55], v[40:41], 0 op_sel_hi:[0,1,0] neg_lo:[1,0,0] neg_hi:[1,0,0]
	v_cvt_pk_bf16_f32 v38, v38, v39
	v_cvt_pk_bf16_f32 v39, v40, v41
	ds_write_b64 v186, v[38:39] offset:2176
	ds_read_b32 v38, v187 offset:168
	s_waitcnt lgkmcnt(0)
	v_pk_fma_f32 v[18:19], v[38:39], v[18:19], 0 op_sel_hi:[0,1,0] neg_lo:[1,0,0] neg_hi:[1,0,0]
	v_pk_fma_f32 v[20:21], v[38:39], v[20:21], 0 op_sel_hi:[0,1,0] neg_lo:[1,0,0] neg_hi:[1,0,0]
	v_cvt_pk_bf16_f32 v18, v18, v19
	v_cvt_pk_bf16_f32 v19, v20, v21
	ds_write_b64 v186, v[18:19] offset:2720
	ds_read_b32 v18, v187 offset:176
	s_waitcnt lgkmcnt(0)
	v_pk_fma_f32 v[10:11], v[18:19], v[10:11], 0 op_sel_hi:[0,1,0] neg_lo:[1,0,0] neg_hi:[1,0,0]
	v_pk_fma_f32 v[12:13], v[18:19], v[12:13], 0 op_sel_hi:[0,1,0] neg_lo:[1,0,0] neg_hi:[1,0,0]
	v_cvt_pk_bf16_f32 v10, v10, v11
	v_cvt_pk_bf16_f32 v11, v12, v13
	ds_write_b64 v186, v[10:11] offset:3264
	ds_read_b32 v10, v187 offset:184
	s_waitcnt lgkmcnt(0)
	v_pk_fma_f32 v[2:3], v[10:11], v[2:3], 0 op_sel_hi:[0,1,0] neg_lo:[1,0,0] neg_hi:[1,0,0]
	v_pk_fma_f32 v[4:5], v[10:11], v[4:5], 0 op_sel_hi:[0,1,0] neg_lo:[1,0,0] neg_hi:[1,0,0]
	v_cvt_pk_bf16_f32 v2, v2, v3
	v_cvt_pk_bf16_f32 v3, v4, v5
	ds_write_b64 v186, v[2:3] offset:3808
	ds_read_b128 a[80:83], v1
	ds_read_b128 a[84:87], v1 offset:64
	ds_read_b128 a[88:91], v1 offset:128
	ds_read_b128 a[92:95], v1 offset:192
	v_lshl_add_u64 v[2:3], v[168:169], 0, s[26:27]
	v_lshl_add_u64 v[4:5], v[170:171], 0, s[26:27]
	v_lshl_add_u64 v[10:11], v[172:173], 0, s[26:27]
	v_lshl_add_u64 v[12:13], v[174:175], 0, s[26:27]
	v_lshl_add_u64 v[18:19], v[176:177], 0, s[26:27]
	v_lshl_add_u64 v[20:21], v[178:179], 0, s[26:27]
	v_lshl_add_u64 v[66:67], v[180:181], 0, s[26:27]
	v_lshl_add_u64 v[68:69], v[182:183], 0, s[26:27]
	global_load_dwordx4 v[106:109], v[2:3], off sc0 sc1 nt
	global_load_dwordx4 v[94:97], v[4:5], off sc0 sc1 nt
	global_load_dwordx4 v[74:77], v[10:11], off sc0 sc1 nt
	global_load_dwordx4 v[54:57], v[12:13], off sc0 sc1 nt
	global_load_dwordx4 v[38:41], v[18:19], off sc0 sc1 nt
	s_nop 0
	global_load_dwordx4 v[18:21], v[20:21], off sc0 sc1 nt
	s_nop 0
	global_load_dwordx4 v[10:13], v[66:67], off sc0 sc1 nt
	global_load_dwordx4 v[2:5], v[68:69], off sc0 sc1 nt
	v_mov_b32_e32 v66, v196
	s_waitcnt vmcnt(23)
	s_waitcnt vmcnt(22)
	s_waitcnt vmcnt(21)
	s_waitcnt vmcnt(20)
	s_waitcnt vmcnt(19)
	s_waitcnt vmcnt(18)
	s_waitcnt vmcnt(17)
	s_waitcnt vmcnt(16)
	ds_read_b32 v66, v187
	s_waitcnt lgkmcnt(0)
	v_pk_fma_f32 v[68:69], v[66:67], v[86:87], 0 op_sel_hi:[0,1,0] neg_lo:[1,0,0] neg_hi:[1,0,0]
	v_pk_fma_f32 v[66:67], v[66:67], v[88:89], 0 op_sel_hi:[0,1,0] neg_lo:[1,0,0] neg_hi:[1,0,0]
	v_cvt_pk_bf16_f32 v68, v68, v69
	v_cvt_pk_bf16_f32 v69, v66, v67
	ds_write_b64 v186, v[68:69]
	ds_read_b32 v66, v187 offset:8
	s_waitcnt lgkmcnt(0)
	v_pk_fma_f32 v[68:69], v[66:67], v[82:83], 0 op_sel_hi:[0,1,0] neg_lo:[1,0,0] neg_hi:[1,0,0]
	v_pk_fma_f32 v[66:67], v[66:67], v[84:85], 0 op_sel_hi:[0,1,0] neg_lo:[1,0,0] neg_hi:[1,0,0]
	v_cvt_pk_bf16_f32 v68, v68, v69
	v_cvt_pk_bf16_f32 v69, v66, v67
	ds_write_b64 v186, v[68:69] offset:544
	ds_read_b32 v66, v187 offset:16
	s_waitcnt lgkmcnt(0)
	v_pk_fma_f32 v[68:69], v[66:67], v[78:79], 0 op_sel_hi:[0,1,0] neg_lo:[1,0,0] neg_hi:[1,0,0]
	v_pk_fma_f32 v[66:67], v[66:67], v[80:81], 0 op_sel_hi:[0,1,0] neg_lo:[1,0,0] neg_hi:[1,0,0]
	v_cvt_pk_bf16_f32 v68, v68, v69
	v_cvt_pk_bf16_f32 v69, v66, v67
	ds_write_b64 v186, v[68:69] offset:1088
	ds_read_b32 v66, v187 offset:24
	s_waitcnt lgkmcnt(0)
	v_pk_fma_f32 v[58:59], v[66:67], v[58:59], 0 op_sel_hi:[0,1,0] neg_lo:[1,0,0] neg_hi:[1,0,0]
	v_pk_fma_f32 v[60:61], v[66:67], v[60:61], 0 op_sel_hi:[0,1,0] neg_lo:[1,0,0] neg_hi:[1,0,0]
	v_cvt_pk_bf16_f32 v58, v58, v59
	v_cvt_pk_bf16_f32 v59, v60, v61
	ds_write_b64 v186, v[58:59] offset:1632
	ds_read_b32 v58, v187 offset:32
	s_waitcnt lgkmcnt(0)
	v_pk_fma_f32 v[46:47], v[58:59], v[46:47], 0 op_sel_hi:[0,1,0] neg_lo:[1,0,0] neg_hi:[1,0,0]
	v_pk_fma_f32 v[48:49], v[58:59], v[48:49], 0 op_sel_hi:[0,1,0] neg_lo:[1,0,0] neg_hi:[1,0,0]
	v_cvt_pk_bf16_f32 v46, v46, v47
	v_cvt_pk_bf16_f32 v47, v48, v49
	ds_write_b64 v186, v[46:47] offset:2176
	ds_read_b32 v46, v187 offset:40
	s_waitcnt lgkmcnt(0)
	v_pk_fma_f32 v[42:43], v[46:47], v[42:43], 0 op_sel_hi:[0,1,0] neg_lo:[1,0,0] neg_hi:[1,0,0]
	v_pk_fma_f32 v[44:45], v[46:47], v[44:45], 0 op_sel_hi:[0,1,0] neg_lo:[1,0,0] neg_hi:[1,0,0]
	v_cvt_pk_bf16_f32 v42, v42, v43
	v_cvt_pk_bf16_f32 v43, v44, v45
	ds_write_b64 v186, v[42:43] offset:2720
	ds_read_b32 v42, v187 offset:48
	s_waitcnt lgkmcnt(0)
	v_pk_fma_f32 v[30:31], v[42:43], v[30:31], 0 op_sel_hi:[0,1,0] neg_lo:[1,0,0] neg_hi:[1,0,0]
	v_pk_fma_f32 v[32:33], v[42:43], v[32:33], 0 op_sel_hi:[0,1,0] neg_lo:[1,0,0] neg_hi:[1,0,0]
	v_cvt_pk_bf16_f32 v30, v30, v31
	v_cvt_pk_bf16_f32 v31, v32, v33
	ds_write_b64 v186, v[30:31] offset:3264
	ds_read_b32 v30, v187 offset:56
	s_waitcnt lgkmcnt(0)
	v_pk_fma_f32 v[26:27], v[30:31], v[26:27], 0 op_sel_hi:[0,1,0] neg_lo:[1,0,0] neg_hi:[1,0,0]
	v_pk_fma_f32 v[28:29], v[30:31], v[28:29], 0 op_sel_hi:[0,1,0] neg_lo:[1,0,0] neg_hi:[1,0,0]
	v_cvt_pk_bf16_f32 v26, v26, v27
	v_cvt_pk_bf16_f32 v27, v28, v29
	ds_write_b64 v186, v[26:27] offset:3808
	ds_read_b128 a[96:99], v1
	ds_read_b128 a[100:103], v1 offset:64
	ds_read_b128 a[104:107], v1 offset:128
	ds_read_b128 a[108:111], v1 offset:192
	v_lshl_add_u64 v[26:27], v[130:131], 0, s[24:25]
	v_add_co_u32_e32 v28, vcc, s7, v26
	s_nop 1
	v_addc_co_u32_e32 v29, vcc, 0, v27, vcc
	global_load_dwordx4 v[102:105], v[26:27], off sc0 sc1 nt
	global_load_dwordx4 v[90:93], v[28:29], off sc0 sc1 nt
	v_add_co_u32_e32 v28, vcc, s36, v26
	s_nop 1
	v_addc_co_u32_e32 v29, vcc, 0, v27, vcc
	v_add_co_u32_e32 v30, vcc, s37, v26
	s_nop 1
	v_addc_co_u32_e32 v31, vcc, 0, v27, vcc
	global_load_dwordx4 v[86:89], v[28:29], off sc0 sc1 nt
	global_load_dwordx4 v[70:73], v[30:31], off sc0 sc1 nt
	v_add_co_u32_e32 v28, vcc, s38, v26
	s_nop 1
	v_addc_co_u32_e32 v29, vcc, 0, v27, vcc
	v_add_co_u32_e32 v30, vcc, s39, v26
	s_nop 1
	v_addc_co_u32_e32 v31, vcc, 0, v27, vcc
	global_load_dwordx4 v[66:69], v[28:29], off sc0 sc1 nt
	global_load_dwordx4 v[46:49], v[30:31], off sc0 sc1 nt
	v_add_co_u32_e32 v28, vcc, s41, v26
	s_nop 1
	v_addc_co_u32_e32 v29, vcc, 0, v27, vcc
	v_add_co_u32_e32 v26, vcc, s42, v26
	s_nop 1
	v_addc_co_u32_e32 v27, vcc, 0, v27, vcc
	global_load_dwordx4 v[42:45], v[28:29], off sc0 sc1 nt
	global_load_dwordx4 v[30:33], v[26:27], off sc0 sc1 nt
	v_mov_b32_e32 v26, v196
	s_waitcnt vmcnt(23)
	s_waitcnt vmcnt(22)
	s_waitcnt vmcnt(21)
	s_waitcnt vmcnt(20)
	s_waitcnt vmcnt(19)
	s_waitcnt vmcnt(18)
	s_waitcnt vmcnt(17)
	s_waitcnt vmcnt(16)
	ds_read_b32 v26, v187 offset:64
	s_waitcnt lgkmcnt(0)
	v_pk_fma_f32 v[28:29], v[26:27], v[110:111], 0 op_sel_hi:[0,1,0] neg_lo:[1,0,0] neg_hi:[1,0,0]
	v_pk_fma_f32 v[26:27], v[26:27], v[112:113], 0 op_sel_hi:[0,1,0] neg_lo:[1,0,0] neg_hi:[1,0,0]
	v_cvt_pk_bf16_f32 v28, v28, v29
	v_cvt_pk_bf16_f32 v29, v26, v27
	ds_write_b64 v186, v[28:29]
	ds_read_b32 v26, v187 offset:72
	s_waitcnt lgkmcnt(0)
	v_pk_fma_f32 v[28:29], v[26:27], v[98:99], 0 op_sel_hi:[0,1,0] neg_lo:[1,0,0] neg_hi:[1,0,0]
	v_pk_fma_f32 v[26:27], v[26:27], v[100:101], 0 op_sel_hi:[0,1,0] neg_lo:[1,0,0] neg_hi:[1,0,0]
	v_cvt_pk_bf16_f32 v28, v28, v29
	v_cvt_pk_bf16_f32 v29, v26, v27
	ds_write_b64 v186, v[28:29] offset:544
	ds_read_b32 v26, v187 offset:80
	s_waitcnt lgkmcnt(0)
	v_pk_fma_f32 v[28:29], v[26:27], v[62:63], 0 op_sel_hi:[0,1,0] neg_lo:[1,0,0] neg_hi:[1,0,0]
	v_pk_fma_f32 v[26:27], v[26:27], v[64:65], 0 op_sel_hi:[0,1,0] neg_lo:[1,0,0] neg_hi:[1,0,0]
	v_cvt_pk_bf16_f32 v28, v28, v29
	v_cvt_pk_bf16_f32 v29, v26, v27
	ds_write_b64 v186, v[28:29] offset:1088
	ds_read_b32 v26, v187 offset:88
	s_waitcnt lgkmcnt(0)
	v_pk_fma_f32 v[28:29], v[26:27], v[50:51], 0 op_sel_hi:[0,1,0] neg_lo:[1,0,0] neg_hi:[1,0,0]
	v_pk_fma_f32 v[26:27], v[26:27], v[52:53], 0 op_sel_hi:[0,1,0] neg_lo:[1,0,0] neg_hi:[1,0,0]
	v_cvt_pk_bf16_f32 v28, v28, v29
	v_cvt_pk_bf16_f32 v29, v26, v27
	ds_write_b64 v186, v[28:29] offset:1632
	ds_read_b32 v26, v187 offset:96
	s_waitcnt lgkmcnt(0)
	v_pk_fma_f32 v[28:29], v[26:27], v[34:35], 0 op_sel_hi:[0,1,0] neg_lo:[1,0,0] neg_hi:[1,0,0]
	v_pk_fma_f32 v[26:27], v[26:27], v[36:37], 0 op_sel_hi:[0,1,0] neg_lo:[1,0,0] neg_hi:[1,0,0]
	v_cvt_pk_bf16_f32 v28, v28, v29
	v_cvt_pk_bf16_f32 v29, v26, v27
	ds_write_b64 v186, v[28:29] offset:2176
	ds_read_b32 v26, v187 offset:104
	s_waitcnt lgkmcnt(0)
	v_pk_fma_f32 v[22:23], v[26:27], v[22:23], 0 op_sel_hi:[0,1,0] neg_lo:[1,0,0] neg_hi:[1,0,0]
	v_pk_fma_f32 v[24:25], v[26:27], v[24:25], 0 op_sel_hi:[0,1,0] neg_lo:[1,0,0] neg_hi:[1,0,0]
	v_cvt_pk_bf16_f32 v22, v22, v23
	v_cvt_pk_bf16_f32 v23, v24, v25
	ds_write_b64 v186, v[22:23] offset:2720
	ds_read_b32 v22, v187 offset:112
	s_waitcnt lgkmcnt(0)
	v_pk_fma_f32 v[14:15], v[22:23], v[14:15], 0 op_sel_hi:[0,1,0] neg_lo:[1,0,0] neg_hi:[1,0,0]
	v_pk_fma_f32 v[16:17], v[22:23], v[16:17], 0 op_sel_hi:[0,1,0] neg_lo:[1,0,0] neg_hi:[1,0,0]
	v_cvt_pk_bf16_f32 v14, v14, v15
	v_cvt_pk_bf16_f32 v15, v16, v17
	ds_write_b64 v186, v[14:15] offset:3264
	ds_read_b32 v14, v187 offset:120
	s_waitcnt lgkmcnt(0)
	v_pk_fma_f32 v[6:7], v[14:15], v[6:7], 0 op_sel_hi:[0,1,0] neg_lo:[1,0,0] neg_hi:[1,0,0]
	v_pk_fma_f32 v[8:9], v[14:15], v[8:9], 0 op_sel_hi:[0,1,0] neg_lo:[1,0,0] neg_hi:[1,0,0]
	v_cvt_pk_bf16_f32 v6, v6, v7
	v_cvt_pk_bf16_f32 v7, v8, v9
	ds_write_b64 v186, v[6:7] offset:3808
	ds_read_b128 a[112:115], v1
	ds_read_b128 a[116:119], v1 offset:64
	ds_read_b128 a[120:123], v1 offset:128
	ds_read_b128 a[124:127], v1 offset:192
	v_lshl_add_u64 v[6:7], v[150:151], 0, s[24:25]
	v_lshl_add_u64 v[8:9], v[152:153], 0, s[24:25]
	v_lshl_add_u64 v[14:15], v[156:157], 0, s[24:25]
	v_lshl_add_u64 v[16:17], v[158:159], 0, s[24:25]
	v_lshl_add_u64 v[22:23], v[160:161], 0, s[24:25]
	v_lshl_add_u64 v[24:25], v[162:163], 0, s[24:25]
	v_lshl_add_u64 v[26:27], v[164:165], 0, s[24:25]
	v_lshl_add_u64 v[28:29], v[166:167], 0, s[24:25]
	global_load_dwordx4 v[110:113], v[6:7], off sc0 sc1 nt
	global_load_dwordx4 v[98:101], v[8:9], off sc0 sc1 nt
	global_load_dwordx4 v[78:81], v[14:15], off sc0 sc1 nt
	global_load_dwordx4 v[58:61], v[16:17], off sc0 sc1 nt
	global_load_dwordx4 v[34:37], v[22:23], off sc0 sc1 nt
	s_nop 0
	global_load_dwordx4 v[22:25], v[24:25], off sc0 sc1 nt
	s_nop 0
	global_load_dwordx4 v[14:17], v[26:27], off sc0 sc1 nt
	global_load_dwordx4 v[6:9], v[28:29], off sc0 sc1 nt
	s_waitcnt vmcnt(23)
	s_waitcnt vmcnt(22)
	s_waitcnt vmcnt(21)
	s_waitcnt vmcnt(20)
	s_waitcnt vmcnt(19)
	s_waitcnt vmcnt(18)
	s_waitcnt vmcnt(17)
	s_waitcnt vmcnt(16)
	ds_read_b32 v26, v187 offset:128
	s_waitcnt lgkmcnt(0)
	v_pk_fma_f32 v[28:29], v[26:27], v[106:107], 0 op_sel_hi:[0,1,0] neg_lo:[1,0,0] neg_hi:[1,0,0]
	v_pk_fma_f32 v[26:27], v[26:27], v[108:109], 0 op_sel_hi:[0,1,0] neg_lo:[1,0,0] neg_hi:[1,0,0]
	v_cvt_pk_bf16_f32 v28, v28, v29
	v_cvt_pk_bf16_f32 v29, v26, v27
	ds_write_b64 v186, v[28:29]
	ds_read_b32 v26, v187 offset:136
	s_waitcnt lgkmcnt(0)
	v_pk_fma_f32 v[28:29], v[26:27], v[94:95], 0 op_sel_hi:[0,1,0] neg_lo:[1,0,0] neg_hi:[1,0,0]
	v_pk_fma_f32 v[26:27], v[26:27], v[96:97], 0 op_sel_hi:[0,1,0] neg_lo:[1,0,0] neg_hi:[1,0,0]
	v_cvt_pk_bf16_f32 v28, v28, v29
	v_cvt_pk_bf16_f32 v29, v26, v27
	ds_write_b64 v186, v[28:29] offset:544
	ds_read_b32 v26, v187 offset:144
	s_waitcnt lgkmcnt(0)
	v_pk_fma_f32 v[28:29], v[26:27], v[74:75], 0 op_sel_hi:[0,1,0] neg_lo:[1,0,0] neg_hi:[1,0,0]
	v_pk_fma_f32 v[26:27], v[26:27], v[76:77], 0 op_sel_hi:[0,1,0] neg_lo:[1,0,0] neg_hi:[1,0,0]
	v_cvt_pk_bf16_f32 v28, v28, v29
	v_cvt_pk_bf16_f32 v29, v26, v27
	ds_write_b64 v186, v[28:29] offset:1088
	ds_read_b32 v26, v187 offset:152
	s_waitcnt lgkmcnt(0)
	v_pk_fma_f32 v[28:29], v[26:27], v[54:55], 0 op_sel_hi:[0,1,0] neg_lo:[1,0,0] neg_hi:[1,0,0]
	v_pk_fma_f32 v[26:27], v[26:27], v[56:57], 0 op_sel_hi:[0,1,0] neg_lo:[1,0,0] neg_hi:[1,0,0]
	v_cvt_pk_bf16_f32 v28, v28, v29
	v_cvt_pk_bf16_f32 v29, v26, v27
	ds_write_b64 v186, v[28:29] offset:1632
	ds_read_b32 v26, v187 offset:160
	s_waitcnt lgkmcnt(0)
	v_pk_fma_f32 v[28:29], v[26:27], v[38:39], 0 op_sel_hi:[0,1,0] neg_lo:[1,0,0] neg_hi:[1,0,0]
	v_pk_fma_f32 v[26:27], v[26:27], v[40:41], 0 op_sel_hi:[0,1,0] neg_lo:[1,0,0] neg_hi:[1,0,0]
	v_cvt_pk_bf16_f32 v28, v28, v29
	v_cvt_pk_bf16_f32 v29, v26, v27
	ds_write_b64 v186, v[28:29] offset:2176
	ds_read_b32 v26, v187 offset:168
	s_waitcnt lgkmcnt(0)
	v_pk_fma_f32 v[18:19], v[26:27], v[18:19], 0 op_sel_hi:[0,1,0] neg_lo:[1,0,0] neg_hi:[1,0,0]
	v_pk_fma_f32 v[20:21], v[26:27], v[20:21], 0 op_sel_hi:[0,1,0] neg_lo:[1,0,0] neg_hi:[1,0,0]
	v_cvt_pk_bf16_f32 v18, v18, v19
	v_cvt_pk_bf16_f32 v19, v20, v21
	ds_write_b64 v186, v[18:19] offset:2720
	ds_read_b32 v18, v187 offset:176
	s_waitcnt lgkmcnt(0)
	v_pk_fma_f32 v[10:11], v[18:19], v[10:11], 0 op_sel_hi:[0,1,0] neg_lo:[1,0,0] neg_hi:[1,0,0]
	v_pk_fma_f32 v[12:13], v[18:19], v[12:13], 0 op_sel_hi:[0,1,0] neg_lo:[1,0,0] neg_hi:[1,0,0]
	v_cvt_pk_bf16_f32 v10, v10, v11
	v_cvt_pk_bf16_f32 v11, v12, v13
	ds_write_b64 v186, v[10:11] offset:3264
	ds_read_b32 v10, v187 offset:184
	s_waitcnt lgkmcnt(0)
	v_pk_fma_f32 v[2:3], v[10:11], v[2:3], 0 op_sel_hi:[0,1,0] neg_lo:[1,0,0] neg_hi:[1,0,0]
	v_pk_fma_f32 v[4:5], v[10:11], v[4:5], 0 op_sel_hi:[0,1,0] neg_lo:[1,0,0] neg_hi:[1,0,0]
	v_cvt_pk_bf16_f32 v2, v2, v3
	v_cvt_pk_bf16_f32 v3, v4, v5
	ds_write_b64 v186, v[2:3] offset:3808
	ds_read_b128 a[128:131], v1
	ds_read_b128 a[132:135], v1 offset:64
	ds_read_b128 a[136:139], v1 offset:128
	ds_read_b128 a[140:143], v1 offset:192
	v_lshl_add_u64 v[2:3], v[168:169], 0, s[24:25]
	v_lshl_add_u64 v[4:5], v[170:171], 0, s[24:25]
	v_lshl_add_u64 v[10:11], v[172:173], 0, s[24:25]
	v_lshl_add_u64 v[12:13], v[174:175], 0, s[24:25]
	v_lshl_add_u64 v[18:19], v[176:177], 0, s[24:25]
	v_lshl_add_u64 v[20:21], v[178:179], 0, s[24:25]
	v_lshl_add_u64 v[50:51], v[180:181], 0, s[24:25]
	v_lshl_add_u64 v[52:53], v[182:183], 0, s[24:25]
	global_load_dwordx4 v[114:117], v[2:3], off sc0 sc1 nt
	global_load_dwordx4 v[94:97], v[4:5], off sc0 sc1 nt
	global_load_dwordx4 v[82:85], v[10:11], off sc0 sc1 nt
	global_load_dwordx4 v[62:65], v[12:13], off sc0 sc1 nt
	global_load_dwordx4 v[38:41], v[18:19], off sc0 sc1 nt
	global_load_dwordx4 v[26:29], v[20:21], off sc0 sc1 nt
	s_nop 0
	global_load_dwordx4 v[10:13], v[50:51], off sc0 sc1 nt
	global_load_dwordx4 v[2:5], v[52:53], off sc0 sc1 nt
	v_mov_b32_e32 v18, v195
	s_waitcnt vmcnt(23)
	s_waitcnt vmcnt(22)
	s_waitcnt vmcnt(21)
	s_waitcnt vmcnt(20)
	s_waitcnt vmcnt(19)
	s_waitcnt vmcnt(18)
	s_waitcnt vmcnt(17)
	s_waitcnt vmcnt(16)
	ds_read_b32 v18, v187
	s_waitcnt lgkmcnt(0)
	v_pk_fma_f32 v[20:21], v[18:19], v[102:103], 0 op_sel_hi:[0,1,0] neg_lo:[1,0,0] neg_hi:[1,0,0]
	v_pk_fma_f32 v[18:19], v[18:19], v[104:105], 0 op_sel_hi:[0,1,0] neg_lo:[1,0,0] neg_hi:[1,0,0]
	v_cvt_pk_bf16_f32 v20, v20, v21
	v_cvt_pk_bf16_f32 v21, v18, v19
	ds_write_b64 v186, v[20:21]
	ds_read_b32 v18, v187 offset:8
	s_waitcnt lgkmcnt(0)
	v_pk_fma_f32 v[20:21], v[18:19], v[90:91], 0 op_sel_hi:[0,1,0] neg_lo:[1,0,0] neg_hi:[1,0,0]
	v_pk_fma_f32 v[18:19], v[18:19], v[92:93], 0 op_sel_hi:[0,1,0] neg_lo:[1,0,0] neg_hi:[1,0,0]
	v_cvt_pk_bf16_f32 v20, v20, v21
	v_cvt_pk_bf16_f32 v21, v18, v19
	ds_write_b64 v186, v[20:21] offset:544
	ds_read_b32 v18, v187 offset:16
	s_waitcnt lgkmcnt(0)
	v_pk_fma_f32 v[20:21], v[18:19], v[86:87], 0 op_sel_hi:[0,1,0] neg_lo:[1,0,0] neg_hi:[1,0,0]
	v_pk_fma_f32 v[18:19], v[18:19], v[88:89], 0 op_sel_hi:[0,1,0] neg_lo:[1,0,0] neg_hi:[1,0,0]
	v_cvt_pk_bf16_f32 v20, v20, v21
	v_cvt_pk_bf16_f32 v21, v18, v19
	ds_write_b64 v186, v[20:21] offset:1088
	ds_read_b32 v18, v187 offset:24
	s_waitcnt lgkmcnt(0)
	v_pk_fma_f32 v[20:21], v[18:19], v[70:71], 0 op_sel_hi:[0,1,0] neg_lo:[1,0,0] neg_hi:[1,0,0]
	v_pk_fma_f32 v[18:19], v[18:19], v[72:73], 0 op_sel_hi:[0,1,0] neg_lo:[1,0,0] neg_hi:[1,0,0]
	v_cvt_pk_bf16_f32 v20, v20, v21
	v_cvt_pk_bf16_f32 v21, v18, v19
	ds_write_b64 v186, v[20:21] offset:1632
	ds_read_b32 v18, v187 offset:32
	s_waitcnt lgkmcnt(0)
	v_pk_fma_f32 v[20:21], v[18:19], v[66:67], 0 op_sel_hi:[0,1,0] neg_lo:[1,0,0] neg_hi:[1,0,0]
	v_pk_fma_f32 v[18:19], v[18:19], v[68:69], 0 op_sel_hi:[0,1,0] neg_lo:[1,0,0] neg_hi:[1,0,0]
	v_cvt_pk_bf16_f32 v20, v20, v21
	v_cvt_pk_bf16_f32 v21, v18, v19
	ds_write_b64 v186, v[20:21] offset:2176
	ds_read_b32 v18, v187 offset:40
	s_waitcnt lgkmcnt(0)
	v_pk_fma_f32 v[20:21], v[18:19], v[46:47], 0 op_sel_hi:[0,1,0] neg_lo:[1,0,0] neg_hi:[1,0,0]
	v_pk_fma_f32 v[18:19], v[18:19], v[48:49], 0 op_sel_hi:[0,1,0] neg_lo:[1,0,0] neg_hi:[1,0,0]
	v_cvt_pk_bf16_f32 v20, v20, v21
	v_cvt_pk_bf16_f32 v21, v18, v19
	ds_write_b64 v186, v[20:21] offset:2720
	ds_read_b32 v18, v187 offset:48
	s_waitcnt lgkmcnt(0)
	v_pk_fma_f32 v[20:21], v[18:19], v[42:43], 0 op_sel_hi:[0,1,0] neg_lo:[1,0,0] neg_hi:[1,0,0]
	v_pk_fma_f32 v[18:19], v[18:19], v[44:45], 0 op_sel_hi:[0,1,0] neg_lo:[1,0,0] neg_hi:[1,0,0]
	v_cvt_pk_bf16_f32 v20, v20, v21
	v_cvt_pk_bf16_f32 v21, v18, v19
	ds_write_b64 v186, v[20:21] offset:3264
	ds_read_b32 v18, v187 offset:56
	s_waitcnt lgkmcnt(0)
	v_pk_fma_f32 v[20:21], v[18:19], v[30:31], 0 op_sel_hi:[0,1,0] neg_lo:[1,0,0] neg_hi:[1,0,0]
	v_pk_fma_f32 v[18:19], v[18:19], v[32:33], 0 op_sel_hi:[0,1,0] neg_lo:[1,0,0] neg_hi:[1,0,0]
	v_cvt_pk_bf16_f32 v20, v20, v21
	v_cvt_pk_bf16_f32 v21, v18, v19
	ds_write_b64 v186, v[20:21] offset:3808
	ds_read_b128 a[144:147], v1
	ds_read_b128 a[148:151], v1 offset:64
	ds_read_b128 a[152:155], v1 offset:128
	ds_read_b128 a[156:159], v1 offset:192
	v_lshl_add_u64 v[18:19], v[130:131], 0, s[22:23]
	v_add_co_u32_e32 v20, vcc, s7, v18
	s_nop 1
	v_addc_co_u32_e32 v21, vcc, 0, v19, vcc
	global_load_dwordx4 v[106:109], v[18:19], off sc0 sc1 nt
	global_load_dwordx4 v[90:93], v[20:21], off sc0 sc1 nt
	v_add_co_u32_e32 v20, vcc, s36, v18
	s_nop 1
	v_addc_co_u32_e32 v21, vcc, 0, v19, vcc
	v_add_co_u32_e32 v30, vcc, s37, v18
	s_nop 1
	v_addc_co_u32_e32 v31, vcc, 0, v19, vcc
	global_load_dwordx4 v[86:89], v[20:21], off sc0 sc1 nt
	global_load_dwordx4 v[74:77], v[30:31], off sc0 sc1 nt
	v_add_co_u32_e32 v20, vcc, s38, v18
	s_nop 1
	v_addc_co_u32_e32 v21, vcc, 0, v19, vcc
	v_add_co_u32_e32 v30, vcc, s39, v18
	s_nop 1
	v_addc_co_u32_e32 v31, vcc, 0, v19, vcc
	global_load_dwordx4 v[70:73], v[20:21], off sc0 sc1 nt
	global_load_dwordx4 v[54:57], v[30:31], off sc0 sc1 nt
	v_add_co_u32_e32 v20, vcc, s41, v18
	s_nop 1
	v_addc_co_u32_e32 v21, vcc, 0, v19, vcc
	v_add_co_u32_e32 v18, vcc, s42, v18
	s_nop 1
	v_addc_co_u32_e32 v19, vcc, 0, v19, vcc
	global_load_dwordx4 v[50:53], v[20:21], off sc0 sc1 nt
	global_load_dwordx4 v[46:49], v[18:19], off sc0 sc1 nt
	v_mov_b32_e32 v18, v195
	s_waitcnt vmcnt(23)
	s_waitcnt vmcnt(22)
	s_waitcnt vmcnt(21)
	s_waitcnt vmcnt(20)
	s_waitcnt vmcnt(19)
	s_waitcnt vmcnt(18)
	s_waitcnt vmcnt(17)
	s_waitcnt vmcnt(16)
	ds_read_b32 v18, v187 offset:64
	s_waitcnt lgkmcnt(0)
	v_pk_fma_f32 v[20:21], v[18:19], v[110:111], 0 op_sel_hi:[0,1,0] neg_lo:[1,0,0] neg_hi:[1,0,0]
	v_pk_fma_f32 v[18:19], v[18:19], v[112:113], 0 op_sel_hi:[0,1,0] neg_lo:[1,0,0] neg_hi:[1,0,0]
	v_cvt_pk_bf16_f32 v20, v20, v21
	v_cvt_pk_bf16_f32 v21, v18, v19
	ds_write_b64 v186, v[20:21]
	ds_read_b32 v18, v187 offset:72
	s_waitcnt lgkmcnt(0)
	v_pk_fma_f32 v[20:21], v[18:19], v[98:99], 0 op_sel_hi:[0,1,0] neg_lo:[1,0,0] neg_hi:[1,0,0]
	v_pk_fma_f32 v[18:19], v[18:19], v[100:101], 0 op_sel_hi:[0,1,0] neg_lo:[1,0,0] neg_hi:[1,0,0]
	v_cvt_pk_bf16_f32 v20, v20, v21
	v_cvt_pk_bf16_f32 v21, v18, v19
	ds_write_b64 v186, v[20:21] offset:544
	ds_read_b32 v18, v187 offset:80
	s_waitcnt lgkmcnt(0)
	v_pk_fma_f32 v[20:21], v[18:19], v[78:79], 0 op_sel_hi:[0,1,0] neg_lo:[1,0,0] neg_hi:[1,0,0]
	v_pk_fma_f32 v[18:19], v[18:19], v[80:81], 0 op_sel_hi:[0,1,0] neg_lo:[1,0,0] neg_hi:[1,0,0]
	v_cvt_pk_bf16_f32 v20, v20, v21
	v_cvt_pk_bf16_f32 v21, v18, v19
	ds_write_b64 v186, v[20:21] offset:1088
	ds_read_b32 v18, v187 offset:88
	s_waitcnt lgkmcnt(0)
	v_pk_fma_f32 v[20:21], v[18:19], v[58:59], 0 op_sel_hi:[0,1,0] neg_lo:[1,0,0] neg_hi:[1,0,0]
	v_pk_fma_f32 v[18:19], v[18:19], v[60:61], 0 op_sel_hi:[0,1,0] neg_lo:[1,0,0] neg_hi:[1,0,0]
	v_cvt_pk_bf16_f32 v20, v20, v21
	v_cvt_pk_bf16_f32 v21, v18, v19
	ds_write_b64 v186, v[20:21] offset:1632
	ds_read_b32 v18, v187 offset:96
	s_waitcnt lgkmcnt(0)
	v_pk_fma_f32 v[20:21], v[18:19], v[34:35], 0 op_sel_hi:[0,1,0] neg_lo:[1,0,0] neg_hi:[1,0,0]
	v_pk_fma_f32 v[18:19], v[18:19], v[36:37], 0 op_sel_hi:[0,1,0] neg_lo:[1,0,0] neg_hi:[1,0,0]
	v_cvt_pk_bf16_f32 v20, v20, v21
	v_cvt_pk_bf16_f32 v21, v18, v19
	ds_write_b64 v186, v[20:21] offset:2176
	ds_read_b32 v18, v187 offset:104
	s_waitcnt lgkmcnt(0)
	v_pk_fma_f32 v[20:21], v[18:19], v[22:23], 0 op_sel_hi:[0,1,0] neg_lo:[1,0,0] neg_hi:[1,0,0]
	v_pk_fma_f32 v[18:19], v[18:19], v[24:25], 0 op_sel_hi:[0,1,0] neg_lo:[1,0,0] neg_hi:[1,0,0]
	v_cvt_pk_bf16_f32 v20, v20, v21
	v_cvt_pk_bf16_f32 v21, v18, v19
	ds_write_b64 v186, v[20:21] offset:2720
	ds_read_b32 v18, v187 offset:112
	s_waitcnt lgkmcnt(0)
	v_pk_fma_f32 v[14:15], v[18:19], v[14:15], 0 op_sel_hi:[0,1,0] neg_lo:[1,0,0] neg_hi:[1,0,0]
	v_pk_fma_f32 v[16:17], v[18:19], v[16:17], 0 op_sel_hi:[0,1,0] neg_lo:[1,0,0] neg_hi:[1,0,0]
	v_cvt_pk_bf16_f32 v14, v14, v15
	v_cvt_pk_bf16_f32 v15, v16, v17
	ds_write_b64 v186, v[14:15] offset:3264
	ds_read_b32 v14, v187 offset:120
	s_waitcnt lgkmcnt(0)
	v_pk_fma_f32 v[6:7], v[14:15], v[6:7], 0 op_sel_hi:[0,1,0] neg_lo:[1,0,0] neg_hi:[1,0,0]
	v_pk_fma_f32 v[8:9], v[14:15], v[8:9], 0 op_sel_hi:[0,1,0] neg_lo:[1,0,0] neg_hi:[1,0,0]
	v_cvt_pk_bf16_f32 v6, v6, v7
	v_cvt_pk_bf16_f32 v7, v8, v9
	ds_write_b64 v186, v[6:7] offset:3808
	ds_read_b128 a[160:163], v1
	ds_read_b128 a[164:167], v1 offset:64
	ds_read_b128 a[168:171], v1 offset:128
	ds_read_b128 a[172:175], v1 offset:192
	v_lshl_add_u64 v[6:7], v[150:151], 0, s[22:23]
	v_lshl_add_u64 v[18:19], v[160:161], 0, s[22:23]
	v_lshl_add_u64 v[20:21], v[162:163], 0, s[22:23]
	v_lshl_add_u64 v[22:23], v[164:165], 0, s[22:23]
	v_lshl_add_u64 v[8:9], v[152:153], 0, s[22:23]
	v_lshl_add_u64 v[14:15], v[156:157], 0, s[22:23]
	v_lshl_add_u64 v[16:17], v[158:159], 0, s[22:23]
	v_lshl_add_u64 v[34:35], v[166:167], 0, s[22:23]
	global_load_dwordx4 v[110:113], v[6:7], off sc0 sc1 nt
	global_load_dwordx4 v[98:101], v[8:9], off sc0 sc1 nt
	global_load_dwordx4 v[78:81], v[14:15], off sc0 sc1 nt
	global_load_dwordx4 v[66:69], v[16:17], off sc0 sc1 nt
	global_load_dwordx4 v[58:61], v[18:19], off sc0 sc1 nt
	global_load_dwordx4 v[30:33], v[20:21], off sc0 sc1 nt
	s_nop 0
	global_load_dwordx4 v[22:25], v[22:23], off sc0 sc1 nt
	s_nop 0
	global_load_dwordx4 v[18:21], v[34:35], off sc0 sc1 nt
	s_waitcnt vmcnt(23)
	s_waitcnt vmcnt(22)
	s_waitcnt vmcnt(21)
	s_waitcnt vmcnt(20)
	s_waitcnt vmcnt(19)
	s_waitcnt vmcnt(18)
	s_waitcnt vmcnt(17)
	s_waitcnt vmcnt(16)
	ds_read_b32 v6, v187 offset:128
	s_waitcnt lgkmcnt(0)
	v_pk_fma_f32 v[8:9], v[6:7], v[114:115], 0 op_sel_hi:[0,1,0] neg_lo:[1,0,0] neg_hi:[1,0,0]
	v_pk_fma_f32 v[6:7], v[6:7], v[116:117], 0 op_sel_hi:[0,1,0] neg_lo:[1,0,0] neg_hi:[1,0,0]
	v_cvt_pk_bf16_f32 v8, v8, v9
	v_cvt_pk_bf16_f32 v9, v6, v7
	ds_write_b64 v186, v[8:9]
	ds_read_b32 v6, v187 offset:136
	s_waitcnt lgkmcnt(0)
	v_pk_fma_f32 v[8:9], v[6:7], v[94:95], 0 op_sel_hi:[0,1,0] neg_lo:[1,0,0] neg_hi:[1,0,0]
	v_pk_fma_f32 v[6:7], v[6:7], v[96:97], 0 op_sel_hi:[0,1,0] neg_lo:[1,0,0] neg_hi:[1,0,0]
	v_cvt_pk_bf16_f32 v8, v8, v9
	v_cvt_pk_bf16_f32 v9, v6, v7
	ds_write_b64 v186, v[8:9] offset:544
	ds_read_b32 v6, v187 offset:144
	s_waitcnt lgkmcnt(0)
	v_pk_fma_f32 v[8:9], v[6:7], v[82:83], 0 op_sel_hi:[0,1,0] neg_lo:[1,0,0] neg_hi:[1,0,0]
	v_pk_fma_f32 v[6:7], v[6:7], v[84:85], 0 op_sel_hi:[0,1,0] neg_lo:[1,0,0] neg_hi:[1,0,0]
	v_cvt_pk_bf16_f32 v8, v8, v9
	v_cvt_pk_bf16_f32 v9, v6, v7
	ds_write_b64 v186, v[8:9] offset:1088
	ds_read_b32 v6, v187 offset:152
	s_waitcnt lgkmcnt(0)
	v_pk_fma_f32 v[8:9], v[6:7], v[62:63], 0 op_sel_hi:[0,1,0] neg_lo:[1,0,0] neg_hi:[1,0,0]
	v_pk_fma_f32 v[6:7], v[6:7], v[64:65], 0 op_sel_hi:[0,1,0] neg_lo:[1,0,0] neg_hi:[1,0,0]
	v_cvt_pk_bf16_f32 v8, v8, v9
	v_cvt_pk_bf16_f32 v9, v6, v7
	ds_write_b64 v186, v[8:9] offset:1632
	ds_read_b32 v6, v187 offset:160
	s_waitcnt lgkmcnt(0)
	v_pk_fma_f32 v[8:9], v[6:7], v[38:39], 0 op_sel_hi:[0,1,0] neg_lo:[1,0,0] neg_hi:[1,0,0]
	v_pk_fma_f32 v[6:7], v[6:7], v[40:41], 0 op_sel_hi:[0,1,0] neg_lo:[1,0,0] neg_hi:[1,0,0]
	v_cvt_pk_bf16_f32 v8, v8, v9
	v_cvt_pk_bf16_f32 v9, v6, v7
	ds_write_b64 v186, v[8:9] offset:2176
	ds_read_b32 v6, v187 offset:168
	s_waitcnt lgkmcnt(0)
	v_pk_fma_f32 v[8:9], v[6:7], v[26:27], 0 op_sel_hi:[0,1,0] neg_lo:[1,0,0] neg_hi:[1,0,0]
	v_pk_fma_f32 v[6:7], v[6:7], v[28:29], 0 op_sel_hi:[0,1,0] neg_lo:[1,0,0] neg_hi:[1,0,0]
	v_cvt_pk_bf16_f32 v8, v8, v9
	v_cvt_pk_bf16_f32 v9, v6, v7
	ds_write_b64 v186, v[8:9] offset:2720
	ds_read_b32 v6, v187 offset:176
	s_waitcnt lgkmcnt(0)
	v_pk_fma_f32 v[8:9], v[6:7], v[10:11], 0 op_sel_hi:[0,1,0] neg_lo:[1,0,0] neg_hi:[1,0,0]
	v_pk_fma_f32 v[6:7], v[6:7], v[12:13], 0 op_sel_hi:[0,1,0] neg_lo:[1,0,0] neg_hi:[1,0,0]
	v_cvt_pk_bf16_f32 v8, v8, v9
	v_cvt_pk_bf16_f32 v9, v6, v7
	ds_write_b64 v186, v[8:9] offset:3264
	ds_read_b32 v6, v187 offset:184
	s_waitcnt lgkmcnt(0)
	v_pk_fma_f32 v[2:3], v[6:7], v[2:3], 0 op_sel_hi:[0,1,0] neg_lo:[1,0,0] neg_hi:[1,0,0]
	v_pk_fma_f32 v[4:5], v[6:7], v[4:5], 0 op_sel_hi:[0,1,0] neg_lo:[1,0,0] neg_hi:[1,0,0]
	v_cvt_pk_bf16_f32 v2, v2, v3
	v_cvt_pk_bf16_f32 v3, v4, v5
	ds_write_b64 v186, v[2:3] offset:3808
	ds_read_b128 a[176:179], v1
	ds_read_b128 a[180:183], v1 offset:64
	ds_read_b128 a[184:187], v1 offset:128
	ds_read_b128 a[188:191], v1 offset:192
	v_lshl_add_u64 v[2:3], v[168:169], 0, s[22:23]
	v_lshl_add_u64 v[4:5], v[170:171], 0, s[22:23]
	v_lshl_add_u64 v[6:7], v[172:173], 0, s[22:23]
	v_lshl_add_u64 v[8:9], v[174:175], 0, s[22:23]
	v_lshl_add_u64 v[10:11], v[176:177], 0, s[22:23]
	v_lshl_add_u64 v[12:13], v[178:179], 0, s[22:23]
	v_lshl_add_u64 v[14:15], v[180:181], 0, s[22:23]
	v_lshl_add_u64 v[16:17], v[182:183], 0, s[22:23]
	global_load_dwordx4 v[114:117], v[2:3], off sc0 sc1 nt
	global_load_dwordx4 v[102:105], v[4:5], off sc0 sc1 nt
	global_load_dwordx4 v[94:97], v[6:7], off sc0 sc1 nt
	global_load_dwordx4 v[82:85], v[8:9], off sc0 sc1 nt
	global_load_dwordx4 v[62:65], v[10:11], off sc0 sc1 nt
	global_load_dwordx4 v[42:45], v[12:13], off sc0 sc1 nt
	global_load_dwordx4 v[38:41], v[14:15], off sc0 sc1 nt
	global_load_dwordx4 v[34:37], v[16:17], off sc0 sc1 nt
	v_mov_b32_e32 v2, v194
	s_waitcnt vmcnt(23)
	s_waitcnt vmcnt(22)
	s_waitcnt vmcnt(21)
	s_waitcnt vmcnt(20)
	s_waitcnt vmcnt(19)
	s_waitcnt vmcnt(18)
	s_waitcnt vmcnt(17)
	s_waitcnt vmcnt(16)
	ds_read_b32 v2, v187
	s_waitcnt lgkmcnt(0)
	v_pk_fma_f32 v[4:5], v[2:3], v[106:107], 0 op_sel_hi:[0,1,0] neg_lo:[1,0,0] neg_hi:[1,0,0]
	v_pk_fma_f32 v[2:3], v[2:3], v[108:109], 0 op_sel_hi:[0,1,0] neg_lo:[1,0,0] neg_hi:[1,0,0]
	v_cvt_pk_bf16_f32 v4, v4, v5
	v_cvt_pk_bf16_f32 v5, v2, v3
	ds_write_b64 v186, v[4:5]
	ds_read_b32 v2, v187 offset:8
	s_waitcnt lgkmcnt(0)
	v_pk_fma_f32 v[4:5], v[2:3], v[90:91], 0 op_sel_hi:[0,1,0] neg_lo:[1,0,0] neg_hi:[1,0,0]
	v_pk_fma_f32 v[2:3], v[2:3], v[92:93], 0 op_sel_hi:[0,1,0] neg_lo:[1,0,0] neg_hi:[1,0,0]
	v_cvt_pk_bf16_f32 v4, v4, v5
	v_cvt_pk_bf16_f32 v5, v2, v3
	ds_write_b64 v186, v[4:5] offset:544
	ds_read_b32 v2, v187 offset:16
	s_waitcnt lgkmcnt(0)
	v_pk_fma_f32 v[4:5], v[2:3], v[86:87], 0 op_sel_hi:[0,1,0] neg_lo:[1,0,0] neg_hi:[1,0,0]
	v_pk_fma_f32 v[2:3], v[2:3], v[88:89], 0 op_sel_hi:[0,1,0] neg_lo:[1,0,0] neg_hi:[1,0,0]
	v_cvt_pk_bf16_f32 v4, v4, v5
	v_cvt_pk_bf16_f32 v5, v2, v3
	ds_write_b64 v186, v[4:5] offset:1088
	ds_read_b32 v2, v187 offset:24
	s_waitcnt lgkmcnt(0)
	v_pk_fma_f32 v[4:5], v[2:3], v[74:75], 0 op_sel_hi:[0,1,0] neg_lo:[1,0,0] neg_hi:[1,0,0]
	v_pk_fma_f32 v[2:3], v[2:3], v[76:77], 0 op_sel_hi:[0,1,0] neg_lo:[1,0,0] neg_hi:[1,0,0]
	v_cvt_pk_bf16_f32 v4, v4, v5
	v_cvt_pk_bf16_f32 v5, v2, v3
	ds_write_b64 v186, v[4:5] offset:1632
	ds_read_b32 v2, v187 offset:32
	s_waitcnt lgkmcnt(0)
	v_pk_fma_f32 v[4:5], v[2:3], v[70:71], 0 op_sel_hi:[0,1,0] neg_lo:[1,0,0] neg_hi:[1,0,0]
	v_pk_fma_f32 v[2:3], v[2:3], v[72:73], 0 op_sel_hi:[0,1,0] neg_lo:[1,0,0] neg_hi:[1,0,0]
	v_cvt_pk_bf16_f32 v4, v4, v5
	v_cvt_pk_bf16_f32 v5, v2, v3
	ds_write_b64 v186, v[4:5] offset:2176
	ds_read_b32 v2, v187 offset:40
	s_waitcnt lgkmcnt(0)
	v_pk_fma_f32 v[4:5], v[2:3], v[54:55], 0 op_sel_hi:[0,1,0] neg_lo:[1,0,0] neg_hi:[1,0,0]
	v_pk_fma_f32 v[2:3], v[2:3], v[56:57], 0 op_sel_hi:[0,1,0] neg_lo:[1,0,0] neg_hi:[1,0,0]
	v_cvt_pk_bf16_f32 v4, v4, v5
	v_cvt_pk_bf16_f32 v5, v2, v3
	ds_write_b64 v186, v[4:5] offset:2720
	ds_read_b32 v2, v187 offset:48
	s_waitcnt lgkmcnt(0)
	v_pk_fma_f32 v[4:5], v[2:3], v[50:51], 0 op_sel_hi:[0,1,0] neg_lo:[1,0,0] neg_hi:[1,0,0]
	v_pk_fma_f32 v[2:3], v[2:3], v[52:53], 0 op_sel_hi:[0,1,0] neg_lo:[1,0,0] neg_hi:[1,0,0]
	v_cvt_pk_bf16_f32 v4, v4, v5
	v_cvt_pk_bf16_f32 v5, v2, v3
	ds_write_b64 v186, v[4:5] offset:3264
	ds_read_b32 v2, v187 offset:56
	s_waitcnt lgkmcnt(0)
	v_pk_fma_f32 v[4:5], v[2:3], v[46:47], 0 op_sel_hi:[0,1,0] neg_lo:[1,0,0] neg_hi:[1,0,0]
	v_pk_fma_f32 v[2:3], v[2:3], v[48:49], 0 op_sel_hi:[0,1,0] neg_lo:[1,0,0] neg_hi:[1,0,0]
	v_cvt_pk_bf16_f32 v4, v4, v5
	v_cvt_pk_bf16_f32 v5, v2, v3
	ds_write_b64 v186, v[4:5] offset:3808
	ds_read_b128 a[192:195], v1
	ds_read_b128 a[196:199], v1 offset:64
	ds_read_b128 a[200:203], v1 offset:128
	ds_read_b128 a[204:207], v1 offset:192
	v_lshl_add_u64 v[118:119], v[130:131], 0, s[20:21]
	v_add_co_u32_e32 v126, vcc, s7, v118
	s_nop 1
	v_addc_co_u32_e32 v127, vcc, 0, v119, vcc
	v_add_co_u32_e32 v128, vcc, s36, v118
	global_load_dwordx4 v[90:93], v[118:119], off sc0 sc1 nt
	global_load_dwordx4 v[86:89], v[126:127], off sc0 sc1 nt
	v_addc_co_u32_e32 v129, vcc, 0, v119, vcc
	v_add_co_u32_e32 v134, vcc, s37, v118
	s_nop 1
	v_addc_co_u32_e32 v135, vcc, 0, v119, vcc
	v_add_co_u32_e32 v136, vcc, s38, v118
	global_load_dwordx4 v[54:57], v[128:129], off sc0 sc1 nt
	global_load_dwordx4 v[50:53], v[134:135], off sc0 sc1 nt
	v_addc_co_u32_e32 v137, vcc, 0, v119, vcc
	v_add_co_u32_e32 v138, vcc, s39, v118
	s_nop 1
	v_addc_co_u32_e32 v139, vcc, 0, v119, vcc
	v_add_co_u32_e32 v140, vcc, s41, v118
	global_load_dwordx4 v[14:17], v[136:137], off sc0 sc1 nt
	global_load_dwordx4 v[10:13], v[138:139], off sc0 sc1 nt
	v_addc_co_u32_e32 v141, vcc, 0, v119, vcc
	v_add_co_u32_e32 v142, vcc, s42, v118
	s_nop 1
	v_addc_co_u32_e32 v143, vcc, 0, v119, vcc
	global_load_dwordx4 v[6:9], v[140:141], off sc0 sc1 nt
	global_load_dwordx4 v[2:5], v[142:143], off sc0 sc1 nt
	v_mov_b32_e32 v26, v194
	s_waitcnt vmcnt(23)
	s_waitcnt vmcnt(22)
	s_waitcnt vmcnt(21)
	s_waitcnt vmcnt(20)
	s_waitcnt vmcnt(19)
	s_waitcnt vmcnt(18)
	s_waitcnt vmcnt(17)
	s_waitcnt vmcnt(16)
	ds_read_b32 v26, v187 offset:64
	s_waitcnt lgkmcnt(0)
	v_pk_fma_f32 v[28:29], v[26:27], v[110:111], 0 op_sel_hi:[0,1,0] neg_lo:[1,0,0] neg_hi:[1,0,0]
	v_pk_fma_f32 v[26:27], v[26:27], v[112:113], 0 op_sel_hi:[0,1,0] neg_lo:[1,0,0] neg_hi:[1,0,0]
	v_cvt_pk_bf16_f32 v28, v28, v29
	v_cvt_pk_bf16_f32 v29, v26, v27
	ds_write_b64 v186, v[28:29]
	ds_read_b32 v26, v187 offset:72
	s_waitcnt lgkmcnt(0)
	v_pk_fma_f32 v[28:29], v[26:27], v[98:99], 0 op_sel_hi:[0,1,0] neg_lo:[1,0,0] neg_hi:[1,0,0]
	v_pk_fma_f32 v[26:27], v[26:27], v[100:101], 0 op_sel_hi:[0,1,0] neg_lo:[1,0,0] neg_hi:[1,0,0]
	v_cvt_pk_bf16_f32 v28, v28, v29
	v_cvt_pk_bf16_f32 v29, v26, v27
	ds_write_b64 v186, v[28:29] offset:544
	ds_read_b32 v26, v187 offset:80
	s_waitcnt lgkmcnt(0)
	v_pk_fma_f32 v[28:29], v[26:27], v[78:79], 0 op_sel_hi:[0,1,0] neg_lo:[1,0,0] neg_hi:[1,0,0]
	v_pk_fma_f32 v[26:27], v[26:27], v[80:81], 0 op_sel_hi:[0,1,0] neg_lo:[1,0,0] neg_hi:[1,0,0]
	v_cvt_pk_bf16_f32 v28, v28, v29
	v_cvt_pk_bf16_f32 v29, v26, v27
	ds_write_b64 v186, v[28:29] offset:1088
	ds_read_b32 v26, v187 offset:88
	s_waitcnt lgkmcnt(0)
	v_pk_fma_f32 v[28:29], v[26:27], v[66:67], 0 op_sel_hi:[0,1,0] neg_lo:[1,0,0] neg_hi:[1,0,0]
	v_pk_fma_f32 v[26:27], v[26:27], v[68:69], 0 op_sel_hi:[0,1,0] neg_lo:[1,0,0] neg_hi:[1,0,0]
	v_cvt_pk_bf16_f32 v28, v28, v29
	v_cvt_pk_bf16_f32 v29, v26, v27
	ds_write_b64 v186, v[28:29] offset:1632
	ds_read_b32 v26, v187 offset:96
	s_waitcnt lgkmcnt(0)
	v_pk_fma_f32 v[28:29], v[26:27], v[58:59], 0 op_sel_hi:[0,1,0] neg_lo:[1,0,0] neg_hi:[1,0,0]
	v_pk_fma_f32 v[26:27], v[26:27], v[60:61], 0 op_sel_hi:[0,1,0] neg_lo:[1,0,0] neg_hi:[1,0,0]
	v_cvt_pk_bf16_f32 v28, v28, v29
	v_cvt_pk_bf16_f32 v29, v26, v27
	ds_write_b64 v186, v[28:29] offset:2176
	ds_read_b32 v26, v187 offset:104
	s_waitcnt lgkmcnt(0)
	v_pk_fma_f32 v[28:29], v[26:27], v[30:31], 0 op_sel_hi:[0,1,0] neg_lo:[1,0,0] neg_hi:[1,0,0]
	v_pk_fma_f32 v[26:27], v[26:27], v[32:33], 0 op_sel_hi:[0,1,0] neg_lo:[1,0,0] neg_hi:[1,0,0]
	v_cvt_pk_bf16_f32 v28, v28, v29
	v_cvt_pk_bf16_f32 v29, v26, v27
	ds_write_b64 v186, v[28:29] offset:2720
	ds_read_b32 v26, v187 offset:112
	s_waitcnt lgkmcnt(0)
	v_pk_fma_f32 v[22:23], v[26:27], v[22:23], 0 op_sel_hi:[0,1,0] neg_lo:[1,0,0] neg_hi:[1,0,0]
	v_pk_fma_f32 v[24:25], v[26:27], v[24:25], 0 op_sel_hi:[0,1,0] neg_lo:[1,0,0] neg_hi:[1,0,0]
	v_cvt_pk_bf16_f32 v22, v22, v23
	v_cvt_pk_bf16_f32 v23, v24, v25
	ds_write_b64 v186, v[22:23] offset:3264
	ds_read_b32 v22, v187 offset:120
	s_waitcnt lgkmcnt(0)
	v_pk_fma_f32 v[18:19], v[22:23], v[18:19], 0 op_sel_hi:[0,1,0] neg_lo:[1,0,0] neg_hi:[1,0,0]
	v_pk_fma_f32 v[20:21], v[22:23], v[20:21], 0 op_sel_hi:[0,1,0] neg_lo:[1,0,0] neg_hi:[1,0,0]
	v_cvt_pk_bf16_f32 v18, v18, v19
	v_cvt_pk_bf16_f32 v19, v20, v21
	ds_write_b64 v186, v[18:19] offset:3808
	ds_read_b128 a[208:211], v1
	ds_read_b128 a[212:215], v1 offset:64
	ds_read_b128 a[216:219], v1 offset:128
	ds_read_b128 a[220:223], v1 offset:192
	v_lshl_add_u64 v[18:19], v[150:151], 0, s[20:21]
	v_lshl_add_u64 v[20:21], v[152:153], 0, s[20:21]
	v_lshl_add_u64 v[22:23], v[156:157], 0, s[20:21]
	v_lshl_add_u64 v[24:25], v[158:159], 0, s[20:21]
	v_lshl_add_u64 v[26:27], v[160:161], 0, s[20:21]
	v_lshl_add_u64 v[28:29], v[162:163], 0, s[20:21]
	v_lshl_add_u64 v[46:47], v[164:165], 0, s[20:21]
	v_lshl_add_u64 v[48:49], v[166:167], 0, s[20:21]
	global_load_dwordx4 v[78:81], v[18:19], off sc0 sc1 nt
	global_load_dwordx4 v[74:77], v[20:21], off sc0 sc1 nt
	global_load_dwordx4 v[70:73], v[22:23], off sc0 sc1 nt
	global_load_dwordx4 v[66:69], v[24:25], off sc0 sc1 nt
	global_load_dwordx4 v[30:33], v[26:27], off sc0 sc1 nt
	s_nop 0
	global_load_dwordx4 v[26:29], v[28:29], off sc0 sc1 nt
	s_nop 0
	global_load_dwordx4 v[22:25], v[46:47], off sc0 sc1 nt
	global_load_dwordx4 v[18:21], v[48:49], off sc0 sc1 nt
	s_waitcnt vmcnt(23)
	s_waitcnt vmcnt(22)
	s_waitcnt vmcnt(21)
	s_waitcnt vmcnt(20)
	s_waitcnt vmcnt(19)
	s_waitcnt vmcnt(18)
	s_waitcnt vmcnt(17)
	s_waitcnt vmcnt(16)
	ds_read_b32 v46, v187 offset:128
	s_waitcnt lgkmcnt(0)
	v_pk_fma_f32 v[48:49], v[46:47], v[114:115], 0 op_sel_hi:[0,1,0] neg_lo:[1,0,0] neg_hi:[1,0,0]
	v_pk_fma_f32 v[46:47], v[46:47], v[116:117], 0 op_sel_hi:[0,1,0] neg_lo:[1,0,0] neg_hi:[1,0,0]
	v_cvt_pk_bf16_f32 v48, v48, v49
	v_cvt_pk_bf16_f32 v49, v46, v47
	ds_write_b64 v186, v[48:49]
	ds_read_b32 v46, v187 offset:136
	s_waitcnt lgkmcnt(0)
	v_pk_fma_f32 v[48:49], v[46:47], v[102:103], 0 op_sel_hi:[0,1,0] neg_lo:[1,0,0] neg_hi:[1,0,0]
	v_pk_fma_f32 v[46:47], v[46:47], v[104:105], 0 op_sel_hi:[0,1,0] neg_lo:[1,0,0] neg_hi:[1,0,0]
	v_cvt_pk_bf16_f32 v48, v48, v49
	v_cvt_pk_bf16_f32 v49, v46, v47
	ds_write_b64 v186, v[48:49] offset:544
	ds_read_b32 v46, v187 offset:144
	s_waitcnt lgkmcnt(0)
	v_pk_fma_f32 v[48:49], v[46:47], v[94:95], 0 op_sel_hi:[0,1,0] neg_lo:[1,0,0] neg_hi:[1,0,0]
	v_pk_fma_f32 v[46:47], v[46:47], v[96:97], 0 op_sel_hi:[0,1,0] neg_lo:[1,0,0] neg_hi:[1,0,0]
	v_cvt_pk_bf16_f32 v48, v48, v49
	v_cvt_pk_bf16_f32 v49, v46, v47
	ds_write_b64 v186, v[48:49] offset:1088
	ds_read_b32 v46, v187 offset:152
	s_waitcnt lgkmcnt(0)
	v_pk_fma_f32 v[48:49], v[46:47], v[82:83], 0 op_sel_hi:[0,1,0] neg_lo:[1,0,0] neg_hi:[1,0,0]
	v_pk_fma_f32 v[46:47], v[46:47], v[84:85], 0 op_sel_hi:[0,1,0] neg_lo:[1,0,0] neg_hi:[1,0,0]
	v_cvt_pk_bf16_f32 v48, v48, v49
	v_cvt_pk_bf16_f32 v49, v46, v47
	ds_write_b64 v186, v[48:49] offset:1632
	ds_read_b32 v46, v187 offset:160
	s_waitcnt lgkmcnt(0)
	v_pk_fma_f32 v[48:49], v[46:47], v[62:63], 0 op_sel_hi:[0,1,0] neg_lo:[1,0,0] neg_hi:[1,0,0]
	v_pk_fma_f32 v[46:47], v[46:47], v[64:65], 0 op_sel_hi:[0,1,0] neg_lo:[1,0,0] neg_hi:[1,0,0]
	v_cvt_pk_bf16_f32 v48, v48, v49
	v_cvt_pk_bf16_f32 v49, v46, v47
	ds_write_b64 v186, v[48:49] offset:2176
	ds_read_b32 v46, v187 offset:168
	s_waitcnt lgkmcnt(0)
	v_pk_fma_f32 v[42:43], v[46:47], v[42:43], 0 op_sel_hi:[0,1,0] neg_lo:[1,0,0] neg_hi:[1,0,0]
	v_pk_fma_f32 v[44:45], v[46:47], v[44:45], 0 op_sel_hi:[0,1,0] neg_lo:[1,0,0] neg_hi:[1,0,0]
	v_cvt_pk_bf16_f32 v42, v42, v43
	v_cvt_pk_bf16_f32 v43, v44, v45
	ds_write_b64 v186, v[42:43] offset:2720
	ds_read_b32 v42, v187 offset:176
	s_waitcnt lgkmcnt(0)
	v_pk_fma_f32 v[38:39], v[42:43], v[38:39], 0 op_sel_hi:[0,1,0] neg_lo:[1,0,0] neg_hi:[1,0,0]
	v_pk_fma_f32 v[40:41], v[42:43], v[40:41], 0 op_sel_hi:[0,1,0] neg_lo:[1,0,0] neg_hi:[1,0,0]
	v_cvt_pk_bf16_f32 v38, v38, v39
	v_cvt_pk_bf16_f32 v39, v40, v41
	ds_write_b64 v186, v[38:39] offset:3264
	ds_read_b32 v38, v187 offset:184
	s_waitcnt lgkmcnt(0)
	v_pk_fma_f32 v[34:35], v[38:39], v[34:35], 0 op_sel_hi:[0,1,0] neg_lo:[1,0,0] neg_hi:[1,0,0]
	v_pk_fma_f32 v[36:37], v[38:39], v[36:37], 0 op_sel_hi:[0,1,0] neg_lo:[1,0,0] neg_hi:[1,0,0]
	v_cvt_pk_bf16_f32 v34, v34, v35
	v_cvt_pk_bf16_f32 v35, v36, v37
	ds_write_b64 v186, v[34:35] offset:3808
	ds_read_b128 a[224:227], v1
	ds_read_b128 a[228:231], v1 offset:64
	ds_read_b128 a[232:235], v1 offset:128
	ds_read_b128 a[236:239], v1 offset:192
	v_lshl_add_u64 v[34:35], v[168:169], 0, s[20:21]
	v_lshl_add_u64 v[36:37], v[170:171], 0, s[20:21]
	v_lshl_add_u64 v[38:39], v[172:173], 0, s[20:21]
	v_lshl_add_u64 v[40:41], v[174:175], 0, s[20:21]
	v_lshl_add_u64 v[42:43], v[176:177], 0, s[20:21]
	v_lshl_add_u64 v[44:45], v[178:179], 0, s[20:21]
	v_lshl_add_u64 v[58:59], v[180:181], 0, s[20:21]
	v_lshl_add_u64 v[60:61], v[182:183], 0, s[20:21]
	global_load_dwordx4 v[122:125], v[34:35], off sc0 sc1 nt
	global_load_dwordx4 v[106:109], v[36:37], off sc0 sc1 nt
	global_load_dwordx4 v[94:97], v[38:39], off sc0 sc1 nt
	global_load_dwordx4 v[82:85], v[40:41], off sc0 sc1 nt
	global_load_dwordx4 v[46:49], v[42:43], off sc0 sc1 nt
	s_nop 0
	global_load_dwordx4 v[42:45], v[44:45], off sc0 sc1 nt
	s_nop 0
	global_load_dwordx4 v[38:41], v[58:59], off sc0 sc1 nt
	global_load_dwordx4 v[34:37], v[60:61], off sc0 sc1 nt
	v_mov_b32_e32 v98, v133
	s_waitcnt vmcnt(23)
	s_waitcnt vmcnt(22)
	s_waitcnt vmcnt(21)
	s_waitcnt vmcnt(20)
	s_waitcnt vmcnt(19)
	s_waitcnt vmcnt(18)
	s_waitcnt vmcnt(17)
	s_waitcnt vmcnt(16)
	ds_read_b32 v58, v187
	v_add_u32_e32 v99, 1, v98
	v_cmp_eq_u32_e32 vcc, v98, v132
	s_nop 1
	v_cndmask_b32_e64 v60, 0, 1.0, vcc
	v_cmp_eq_u32_e32 vcc, v99, v132
	s_nop 1
	v_cndmask_b32_e64 v61, 0, 1.0, vcc
	s_waitcnt lgkmcnt(0)
	v_pk_fma_f32 v[62:63], v[58:59], v[90:91], v[60:61] op_sel_hi:[0,1,1] neg_lo:[1,0,0] neg_hi:[1,0,0]
	v_add_u32_e32 v90, 3, v98
	v_add_u32_e32 v91, 2, v98
	v_cmp_eq_u32_e32 vcc, v90, v132
	v_cvt_pk_bf16_f32 v62, v62, v63
	s_nop 0
	v_cndmask_b32_e64 v65, 0, 1.0, vcc
	v_cmp_eq_u32_e32 vcc, v91, v132
	s_nop 1
	v_cndmask_b32_e64 v64, 0, 1.0, vcc
	v_pk_fma_f32 v[58:59], v[58:59], v[92:93], v[64:65] op_sel_hi:[0,1,1] neg_lo:[1,0,0] neg_hi:[1,0,0]
	v_cvt_pk_bf16_f32 v63, v58, v59
	ds_write_b64 v186, v[62:63]
	ds_read_b32 v58, v187 offset:8
	v_cmp_eq_u32_e32 vcc, v98, v193
	s_nop 1
	v_cndmask_b32_e64 v62, 0, 1.0, vcc
	v_cmp_eq_u32_e32 vcc, v99, v193
	s_nop 1
	v_cndmask_b32_e64 v63, 0, 1.0, vcc
	v_cmp_eq_u32_e32 vcc, v90, v193
	s_waitcnt lgkmcnt(0)
	v_pk_fma_f32 v[62:63], v[58:59], v[86:87], v[62:63] op_sel_hi:[0,1,1] neg_lo:[1,0,0] neg_hi:[1,0,0]
	v_cvt_pk_bf16_f32 v62, v62, v63
	v_cndmask_b32_e64 v61, 0, 1.0, vcc
	v_pk_fma_f32 v[58:59], v[58:59], v[88:89], v[60:61] op_sel_hi:[0,1,1] neg_lo:[1,0,0] neg_hi:[1,0,0]
	v_cvt_pk_bf16_f32 v63, v58, v59
	ds_write_b64 v186, v[62:63] offset:544
	ds_read_b32 v58, v187 offset:16
	v_cmp_eq_u32_e32 vcc, v98, v192
	s_nop 1
	v_cndmask_b32_e64 v60, 0, 1.0, vcc
	v_cmp_eq_u32_e32 vcc, v99, v192
	s_nop 1
	v_cndmask_b32_e64 v61, 0, 1.0, vcc
	v_cmp_eq_u32_e32 vcc, v90, v192
	s_waitcnt lgkmcnt(0)
	v_pk_fma_f32 v[54:55], v[58:59], v[54:55], v[60:61] op_sel_hi:[0,1,1] neg_lo:[1,0,0] neg_hi:[1,0,0]
	v_cvt_pk_bf16_f32 v54, v54, v55
	v_cndmask_b32_e64 v61, 0, 1.0, vcc
	v_cmp_eq_u32_e32 vcc, v91, v192
	s_nop 1
	v_cndmask_b32_e64 v60, 0, 1.0, vcc
	v_pk_fma_f32 v[56:57], v[58:59], v[56:57], v[60:61] op_sel_hi:[0,1,1] neg_lo:[1,0,0] neg_hi:[1,0,0]
	v_cvt_pk_bf16_f32 v55, v56, v57
	ds_write_b64 v186, v[54:55] offset:1088
	ds_read_b32 v54, v187 offset:24
	v_cmp_eq_u32_e32 vcc, v98, v190
	s_nop 1
	v_cndmask_b32_e64 v56, 0, 1.0, vcc
	v_cmp_eq_u32_e32 vcc, v99, v190
	s_nop 1
	v_cndmask_b32_e64 v57, 0, 1.0, vcc
	v_cmp_eq_u32_e32 vcc, v90, v190
	s_waitcnt lgkmcnt(0)
	v_pk_fma_f32 v[50:51], v[54:55], v[50:51], v[56:57] op_sel_hi:[0,1,1] neg_lo:[1,0,0] neg_hi:[1,0,0]
	v_cvt_pk_bf16_f32 v50, v50, v51
	v_cndmask_b32_e64 v57, 0, 1.0, vcc
	v_cmp_eq_u32_e32 vcc, v91, v190
	s_nop 1
	v_cndmask_b32_e64 v56, 0, 1.0, vcc
	v_pk_fma_f32 v[52:53], v[54:55], v[52:53], v[56:57] op_sel_hi:[0,1,1] neg_lo:[1,0,0] neg_hi:[1,0,0]
	v_cvt_pk_bf16_f32 v51, v52, v53
	ds_write_b64 v186, v[50:51] offset:1632
	ds_read_b32 v50, v187 offset:32
	v_cmp_eq_u32_e32 vcc, v98, v149
	s_nop 1
	v_cndmask_b32_e64 v52, 0, 1.0, vcc
	v_cmp_eq_u32_e32 vcc, v99, v149
	s_nop 1
	v_cndmask_b32_e64 v53, 0, 1.0, vcc
	v_cmp_eq_u32_e32 vcc, v90, v149
	s_waitcnt lgkmcnt(0)
	v_pk_fma_f32 v[14:15], v[50:51], v[14:15], v[52:53] op_sel_hi:[0,1,1] neg_lo:[1,0,0] neg_hi:[1,0,0]
	v_cvt_pk_bf16_f32 v14, v14, v15
	v_cndmask_b32_e64 v53, 0, 1.0, vcc
	v_cmp_eq_u32_e32 vcc, v91, v149
	s_nop 1
	v_cndmask_b32_e64 v52, 0, 1.0, vcc
	v_pk_fma_f32 v[16:17], v[50:51], v[16:17], v[52:53] op_sel_hi:[0,1,1] neg_lo:[1,0,0] neg_hi:[1,0,0]
	v_cvt_pk_bf16_f32 v15, v16, v17
	ds_write_b64 v186, v[14:15] offset:2176
	ds_read_b32 v14, v187 offset:40
	v_cmp_eq_u32_e32 vcc, v98, v148
	s_nop 1
	v_cndmask_b32_e64 v16, 0, 1.0, vcc
	v_cmp_eq_u32_e32 vcc, v99, v148
	s_nop 1
	v_cndmask_b32_e64 v17, 0, 1.0, vcc
	v_cmp_eq_u32_e32 vcc, v90, v148
	s_waitcnt lgkmcnt(0)
	v_pk_fma_f32 v[10:11], v[14:15], v[10:11], v[16:17] op_sel_hi:[0,1,1] neg_lo:[1,0,0] neg_hi:[1,0,0]
	v_cvt_pk_bf16_f32 v10, v10, v11
	v_cndmask_b32_e64 v17, 0, 1.0, vcc
	v_cmp_eq_u32_e32 vcc, v91, v148
	s_nop 1
	v_cndmask_b32_e64 v16, 0, 1.0, vcc
	v_pk_fma_f32 v[12:13], v[14:15], v[12:13], v[16:17] op_sel_hi:[0,1,1] neg_lo:[1,0,0] neg_hi:[1,0,0]
	v_cvt_pk_bf16_f32 v11, v12, v13
	ds_write_b64 v186, v[10:11] offset:2720
	ds_read_b32 v10, v187 offset:48
	v_cmp_eq_u32_e32 vcc, v98, v147
	s_nop 1
	v_cndmask_b32_e64 v12, 0, 1.0, vcc
	v_cmp_eq_u32_e32 vcc, v99, v147
	s_nop 1
	v_cndmask_b32_e64 v13, 0, 1.0, vcc
	v_cmp_eq_u32_e32 vcc, v90, v147
	s_waitcnt lgkmcnt(0)
	v_pk_fma_f32 v[6:7], v[10:11], v[6:7], v[12:13] op_sel_hi:[0,1,1] neg_lo:[1,0,0] neg_hi:[1,0,0]
	v_cvt_pk_bf16_f32 v6, v6, v7
	v_cndmask_b32_e64 v13, 0, 1.0, vcc
	v_cmp_eq_u32_e32 vcc, v91, v147
	s_nop 1
	v_cndmask_b32_e64 v12, 0, 1.0, vcc
	v_pk_fma_f32 v[8:9], v[10:11], v[8:9], v[12:13] op_sel_hi:[0,1,1] neg_lo:[1,0,0] neg_hi:[1,0,0]
	v_cvt_pk_bf16_f32 v7, v8, v9
	ds_write_b64 v186, v[6:7] offset:3264
	ds_read_b32 v6, v187 offset:56
	v_cmp_eq_u32_e32 vcc, v98, v146
	s_nop 1
	v_cndmask_b32_e64 v8, 0, 1.0, vcc
	v_cmp_eq_u32_e32 vcc, v99, v146
	s_nop 1
	v_cndmask_b32_e64 v9, 0, 1.0, vcc
	v_cmp_eq_u32_e32 vcc, v90, v146
	s_waitcnt lgkmcnt(0)
	v_pk_fma_f32 v[2:3], v[6:7], v[2:3], v[8:9] op_sel_hi:[0,1,1] neg_lo:[1,0,0] neg_hi:[1,0,0]
	v_cvt_pk_bf16_f32 v2, v2, v3
	v_cndmask_b32_e64 v9, 0, 1.0, vcc
	v_cmp_eq_u32_e32 vcc, v91, v146
	s_nop 1
	v_cndmask_b32_e64 v8, 0, 1.0, vcc
	v_pk_fma_f32 v[4:5], v[6:7], v[4:5], v[8:9] op_sel_hi:[0,1,1] neg_lo:[1,0,0] neg_hi:[1,0,0]
	v_cvt_pk_bf16_f32 v3, v4, v5
	ds_write_b64 v186, v[2:3] offset:3808
	ds_read_b128 v[2:5], v1
	ds_read_b128 v[6:9], v1 offset:64
	ds_read_b128 v[10:13], v1 offset:128
	ds_read_b128 v[14:17], v1 offset:192
	global_load_dwordx4 v[118:121], v[118:119], off offset:512 sc0 sc1 nt
	s_nop 0
	global_load_dwordx4 v[110:113], v[126:127], off offset:512 sc0 sc1 nt
	global_load_dwordx4 v[98:101], v[128:129], off offset:512 sc0 sc1 nt
	global_load_dwordx4 v[86:89], v[134:135], off offset:512 sc0 sc1 nt
	global_load_dwordx4 v[62:65], v[136:137], off offset:512 sc0 sc1 nt
	global_load_dwordx4 v[58:61], v[138:139], off offset:512 sc0 sc1 nt
	global_load_dwordx4 v[54:57], v[140:141], off offset:512 sc0 sc1 nt
	global_load_dwordx4 v[50:53], v[142:143], off offset:512 sc0 sc1 nt
	v_mov_b32_e32 v91, v133
	s_waitcnt vmcnt(23)
	s_waitcnt vmcnt(22)
	s_waitcnt vmcnt(21)
	s_waitcnt vmcnt(20)
	s_waitcnt vmcnt(19)
	s_waitcnt vmcnt(18)
	s_waitcnt vmcnt(17)
	s_waitcnt vmcnt(16)
	ds_read_b32 v90, v187 offset:64
	v_or_b32_e32 v138, 16, v132
	v_add_u32_e32 v102, 1, v91
	v_cmp_eq_u32_e32 vcc, v91, v138
	v_add_u32_e32 v103, 3, v91
	v_add_u32_e32 v104, 2, v91
	v_cndmask_b32_e64 v92, 0, 1.0, vcc
	v_cmp_eq_u32_e32 vcc, v102, v138
	v_or_b32_e32 v139, 18, v132
	v_or_b32_e32 v140, 20, v132
	v_cndmask_b32_e64 v93, 0, 1.0, vcc
	v_cmp_eq_u32_e32 vcc, v103, v138
	s_waitcnt lgkmcnt(0)
	v_pk_fma_f32 v[78:79], v[90:91], v[78:79], v[92:93] op_sel_hi:[0,1,1] neg_lo:[1,0,0] neg_hi:[1,0,0]
	v_cvt_pk_bf16_f32 v78, v78, v79
	v_cndmask_b32_e64 v93, 0, 1.0, vcc
	v_cmp_eq_u32_e32 vcc, v104, v138
	v_or_b32_e32 v141, 22, v132
	v_or_b32_e32 v142, 24, v132
	v_cndmask_b32_e64 v92, 0, 1.0, vcc
	v_pk_fma_f32 v[80:81], v[90:91], v[80:81], v[92:93] op_sel_hi:[0,1,1] neg_lo:[1,0,0] neg_hi:[1,0,0]
	v_cvt_pk_bf16_f32 v79, v80, v81
	ds_write_b64 v186, v[78:79]
	ds_read_b32 v78, v187 offset:72
	v_cmp_eq_u32_e32 vcc, v91, v139
	v_or_b32_e32 v143, 26, v132
	v_or_b32_e32 v144, 28, v132
	v_cndmask_b32_e64 v80, 0, 1.0, vcc
	v_cmp_eq_u32_e32 vcc, v102, v139
	v_or_b32_e32 v145, 30, v132
	s_nop 0
	v_cndmask_b32_e64 v81, 0, 1.0, vcc
	v_cmp_eq_u32_e32 vcc, v103, v139
	s_waitcnt lgkmcnt(0)
	v_pk_fma_f32 v[74:75], v[78:79], v[74:75], v[80:81] op_sel_hi:[0,1,1] neg_lo:[1,0,0] neg_hi:[1,0,0]
	v_cvt_pk_bf16_f32 v74, v74, v75
	v_cndmask_b32_e64 v81, 0, 1.0, vcc
	v_cmp_eq_u32_e32 vcc, v104, v139
	s_nop 1
	v_cndmask_b32_e64 v80, 0, 1.0, vcc
	v_pk_fma_f32 v[76:77], v[78:79], v[76:77], v[80:81] op_sel_hi:[0,1,1] neg_lo:[1,0,0] neg_hi:[1,0,0]
	v_cvt_pk_bf16_f32 v75, v76, v77
	ds_write_b64 v186, v[74:75] offset:544
	ds_read_b32 v74, v187 offset:80
	v_cmp_eq_u32_e32 vcc, v91, v140
	s_nop 1
	v_cndmask_b32_e64 v76, 0, 1.0, vcc
	v_cmp_eq_u32_e32 vcc, v102, v140
	s_nop 1
	v_cndmask_b32_e64 v77, 0, 1.0, vcc
	v_cmp_eq_u32_e32 vcc, v103, v140
	s_waitcnt lgkmcnt(0)
	v_pk_fma_f32 v[70:71], v[74:75], v[70:71], v[76:77] op_sel_hi:[0,1,1] neg_lo:[1,0,0] neg_hi:[1,0,0]
	v_cvt_pk_bf16_f32 v70, v70, v71
	v_cndmask_b32_e64 v77, 0, 1.0, vcc
	v_cmp_eq_u32_e32 vcc, v104, v140
	s_nop 1
	v_cndmask_b32_e64 v76, 0, 1.0, vcc
	v_pk_fma_f32 v[72:73], v[74:75], v[72:73], v[76:77] op_sel_hi:[0,1,1] neg_lo:[1,0,0] neg_hi:[1,0,0]
	v_cvt_pk_bf16_f32 v71, v72, v73
	ds_write_b64 v186, v[70:71] offset:1088
	ds_read_b32 v70, v187 offset:88
	v_cmp_eq_u32_e32 vcc, v91, v141
	s_nop 1
	v_cndmask_b32_e64 v72, 0, 1.0, vcc
	v_cmp_eq_u32_e32 vcc, v102, v141
	s_nop 1
	v_cndmask_b32_e64 v73, 0, 1.0, vcc
	v_cmp_eq_u32_e32 vcc, v103, v141
	s_waitcnt lgkmcnt(0)
	v_pk_fma_f32 v[66:67], v[70:71], v[66:67], v[72:73] op_sel_hi:[0,1,1] neg_lo:[1,0,0] neg_hi:[1,0,0]
	v_cvt_pk_bf16_f32 v66, v66, v67
	v_cndmask_b32_e64 v73, 0, 1.0, vcc
	v_cmp_eq_u32_e32 vcc, v104, v141
	s_nop 1
	v_cndmask_b32_e64 v72, 0, 1.0, vcc
	v_pk_fma_f32 v[68:69], v[70:71], v[68:69], v[72:73] op_sel_hi:[0,1,1] neg_lo:[1,0,0] neg_hi:[1,0,0]
	v_cvt_pk_bf16_f32 v67, v68, v69
	ds_write_b64 v186, v[66:67] offset:1632
	ds_read_b32 v66, v187 offset:96
	v_cmp_eq_u32_e32 vcc, v91, v142
	s_nop 1
	v_cndmask_b32_e64 v68, 0, 1.0, vcc
	v_cmp_eq_u32_e32 vcc, v102, v142
	s_nop 1
	v_cndmask_b32_e64 v69, 0, 1.0, vcc
	v_cmp_eq_u32_e32 vcc, v103, v142
	s_waitcnt lgkmcnt(0)
	v_pk_fma_f32 v[30:31], v[66:67], v[30:31], v[68:69] op_sel_hi:[0,1,1] neg_lo:[1,0,0] neg_hi:[1,0,0]
	v_cvt_pk_bf16_f32 v30, v30, v31
	v_cndmask_b32_e64 v69, 0, 1.0, vcc
	v_cmp_eq_u32_e32 vcc, v104, v142
	s_nop 1
	v_cndmask_b32_e64 v68, 0, 1.0, vcc
	v_pk_fma_f32 v[32:33], v[66:67], v[32:33], v[68:69] op_sel_hi:[0,1,1] neg_lo:[1,0,0] neg_hi:[1,0,0]
	v_cvt_pk_bf16_f32 v31, v32, v33
	ds_write_b64 v186, v[30:31] offset:2176
	ds_read_b32 v30, v187 offset:104
	v_cmp_eq_u32_e32 vcc, v91, v143
	s_nop 1
	v_cndmask_b32_e64 v32, 0, 1.0, vcc
	v_cmp_eq_u32_e32 vcc, v102, v143
	s_nop 1
	v_cndmask_b32_e64 v33, 0, 1.0, vcc
	v_cmp_eq_u32_e32 vcc, v103, v143
	s_waitcnt lgkmcnt(0)
	v_pk_fma_f32 v[26:27], v[30:31], v[26:27], v[32:33] op_sel_hi:[0,1,1] neg_lo:[1,0,0] neg_hi:[1,0,0]
	v_cvt_pk_bf16_f32 v26, v26, v27
	v_cndmask_b32_e64 v33, 0, 1.0, vcc
	v_cmp_eq_u32_e32 vcc, v104, v143
	s_nop 1
	v_cndmask_b32_e64 v32, 0, 1.0, vcc
	v_pk_fma_f32 v[28:29], v[30:31], v[28:29], v[32:33] op_sel_hi:[0,1,1] neg_lo:[1,0,0] neg_hi:[1,0,0]
	v_cvt_pk_bf16_f32 v27, v28, v29
	ds_write_b64 v186, v[26:27] offset:2720
	ds_read_b32 v26, v187 offset:112
	v_cmp_eq_u32_e32 vcc, v91, v144
	s_nop 1
	v_cndmask_b32_e64 v28, 0, 1.0, vcc
	v_cmp_eq_u32_e32 vcc, v102, v144
	s_nop 1
	v_cndmask_b32_e64 v29, 0, 1.0, vcc
	v_cmp_eq_u32_e32 vcc, v103, v144
	s_waitcnt lgkmcnt(0)
	v_pk_fma_f32 v[22:23], v[26:27], v[22:23], v[28:29] op_sel_hi:[0,1,1] neg_lo:[1,0,0] neg_hi:[1,0,0]
	v_cvt_pk_bf16_f32 v22, v22, v23
	v_cndmask_b32_e64 v29, 0, 1.0, vcc
	v_cmp_eq_u32_e32 vcc, v104, v144
	s_nop 1
	v_cndmask_b32_e64 v28, 0, 1.0, vcc
	v_pk_fma_f32 v[24:25], v[26:27], v[24:25], v[28:29] op_sel_hi:[0,1,1] neg_lo:[1,0,0] neg_hi:[1,0,0]
	v_cvt_pk_bf16_f32 v23, v24, v25
	ds_write_b64 v186, v[22:23] offset:3264
	ds_read_b32 v22, v187 offset:120
	v_cmp_eq_u32_e32 vcc, v91, v145
	s_nop 1
	v_cndmask_b32_e64 v24, 0, 1.0, vcc
	v_cmp_eq_u32_e32 vcc, v102, v145
	s_nop 1
	v_cndmask_b32_e64 v25, 0, 1.0, vcc
	v_cmp_eq_u32_e32 vcc, v103, v145
	s_waitcnt lgkmcnt(0)
	v_pk_fma_f32 v[18:19], v[22:23], v[18:19], v[24:25] op_sel_hi:[0,1,1] neg_lo:[1,0,0] neg_hi:[1,0,0]
	v_cvt_pk_bf16_f32 v18, v18, v19
	v_cndmask_b32_e64 v25, 0, 1.0, vcc
	v_cmp_eq_u32_e32 vcc, v104, v145
	s_nop 1
	v_cndmask_b32_e64 v24, 0, 1.0, vcc
	v_pk_fma_f32 v[20:21], v[22:23], v[20:21], v[24:25] op_sel_hi:[0,1,1] neg_lo:[1,0,0] neg_hi:[1,0,0]
	v_cvt_pk_bf16_f32 v19, v20, v21
	ds_write_b64 v186, v[18:19] offset:3808
	ds_read_b128 v[18:21], v1
	ds_read_b128 v[22:25], v1 offset:64
	ds_read_b128 v[26:29], v1 offset:128
	ds_read_b128 v[30:33], v1 offset:192
	v_lshl_add_u64 v[66:67], v[150:151], 0, s[8:9]
	v_lshl_add_u64 v[68:69], v[152:153], 0, s[8:9]
	v_lshl_add_u64 v[70:71], v[156:157], 0, s[8:9]
	v_lshl_add_u64 v[72:73], v[158:159], 0, s[8:9]
	v_lshl_add_u64 v[74:75], v[160:161], 0, s[8:9]
	v_lshl_add_u64 v[76:77], v[162:163], 0, s[8:9]
	v_lshl_add_u64 v[134:135], v[164:165], 0, s[8:9]
	v_lshl_add_u64 v[136:137], v[166:167], 0, s[8:9]
	global_load_dwordx4 v[126:129], v[66:67], off sc0 sc1 nt
	global_load_dwordx4 v[114:117], v[68:69], off sc0 sc1 nt
	global_load_dwordx4 v[102:105], v[70:71], off sc0 sc1 nt
	global_load_dwordx4 v[90:93], v[72:73], off sc0 sc1 nt
	global_load_dwordx4 v[78:81], v[74:75], off sc0 sc1 nt
	s_nop 0
	global_load_dwordx4 v[74:77], v[76:77], off sc0 sc1 nt
	s_nop 0
	global_load_dwordx4 v[70:73], v[134:135], off sc0 sc1 nt
	global_load_dwordx4 v[66:69], v[136:137], off sc0 sc1 nt
	s_waitcnt vmcnt(23)
	s_waitcnt vmcnt(22)
	s_waitcnt vmcnt(21)
	s_waitcnt vmcnt(20)
	s_waitcnt vmcnt(19)
	s_waitcnt vmcnt(18)
	s_waitcnt vmcnt(17)
	s_waitcnt vmcnt(16)
	ds_read_b32 v134, v187 offset:128
	v_or_b32_e32 v194, 32, v132
	v_add_u32_e32 v135, 1, v133
	v_cmp_eq_u32_e32 vcc, v133, v194
	v_add_u32_e32 v202, 3, v133
	v_add_u32_e32 v203, 2, v133
	v_cndmask_b32_e64 v136, 0, 1.0, vcc
	v_cmp_eq_u32_e32 vcc, v135, v194
	v_or_b32_e32 v195, 34, v132
	v_or_b32_e32 v196, 36, v132
	v_cndmask_b32_e64 v137, 0, 1.0, vcc
	v_cmp_eq_u32_e32 vcc, v202, v194
	s_waitcnt lgkmcnt(0)
	v_pk_fma_f32 v[122:123], v[134:135], v[122:123], v[136:137] op_sel_hi:[0,1,1] neg_lo:[1,0,0] neg_hi:[1,0,0]
	v_cvt_pk_bf16_f32 v122, v122, v123
	v_cndmask_b32_e64 v137, 0, 1.0, vcc
	v_cmp_eq_u32_e32 vcc, v203, v194
	v_or_b32_e32 v197, 38, v132
	v_or_b32_e32 v198, 40, v132
	v_cndmask_b32_e64 v136, 0, 1.0, vcc
	v_pk_fma_f32 v[124:125], v[134:135], v[124:125], v[136:137] op_sel_hi:[0,1,1] neg_lo:[1,0,0] neg_hi:[1,0,0]
	v_cvt_pk_bf16_f32 v123, v124, v125
	ds_write_b64 v186, v[122:123]
	ds_read_b32 v122, v187 offset:136
	v_cmp_eq_u32_e32 vcc, v133, v195
	v_or_b32_e32 v199, 42, v132
	v_or_b32_e32 v200, 44, v132
	v_cndmask_b32_e64 v124, 0, 1.0, vcc
	v_cmp_eq_u32_e32 vcc, v135, v195
	v_or_b32_e32 v201, 46, v132
	s_nop 0
	v_cndmask_b32_e64 v125, 0, 1.0, vcc
	v_cmp_eq_u32_e32 vcc, v202, v195
	s_waitcnt lgkmcnt(0)
	v_pk_fma_f32 v[106:107], v[122:123], v[106:107], v[124:125] op_sel_hi:[0,1,1] neg_lo:[1,0,0] neg_hi:[1,0,0]
	v_cvt_pk_bf16_f32 v106, v106, v107
	v_cndmask_b32_e64 v125, 0, 1.0, vcc
	v_cmp_eq_u32_e32 vcc, v203, v195
	s_nop 1
	v_cndmask_b32_e64 v124, 0, 1.0, vcc
	v_pk_fma_f32 v[108:109], v[122:123], v[108:109], v[124:125] op_sel_hi:[0,1,1] neg_lo:[1,0,0] neg_hi:[1,0,0]
	v_cvt_pk_bf16_f32 v107, v108, v109
	ds_write_b64 v186, v[106:107] offset:544
	ds_read_b32 v106, v187 offset:144
	v_cmp_eq_u32_e32 vcc, v133, v196
	s_nop 1
	v_cndmask_b32_e64 v108, 0, 1.0, vcc
	v_cmp_eq_u32_e32 vcc, v135, v196
	s_nop 1
	v_cndmask_b32_e64 v109, 0, 1.0, vcc
	v_cmp_eq_u32_e32 vcc, v202, v196
	s_waitcnt lgkmcnt(0)
	v_pk_fma_f32 v[94:95], v[106:107], v[94:95], v[108:109] op_sel_hi:[0,1,1] neg_lo:[1,0,0] neg_hi:[1,0,0]
	v_cvt_pk_bf16_f32 v94, v94, v95
	v_cndmask_b32_e64 v109, 0, 1.0, vcc
	v_cmp_eq_u32_e32 vcc, v203, v196
	s_nop 1
	v_cndmask_b32_e64 v108, 0, 1.0, vcc
	v_pk_fma_f32 v[96:97], v[106:107], v[96:97], v[108:109] op_sel_hi:[0,1,1] neg_lo:[1,0,0] neg_hi:[1,0,0]
	v_cvt_pk_bf16_f32 v95, v96, v97
	ds_write_b64 v186, v[94:95] offset:1088
	ds_read_b32 v94, v187 offset:152
	v_cmp_eq_u32_e32 vcc, v133, v197
	s_nop 1
	v_cndmask_b32_e64 v96, 0, 1.0, vcc
	v_cmp_eq_u32_e32 vcc, v135, v197
	s_nop 1
	v_cndmask_b32_e64 v97, 0, 1.0, vcc
	v_cmp_eq_u32_e32 vcc, v202, v197
	s_waitcnt lgkmcnt(0)
	v_pk_fma_f32 v[82:83], v[94:95], v[82:83], v[96:97] op_sel_hi:[0,1,1] neg_lo:[1,0,0] neg_hi:[1,0,0]
	v_cvt_pk_bf16_f32 v82, v82, v83
	v_cndmask_b32_e64 v97, 0, 1.0, vcc
	v_cmp_eq_u32_e32 vcc, v203, v197
	s_nop 1
	v_cndmask_b32_e64 v96, 0, 1.0, vcc
	v_pk_fma_f32 v[84:85], v[94:95], v[84:85], v[96:97] op_sel_hi:[0,1,1] neg_lo:[1,0,0] neg_hi:[1,0,0]
	v_cvt_pk_bf16_f32 v83, v84, v85
	ds_write_b64 v186, v[82:83] offset:1632
	ds_read_b32 v82, v187 offset:160
	v_cmp_eq_u32_e32 vcc, v133, v198
	s_nop 1
	v_cndmask_b32_e64 v84, 0, 1.0, vcc
	v_cmp_eq_u32_e32 vcc, v135, v198
	s_nop 1
	v_cndmask_b32_e64 v85, 0, 1.0, vcc
	v_cmp_eq_u32_e32 vcc, v202, v198
	s_waitcnt lgkmcnt(0)
	v_pk_fma_f32 v[46:47], v[82:83], v[46:47], v[84:85] op_sel_hi:[0,1,1] neg_lo:[1,0,0] neg_hi:[1,0,0]
	v_cvt_pk_bf16_f32 v46, v46, v47
	v_cndmask_b32_e64 v85, 0, 1.0, vcc
	v_cmp_eq_u32_e32 vcc, v203, v198
	s_nop 1
	v_cndmask_b32_e64 v84, 0, 1.0, vcc
	v_pk_fma_f32 v[48:49], v[82:83], v[48:49], v[84:85] op_sel_hi:[0,1,1] neg_lo:[1,0,0] neg_hi:[1,0,0]
	v_cvt_pk_bf16_f32 v47, v48, v49
	ds_write_b64 v186, v[46:47] offset:2176
	ds_read_b32 v46, v187 offset:168
	v_cmp_eq_u32_e32 vcc, v133, v199
	s_nop 1
	v_cndmask_b32_e64 v48, 0, 1.0, vcc
	v_cmp_eq_u32_e32 vcc, v135, v199
	s_nop 1
	v_cndmask_b32_e64 v49, 0, 1.0, vcc
	v_cmp_eq_u32_e32 vcc, v202, v199
	s_waitcnt lgkmcnt(0)
	v_pk_fma_f32 v[42:43], v[46:47], v[42:43], v[48:49] op_sel_hi:[0,1,1] neg_lo:[1,0,0] neg_hi:[1,0,0]
	v_cvt_pk_bf16_f32 v42, v42, v43
	v_cndmask_b32_e64 v49, 0, 1.0, vcc
	v_cmp_eq_u32_e32 vcc, v203, v199
	s_nop 1
	v_cndmask_b32_e64 v48, 0, 1.0, vcc
	v_pk_fma_f32 v[44:45], v[46:47], v[44:45], v[48:49] op_sel_hi:[0,1,1] neg_lo:[1,0,0] neg_hi:[1,0,0]
	v_cvt_pk_bf16_f32 v43, v44, v45
	ds_write_b64 v186, v[42:43] offset:2720
	ds_read_b32 v42, v187 offset:176
	v_cmp_eq_u32_e32 vcc, v133, v200
	s_nop 1
	v_cndmask_b32_e64 v44, 0, 1.0, vcc
	v_cmp_eq_u32_e32 vcc, v135, v200
	s_nop 1
	v_cndmask_b32_e64 v45, 0, 1.0, vcc
	v_cmp_eq_u32_e32 vcc, v202, v200
	s_waitcnt lgkmcnt(0)
	v_pk_fma_f32 v[38:39], v[42:43], v[38:39], v[44:45] op_sel_hi:[0,1,1] neg_lo:[1,0,0] neg_hi:[1,0,0]
	v_cvt_pk_bf16_f32 v38, v38, v39
	v_cndmask_b32_e64 v45, 0, 1.0, vcc
	v_cmp_eq_u32_e32 vcc, v203, v200
	s_nop 1
	v_cndmask_b32_e64 v44, 0, 1.0, vcc
	v_pk_fma_f32 v[40:41], v[42:43], v[40:41], v[44:45] op_sel_hi:[0,1,1] neg_lo:[1,0,0] neg_hi:[1,0,0]
	v_cvt_pk_bf16_f32 v39, v40, v41
	ds_write_b64 v186, v[38:39] offset:3264
	ds_read_b32 v38, v187 offset:184
	v_cmp_eq_u32_e32 vcc, v133, v201
	s_nop 1
	v_cndmask_b32_e64 v40, 0, 1.0, vcc
	v_cmp_eq_u32_e32 vcc, v135, v201
	s_nop 1
	v_cndmask_b32_e64 v41, 0, 1.0, vcc
	v_cmp_eq_u32_e32 vcc, v202, v201
	s_waitcnt lgkmcnt(0)
	v_pk_fma_f32 v[34:35], v[38:39], v[34:35], v[40:41] op_sel_hi:[0,1,1] neg_lo:[1,0,0] neg_hi:[1,0,0]
	v_cvt_pk_bf16_f32 v34, v34, v35
	v_cndmask_b32_e64 v41, 0, 1.0, vcc
	v_cmp_eq_u32_e32 vcc, v203, v201
	s_nop 1
	v_cndmask_b32_e64 v40, 0, 1.0, vcc
	v_pk_fma_f32 v[36:37], v[38:39], v[36:37], v[40:41] op_sel_hi:[0,1,1] neg_lo:[1,0,0] neg_hi:[1,0,0]
	v_cvt_pk_bf16_f32 v35, v36, v37
	ds_write_b64 v186, v[34:35] offset:3808
	ds_read_b128 v[34:37], v1
	ds_read_b128 v[38:41], v1 offset:64
	ds_read_b128 v[42:45], v1 offset:128
	ds_read_b128 v[46:49], v1 offset:192
	v_mov_b32_e32 v106, v189
	s_waitcnt vmcnt(15)
	s_waitcnt vmcnt(14)
	s_waitcnt vmcnt(13)
	s_waitcnt vmcnt(12)
	s_waitcnt vmcnt(11)
	s_waitcnt vmcnt(10)
	s_waitcnt vmcnt(9)
	s_waitcnt vmcnt(8)
	ds_read_b32 v82, v187
	v_add_u32_e32 v107, 1, v106
	v_cmp_eq_u32_e32 vcc, v106, v132
	v_add_u32_e32 v108, 3, v106
	v_add_u32_e32 v109, 2, v106
	v_cndmask_b32_e64 v84, 0, 1.0, vcc
	v_cmp_eq_u32_e32 vcc, v107, v132
	s_nop 1
	v_cndmask_b32_e64 v85, 0, 1.0, vcc
	v_cmp_eq_u32_e32 vcc, v108, v132
	s_waitcnt lgkmcnt(0)
	v_pk_fma_f32 v[94:95], v[82:83], v[118:119], v[84:85] op_sel_hi:[0,1,1] neg_lo:[1,0,0] neg_hi:[1,0,0]
	v_cvt_pk_bf16_f32 v94, v94, v95
	v_cndmask_b32_e64 v97, 0, 1.0, vcc
	v_cmp_eq_u32_e32 vcc, v109, v132
	s_nop 1
	v_cndmask_b32_e64 v96, 0, 1.0, vcc
	v_pk_fma_f32 v[82:83], v[82:83], v[120:121], v[96:97] op_sel_hi:[0,1,1] neg_lo:[1,0,0] neg_hi:[1,0,0]
	v_cvt_pk_bf16_f32 v95, v82, v83
	ds_write_b64 v186, v[94:95]
	ds_read_b32 v82, v187 offset:8
	v_cmp_eq_u32_e32 vcc, v106, v193
	s_nop 1
	v_cndmask_b32_e64 v94, 0, 1.0, vcc
	v_cmp_eq_u32_e32 vcc, v107, v193
	s_nop 1
	v_cndmask_b32_e64 v95, 0, 1.0, vcc
	v_cmp_eq_u32_e32 vcc, v108, v193
	s_waitcnt lgkmcnt(0)
	v_pk_fma_f32 v[94:95], v[82:83], v[110:111], v[94:95] op_sel_hi:[0,1,1] neg_lo:[1,0,0] neg_hi:[1,0,0]
	v_cvt_pk_bf16_f32 v94, v94, v95
	v_cndmask_b32_e64 v85, 0, 1.0, vcc
	v_pk_fma_f32 v[82:83], v[82:83], v[112:113], v[84:85] op_sel_hi:[0,1,1] neg_lo:[1,0,0] neg_hi:[1,0,0]
	v_cvt_pk_bf16_f32 v95, v82, v83
	ds_write_b64 v186, v[94:95] offset:544
	ds_read_b32 v82, v187 offset:16
	v_cmp_eq_u32_e32 vcc, v106, v192
	s_nop 1
	v_cndmask_b32_e64 v84, 0, 1.0, vcc
	v_cmp_eq_u32_e32 vcc, v107, v192
	s_nop 1
	v_cndmask_b32_e64 v85, 0, 1.0, vcc
	v_cmp_eq_u32_e32 vcc, v108, v192
	s_waitcnt lgkmcnt(0)
	v_pk_fma_f32 v[84:85], v[82:83], v[98:99], v[84:85] op_sel_hi:[0,1,1] neg_lo:[1,0,0] neg_hi:[1,0,0]
	v_cvt_pk_bf16_f32 v84, v84, v85
	v_cndmask_b32_e64 v95, 0, 1.0, vcc
	v_cmp_eq_u32_e32 vcc, v109, v192
	s_nop 1
	v_cndmask_b32_e64 v94, 0, 1.0, vcc
	v_pk_fma_f32 v[82:83], v[82:83], v[100:101], v[94:95] op_sel_hi:[0,1,1] neg_lo:[1,0,0] neg_hi:[1,0,0]
	v_cvt_pk_bf16_f32 v85, v82, v83
	ds_write_b64 v186, v[84:85] offset:1088
	ds_read_b32 v82, v187 offset:24
	v_cmp_eq_u32_e32 vcc, v106, v190
	s_nop 1
	v_cndmask_b32_e64 v84, 0, 1.0, vcc
	v_cmp_eq_u32_e32 vcc, v107, v190
	s_nop 1
	v_cndmask_b32_e64 v85, 0, 1.0, vcc
	v_cmp_eq_u32_e32 vcc, v108, v190
	s_waitcnt lgkmcnt(0)
	v_pk_fma_f32 v[84:85], v[82:83], v[86:87], v[84:85] op_sel_hi:[0,1,1] neg_lo:[1,0,0] neg_hi:[1,0,0]
	v_cvt_pk_bf16_f32 v84, v84, v85
	v_cndmask_b32_e64 v87, 0, 1.0, vcc
	v_cmp_eq_u32_e32 vcc, v109, v190
	s_nop 1
	v_cndmask_b32_e64 v86, 0, 1.0, vcc
	v_pk_fma_f32 v[82:83], v[82:83], v[88:89], v[86:87] op_sel_hi:[0,1,1] neg_lo:[1,0,0] neg_hi:[1,0,0]
	v_cvt_pk_bf16_f32 v85, v82, v83
	ds_write_b64 v186, v[84:85] offset:1632
	ds_read_b32 v82, v187 offset:32
	v_cmp_eq_u32_e32 vcc, v106, v149
	s_nop 1
	v_cndmask_b32_e64 v84, 0, 1.0, vcc
	v_cmp_eq_u32_e32 vcc, v107, v149
	s_nop 1
	v_cndmask_b32_e64 v85, 0, 1.0, vcc
	v_cmp_eq_u32_e32 vcc, v108, v149
	s_waitcnt lgkmcnt(0)
	v_pk_fma_f32 v[62:63], v[82:83], v[62:63], v[84:85] op_sel_hi:[0,1,1] neg_lo:[1,0,0] neg_hi:[1,0,0]
	v_cvt_pk_bf16_f32 v62, v62, v63
	v_cndmask_b32_e64 v85, 0, 1.0, vcc
	v_cmp_eq_u32_e32 vcc, v109, v149
	s_nop 1
	v_cndmask_b32_e64 v84, 0, 1.0, vcc
	v_pk_fma_f32 v[64:65], v[82:83], v[64:65], v[84:85] op_sel_hi:[0,1,1] neg_lo:[1,0,0] neg_hi:[1,0,0]
	v_cvt_pk_bf16_f32 v63, v64, v65
	ds_write_b64 v186, v[62:63] offset:2176
	ds_read_b32 v62, v187 offset:40
	v_cmp_eq_u32_e32 vcc, v106, v148
	s_nop 1
	v_cndmask_b32_e64 v64, 0, 1.0, vcc
	v_cmp_eq_u32_e32 vcc, v107, v148
	s_nop 1
	v_cndmask_b32_e64 v65, 0, 1.0, vcc
	v_cmp_eq_u32_e32 vcc, v108, v148
	s_waitcnt lgkmcnt(0)
	v_pk_fma_f32 v[58:59], v[62:63], v[58:59], v[64:65] op_sel_hi:[0,1,1] neg_lo:[1,0,0] neg_hi:[1,0,0]
	v_cvt_pk_bf16_f32 v58, v58, v59
	v_cndmask_b32_e64 v65, 0, 1.0, vcc
	v_cmp_eq_u32_e32 vcc, v109, v148
	s_nop 1
	v_cndmask_b32_e64 v64, 0, 1.0, vcc
	v_pk_fma_f32 v[60:61], v[62:63], v[60:61], v[64:65] op_sel_hi:[0,1,1] neg_lo:[1,0,0] neg_hi:[1,0,0]
	v_cvt_pk_bf16_f32 v59, v60, v61
	ds_write_b64 v186, v[58:59] offset:2720
	ds_read_b32 v58, v187 offset:48
	v_cmp_eq_u32_e32 vcc, v106, v147
	s_nop 1
	v_cndmask_b32_e64 v60, 0, 1.0, vcc
	v_cmp_eq_u32_e32 vcc, v107, v147
	s_nop 1
	v_cndmask_b32_e64 v61, 0, 1.0, vcc
	v_cmp_eq_u32_e32 vcc, v108, v147
	s_waitcnt lgkmcnt(0)
	v_pk_fma_f32 v[54:55], v[58:59], v[54:55], v[60:61] op_sel_hi:[0,1,1] neg_lo:[1,0,0] neg_hi:[1,0,0]
	v_cvt_pk_bf16_f32 v54, v54, v55
	v_cndmask_b32_e64 v61, 0, 1.0, vcc
	v_cmp_eq_u32_e32 vcc, v109, v147
	s_nop 1
	v_cndmask_b32_e64 v60, 0, 1.0, vcc
	v_pk_fma_f32 v[56:57], v[58:59], v[56:57], v[60:61] op_sel_hi:[0,1,1] neg_lo:[1,0,0] neg_hi:[1,0,0]
	v_cvt_pk_bf16_f32 v55, v56, v57
	ds_write_b64 v186, v[54:55] offset:3264
	ds_read_b32 v54, v187 offset:56
	v_cmp_eq_u32_e32 vcc, v106, v146
	s_nop 1
	v_cndmask_b32_e64 v56, 0, 1.0, vcc
	v_cmp_eq_u32_e32 vcc, v107, v146
	s_nop 1
	v_cndmask_b32_e64 v57, 0, 1.0, vcc
	v_cmp_eq_u32_e32 vcc, v108, v146
	s_waitcnt lgkmcnt(0)
	v_pk_fma_f32 v[50:51], v[54:55], v[50:51], v[56:57] op_sel_hi:[0,1,1] neg_lo:[1,0,0] neg_hi:[1,0,0]
	v_cvt_pk_bf16_f32 v50, v50, v51
	v_cndmask_b32_e64 v57, 0, 1.0, vcc
	v_cmp_eq_u32_e32 vcc, v109, v146
	s_nop 1
	v_cndmask_b32_e64 v56, 0, 1.0, vcc
	v_pk_fma_f32 v[52:53], v[54:55], v[52:53], v[56:57] op_sel_hi:[0,1,1] neg_lo:[1,0,0] neg_hi:[1,0,0]
	v_cvt_pk_bf16_f32 v51, v52, v53
	ds_write_b64 v186, v[50:51] offset:3808
	ds_read_b128 v[50:53], v1
	ds_read_b128 v[54:57], v1 offset:64
	ds_read_b128 v[58:61], v1 offset:128
	ds_read_b128 v[62:65], v1 offset:192
	v_lshl_add_u64 v[82:83], v[168:169], 0, s[8:9]
	v_lshl_add_u64 v[84:85], v[170:171], 0, s[8:9]
	v_lshl_add_u64 v[86:87], v[172:173], 0, s[8:9]
	v_lshl_add_u64 v[88:89], v[174:175], 0, s[8:9]
	v_lshl_add_u64 v[94:95], v[176:177], 0, s[8:9]
	v_lshl_add_u64 v[96:97], v[178:179], 0, s[8:9]
	v_lshl_add_u64 v[122:123], v[180:181], 0, s[8:9]
	v_lshl_add_u64 v[124:125], v[182:183], 0, s[8:9]
	global_load_dwordx4 v[134:137], v[82:83], off sc0 sc1 nt
	global_load_dwordx4 v[118:121], v[84:85], off sc0 sc1 nt
	global_load_dwordx4 v[110:113], v[86:87], off sc0 sc1 nt
	global_load_dwordx4 v[106:109], v[88:89], off sc0 sc1 nt
	global_load_dwordx4 v[98:101], v[94:95], off sc0 sc1 nt
	s_nop 0
	global_load_dwordx4 v[94:97], v[96:97], off sc0 sc1 nt
	s_nop 0
	global_load_dwordx4 v[86:89], v[122:123], off sc0 sc1 nt
	global_load_dwordx4 v[82:85], v[124:125], off sc0 sc1 nt
	v_mov_b32_e32 v132, v189
	s_waitcnt vmcnt(15)
	s_waitcnt vmcnt(14)
	s_waitcnt vmcnt(13)
	s_waitcnt vmcnt(12)
	s_waitcnt vmcnt(11)
	s_waitcnt vmcnt(10)
	s_waitcnt vmcnt(9)
	s_waitcnt vmcnt(8)
	ds_read_b32 v122, v187 offset:64
	v_add_u32_e32 v133, 1, v132
	v_cmp_eq_u32_e32 vcc, v132, v138
	v_add_u32_e32 v146, 3, v132
	v_add_u32_e32 v147, 2, v132
	v_cndmask_b32_e64 v124, 0, 1.0, vcc
	v_cmp_eq_u32_e32 vcc, v133, v138
	s_nop 1
	v_cndmask_b32_e64 v125, 0, 1.0, vcc
	v_cmp_eq_u32_e32 vcc, v146, v138
	s_waitcnt lgkmcnt(0)
	v_pk_fma_f32 v[124:125], v[122:123], v[126:127], v[124:125] op_sel_hi:[0,1,1] neg_lo:[1,0,0] neg_hi:[1,0,0]
	v_cvt_pk_bf16_f32 v124, v124, v125
	v_cndmask_b32_e64 v127, 0, 1.0, vcc
	v_cmp_eq_u32_e32 vcc, v147, v138
	s_nop 1
	v_cndmask_b32_e64 v126, 0, 1.0, vcc
	v_pk_fma_f32 v[122:123], v[122:123], v[128:129], v[126:127] op_sel_hi:[0,1,1] neg_lo:[1,0,0] neg_hi:[1,0,0]
	v_cvt_pk_bf16_f32 v125, v122, v123
	ds_write_b64 v186, v[124:125]
	ds_read_b32 v122, v187 offset:72
	v_cmp_eq_u32_e32 vcc, v132, v139
	s_nop 1
	v_cndmask_b32_e64 v124, 0, 1.0, vcc
	v_cmp_eq_u32_e32 vcc, v133, v139
	s_nop 1
	v_cndmask_b32_e64 v125, 0, 1.0, vcc
	v_cmp_eq_u32_e32 vcc, v146, v139
	s_waitcnt lgkmcnt(0)
	v_pk_fma_f32 v[114:115], v[122:123], v[114:115], v[124:125] op_sel_hi:[0,1,1] neg_lo:[1,0,0] neg_hi:[1,0,0]
	v_cvt_pk_bf16_f32 v114, v114, v115
	v_cndmask_b32_e64 v125, 0, 1.0, vcc
	v_cmp_eq_u32_e32 vcc, v147, v139
	s_nop 1
	v_cndmask_b32_e64 v124, 0, 1.0, vcc
	v_pk_fma_f32 v[116:117], v[122:123], v[116:117], v[124:125] op_sel_hi:[0,1,1] neg_lo:[1,0,0] neg_hi:[1,0,0]
	v_cvt_pk_bf16_f32 v115, v116, v117
	ds_write_b64 v186, v[114:115] offset:544
	ds_read_b32 v114, v187 offset:80
	v_cmp_eq_u32_e32 vcc, v132, v140
	s_nop 1
	v_cndmask_b32_e64 v116, 0, 1.0, vcc
	v_cmp_eq_u32_e32 vcc, v133, v140
	s_nop 1
	v_cndmask_b32_e64 v117, 0, 1.0, vcc
	v_cmp_eq_u32_e32 vcc, v146, v140
	s_waitcnt lgkmcnt(0)
	v_pk_fma_f32 v[102:103], v[114:115], v[102:103], v[116:117] op_sel_hi:[0,1,1] neg_lo:[1,0,0] neg_hi:[1,0,0]
	v_cvt_pk_bf16_f32 v102, v102, v103
	v_cndmask_b32_e64 v117, 0, 1.0, vcc
	v_cmp_eq_u32_e32 vcc, v147, v140
	s_nop 1
	v_cndmask_b32_e64 v116, 0, 1.0, vcc
	v_pk_fma_f32 v[104:105], v[114:115], v[104:105], v[116:117] op_sel_hi:[0,1,1] neg_lo:[1,0,0] neg_hi:[1,0,0]
	v_cvt_pk_bf16_f32 v103, v104, v105
	ds_write_b64 v186, v[102:103] offset:1088
	ds_read_b32 v102, v187 offset:88
	v_cmp_eq_u32_e32 vcc, v132, v141
	s_nop 1
	v_cndmask_b32_e64 v104, 0, 1.0, vcc
	v_cmp_eq_u32_e32 vcc, v133, v141
	s_nop 1
	v_cndmask_b32_e64 v105, 0, 1.0, vcc
	v_cmp_eq_u32_e32 vcc, v146, v141
	s_waitcnt lgkmcnt(0)
	v_pk_fma_f32 v[90:91], v[102:103], v[90:91], v[104:105] op_sel_hi:[0,1,1] neg_lo:[1,0,0] neg_hi:[1,0,0]
	v_cvt_pk_bf16_f32 v90, v90, v91
	v_cndmask_b32_e64 v105, 0, 1.0, vcc
	v_cmp_eq_u32_e32 vcc, v147, v141
	s_nop 1
	v_cndmask_b32_e64 v104, 0, 1.0, vcc
	v_pk_fma_f32 v[92:93], v[102:103], v[92:93], v[104:105] op_sel_hi:[0,1,1] neg_lo:[1,0,0] neg_hi:[1,0,0]
	v_cvt_pk_bf16_f32 v91, v92, v93
	ds_write_b64 v186, v[90:91] offset:1632
	ds_read_b32 v90, v187 offset:96
	v_cmp_eq_u32_e32 vcc, v132, v142
	s_nop 1
	v_cndmask_b32_e64 v92, 0, 1.0, vcc
	v_cmp_eq_u32_e32 vcc, v133, v142
	s_nop 1
	v_cndmask_b32_e64 v93, 0, 1.0, vcc
	v_cmp_eq_u32_e32 vcc, v146, v142
	s_waitcnt lgkmcnt(0)
	v_pk_fma_f32 v[78:79], v[90:91], v[78:79], v[92:93] op_sel_hi:[0,1,1] neg_lo:[1,0,0] neg_hi:[1,0,0]
	v_cvt_pk_bf16_f32 v78, v78, v79
	v_cndmask_b32_e64 v93, 0, 1.0, vcc
	v_cmp_eq_u32_e32 vcc, v147, v142
	s_nop 1
	v_cndmask_b32_e64 v92, 0, 1.0, vcc
	v_pk_fma_f32 v[80:81], v[90:91], v[80:81], v[92:93] op_sel_hi:[0,1,1] neg_lo:[1,0,0] neg_hi:[1,0,0]
	v_cvt_pk_bf16_f32 v79, v80, v81
	ds_write_b64 v186, v[78:79] offset:2176
	ds_read_b32 v78, v187 offset:104
	v_cmp_eq_u32_e32 vcc, v132, v143
	s_nop 1
	v_cndmask_b32_e64 v80, 0, 1.0, vcc
	v_cmp_eq_u32_e32 vcc, v133, v143
	s_nop 1
	v_cndmask_b32_e64 v81, 0, 1.0, vcc
	v_cmp_eq_u32_e32 vcc, v146, v143
	s_waitcnt lgkmcnt(0)
	v_pk_fma_f32 v[74:75], v[78:79], v[74:75], v[80:81] op_sel_hi:[0,1,1] neg_lo:[1,0,0] neg_hi:[1,0,0]
	v_cvt_pk_bf16_f32 v74, v74, v75
	v_cndmask_b32_e64 v81, 0, 1.0, vcc
	v_cmp_eq_u32_e32 vcc, v147, v143
	s_nop 1
	v_cndmask_b32_e64 v80, 0, 1.0, vcc
	v_pk_fma_f32 v[76:77], v[78:79], v[76:77], v[80:81] op_sel_hi:[0,1,1] neg_lo:[1,0,0] neg_hi:[1,0,0]
	v_cvt_pk_bf16_f32 v75, v76, v77
	ds_write_b64 v186, v[74:75] offset:2720
	ds_read_b32 v74, v187 offset:112
	v_cmp_eq_u32_e32 vcc, v132, v144
	s_nop 1
	v_cndmask_b32_e64 v76, 0, 1.0, vcc
	v_cmp_eq_u32_e32 vcc, v133, v144
	s_nop 1
	v_cndmask_b32_e64 v77, 0, 1.0, vcc
	v_cmp_eq_u32_e32 vcc, v146, v144
	s_waitcnt lgkmcnt(0)
	v_pk_fma_f32 v[70:71], v[74:75], v[70:71], v[76:77] op_sel_hi:[0,1,1] neg_lo:[1,0,0] neg_hi:[1,0,0]
	v_cvt_pk_bf16_f32 v70, v70, v71
	v_cndmask_b32_e64 v77, 0, 1.0, vcc
	v_cmp_eq_u32_e32 vcc, v147, v144
	s_nop 1
	v_cndmask_b32_e64 v76, 0, 1.0, vcc
	v_pk_fma_f32 v[72:73], v[74:75], v[72:73], v[76:77] op_sel_hi:[0,1,1] neg_lo:[1,0,0] neg_hi:[1,0,0]
	v_cvt_pk_bf16_f32 v71, v72, v73
	ds_write_b64 v186, v[70:71] offset:3264
	ds_read_b32 v70, v187 offset:120
	v_cmp_eq_u32_e32 vcc, v132, v145
	s_nop 1
	v_cndmask_b32_e64 v72, 0, 1.0, vcc
	v_cmp_eq_u32_e32 vcc, v133, v145
	s_nop 1
	v_cndmask_b32_e64 v73, 0, 1.0, vcc
	v_cmp_eq_u32_e32 vcc, v146, v145
	s_waitcnt lgkmcnt(0)
	v_pk_fma_f32 v[66:67], v[70:71], v[66:67], v[72:73] op_sel_hi:[0,1,1] neg_lo:[1,0,0] neg_hi:[1,0,0]
	v_cvt_pk_bf16_f32 v66, v66, v67
	v_cndmask_b32_e64 v73, 0, 1.0, vcc
	v_cmp_eq_u32_e32 vcc, v147, v145
	s_nop 1
	v_cndmask_b32_e64 v72, 0, 1.0, vcc
	v_pk_fma_f32 v[68:69], v[70:71], v[68:69], v[72:73] op_sel_hi:[0,1,1] neg_lo:[1,0,0] neg_hi:[1,0,0]
	v_cvt_pk_bf16_f32 v67, v68, v69
	ds_write_b64 v186, v[66:67] offset:3808
	ds_read_b128 v[66:69], v1
	ds_read_b128 v[70:73], v1 offset:64
	ds_read_b128 v[74:77], v1 offset:128
	ds_read_b128 v[78:81], v1 offset:192
	v_lshl_add_u64 v[90:91], v[130:131], 0, s[0:1]
	v_add_co_u32_e32 v92, vcc, s7, v90
	s_nop 1
	v_addc_co_u32_e32 v93, vcc, 0, v91, vcc
	global_load_dwordx4 v[146:149], v[90:91], off sc0 sc1 nt
	global_load_dwordx4 v[142:145], v[92:93], off sc0 sc1 nt
	v_add_co_u32_e32 v92, vcc, s36, v90
	s_nop 1
	v_addc_co_u32_e32 v93, vcc, 0, v91, vcc
	v_add_co_u32_e32 v102, vcc, s37, v90
	s_nop 1
	v_addc_co_u32_e32 v103, vcc, 0, v91, vcc
	global_load_dwordx4 v[138:141], v[92:93], off sc0 sc1 nt
	global_load_dwordx4 v[130:133], v[102:103], off sc0 sc1 nt
	v_add_co_u32_e32 v92, vcc, s38, v90
	s_nop 1
	v_addc_co_u32_e32 v93, vcc, 0, v91, vcc
	v_add_co_u32_e32 v102, vcc, s39, v90
	s_nop 1
	v_addc_co_u32_e32 v103, vcc, 0, v91, vcc
	global_load_dwordx4 v[126:129], v[92:93], off sc0 sc1 nt
	global_load_dwordx4 v[122:125], v[102:103], off sc0 sc1 nt
	v_add_co_u32_e32 v92, vcc, s41, v90
	s_nop 1
	v_addc_co_u32_e32 v93, vcc, 0, v91, vcc
	v_add_co_u32_e32 v90, vcc, s42, v90
	s_nop 1
	v_addc_co_u32_e32 v91, vcc, 0, v91, vcc
	global_load_dwordx4 v[114:117], v[92:93], off sc0 sc1 nt
	global_load_dwordx4 v[102:105], v[90:91], off sc0 sc1 nt
	s_waitcnt vmcnt(15)
	s_waitcnt vmcnt(14)
	s_waitcnt vmcnt(13)
	s_waitcnt vmcnt(12)
	s_waitcnt vmcnt(11)
	s_waitcnt vmcnt(10)
	s_waitcnt vmcnt(9)
	s_waitcnt vmcnt(8)
	ds_read_b32 v90, v187 offset:128
	v_add_u32_e32 v190, 1, v189
	v_cmp_eq_u32_e32 vcc, v189, v194
	v_add_u32_e32 v192, 3, v189
	v_add_u32_e32 v193, 2, v189
	v_cndmask_b32_e64 v92, 0, 1.0, vcc
	v_cmp_eq_u32_e32 vcc, v190, v194
	s_nop 1
	v_cndmask_b32_e64 v93, 0, 1.0, vcc
	v_cmp_eq_u32_e32 vcc, v192, v194
	s_waitcnt lgkmcnt(0)
	v_pk_fma_f32 v[92:93], v[90:91], v[134:135], v[92:93] op_sel_hi:[0,1,1] neg_lo:[1,0,0] neg_hi:[1,0,0]
	v_cvt_pk_bf16_f32 v92, v92, v93
	v_cndmask_b32_e64 v135, 0, 1.0, vcc
	v_cmp_eq_u32_e32 vcc, v193, v194
	s_nop 1
	v_cndmask_b32_e64 v134, 0, 1.0, vcc
	v_pk_fma_f32 v[90:91], v[90:91], v[136:137], v[134:135] op_sel_hi:[0,1,1] neg_lo:[1,0,0] neg_hi:[1,0,0]
	v_cvt_pk_bf16_f32 v93, v90, v91
	ds_write_b64 v186, v[92:93]
	ds_read_b32 v90, v187 offset:136
	v_cmp_eq_u32_e32 vcc, v189, v195
	s_nop 1
	v_cndmask_b32_e64 v92, 0, 1.0, vcc
	v_cmp_eq_u32_e32 vcc, v190, v195
	s_nop 1
	v_cndmask_b32_e64 v93, 0, 1.0, vcc
	v_cmp_eq_u32_e32 vcc, v192, v195
	s_waitcnt lgkmcnt(0)
	v_pk_fma_f32 v[92:93], v[90:91], v[118:119], v[92:93] op_sel_hi:[0,1,1] neg_lo:[1,0,0] neg_hi:[1,0,0]
	v_cvt_pk_bf16_f32 v92, v92, v93
	v_cndmask_b32_e64 v119, 0, 1.0, vcc
	v_cmp_eq_u32_e32 vcc, v193, v195
	s_nop 1
	v_cndmask_b32_e64 v118, 0, 1.0, vcc
	v_pk_fma_f32 v[90:91], v[90:91], v[120:121], v[118:119] op_sel_hi:[0,1,1] neg_lo:[1,0,0] neg_hi:[1,0,0]
	v_cvt_pk_bf16_f32 v93, v90, v91
	ds_write_b64 v186, v[92:93] offset:544
	ds_read_b32 v90, v187 offset:144
	v_cmp_eq_u32_e32 vcc, v189, v196
	s_nop 1
	v_cndmask_b32_e64 v92, 0, 1.0, vcc
	v_cmp_eq_u32_e32 vcc, v190, v196
	s_nop 1
	v_cndmask_b32_e64 v93, 0, 1.0, vcc
	v_cmp_eq_u32_e32 vcc, v192, v196
	s_waitcnt lgkmcnt(0)
	v_pk_fma_f32 v[92:93], v[90:91], v[110:111], v[92:93] op_sel_hi:[0,1,1] neg_lo:[1,0,0] neg_hi:[1,0,0]
	v_cvt_pk_bf16_f32 v92, v92, v93
	v_cndmask_b32_e64 v111, 0, 1.0, vcc
	v_cmp_eq_u32_e32 vcc, v193, v196
	s_nop 1
	v_cndmask_b32_e64 v110, 0, 1.0, vcc
	v_pk_fma_f32 v[90:91], v[90:91], v[112:113], v[110:111] op_sel_hi:[0,1,1] neg_lo:[1,0,0] neg_hi:[1,0,0]
	v_cvt_pk_bf16_f32 v93, v90, v91
	ds_write_b64 v186, v[92:93] offset:1088
	ds_read_b32 v90, v187 offset:152
	v_cmp_eq_u32_e32 vcc, v189, v197
	s_nop 1
	v_cndmask_b32_e64 v92, 0, 1.0, vcc
	v_cmp_eq_u32_e32 vcc, v190, v197
	s_nop 1
	v_cndmask_b32_e64 v93, 0, 1.0, vcc
	v_cmp_eq_u32_e32 vcc, v192, v197
	s_waitcnt lgkmcnt(0)
	v_pk_fma_f32 v[92:93], v[90:91], v[106:107], v[92:93] op_sel_hi:[0,1,1] neg_lo:[1,0,0] neg_hi:[1,0,0]
	v_cvt_pk_bf16_f32 v92, v92, v93
	v_cndmask_b32_e64 v107, 0, 1.0, vcc
	v_cmp_eq_u32_e32 vcc, v193, v197
	s_nop 1
	v_cndmask_b32_e64 v106, 0, 1.0, vcc
	v_pk_fma_f32 v[90:91], v[90:91], v[108:109], v[106:107] op_sel_hi:[0,1,1] neg_lo:[1,0,0] neg_hi:[1,0,0]
	v_cvt_pk_bf16_f32 v93, v90, v91
	ds_write_b64 v186, v[92:93] offset:1632
	ds_read_b32 v90, v187 offset:160
	v_cmp_eq_u32_e32 vcc, v189, v198
	s_nop 1
	v_cndmask_b32_e64 v92, 0, 1.0, vcc
	v_cmp_eq_u32_e32 vcc, v190, v198
	s_nop 1
	v_cndmask_b32_e64 v93, 0, 1.0, vcc
	v_cmp_eq_u32_e32 vcc, v192, v198
	s_waitcnt lgkmcnt(0)
	v_pk_fma_f32 v[92:93], v[90:91], v[98:99], v[92:93] op_sel_hi:[0,1,1] neg_lo:[1,0,0] neg_hi:[1,0,0]
	v_cvt_pk_bf16_f32 v92, v92, v93
	v_cndmask_b32_e64 v99, 0, 1.0, vcc
	v_cmp_eq_u32_e32 vcc, v193, v198
	s_nop 1
	v_cndmask_b32_e64 v98, 0, 1.0, vcc
	v_pk_fma_f32 v[90:91], v[90:91], v[100:101], v[98:99] op_sel_hi:[0,1,1] neg_lo:[1,0,0] neg_hi:[1,0,0]
	v_cvt_pk_bf16_f32 v93, v90, v91
	ds_write_b64 v186, v[92:93] offset:2176
	ds_read_b32 v90, v187 offset:168
	v_cmp_eq_u32_e32 vcc, v189, v199
	s_nop 1
	v_cndmask_b32_e64 v92, 0, 1.0, vcc
	v_cmp_eq_u32_e32 vcc, v190, v199
	s_nop 1
	v_cndmask_b32_e64 v93, 0, 1.0, vcc
	v_cmp_eq_u32_e32 vcc, v192, v199
	s_waitcnt lgkmcnt(0)
	v_pk_fma_f32 v[92:93], v[90:91], v[94:95], v[92:93] op_sel_hi:[0,1,1] neg_lo:[1,0,0] neg_hi:[1,0,0]
	v_cvt_pk_bf16_f32 v92, v92, v93
	v_cndmask_b32_e64 v95, 0, 1.0, vcc
	v_cmp_eq_u32_e32 vcc, v193, v199
	s_nop 1
	v_cndmask_b32_e64 v94, 0, 1.0, vcc
	v_pk_fma_f32 v[90:91], v[90:91], v[96:97], v[94:95] op_sel_hi:[0,1,1] neg_lo:[1,0,0] neg_hi:[1,0,0]
	v_cvt_pk_bf16_f32 v93, v90, v91
	ds_write_b64 v186, v[92:93] offset:2720
	ds_read_b32 v90, v187 offset:176
	v_cmp_eq_u32_e32 vcc, v189, v200
	s_nop 1
	v_cndmask_b32_e64 v92, 0, 1.0, vcc
	v_cmp_eq_u32_e32 vcc, v190, v200
	s_nop 1
	v_cndmask_b32_e64 v93, 0, 1.0, vcc
	v_cmp_eq_u32_e32 vcc, v192, v200
	s_waitcnt lgkmcnt(0)
	v_pk_fma_f32 v[86:87], v[90:91], v[86:87], v[92:93] op_sel_hi:[0,1,1] neg_lo:[1,0,0] neg_hi:[1,0,0]
	v_cvt_pk_bf16_f32 v86, v86, v87
	v_cndmask_b32_e64 v93, 0, 1.0, vcc
	v_cmp_eq_u32_e32 vcc, v193, v200
	s_nop 1
	v_cndmask_b32_e64 v92, 0, 1.0, vcc
	v_pk_fma_f32 v[88:89], v[90:91], v[88:89], v[92:93] op_sel_hi:[0,1,1] neg_lo:[1,0,0] neg_hi:[1,0,0]
	v_cvt_pk_bf16_f32 v87, v88, v89
	ds_write_b64 v186, v[86:87] offset:3264
	ds_read_b32 v86, v187 offset:184
	v_cmp_eq_u32_e32 vcc, v189, v201
	s_nop 1
	v_cndmask_b32_e64 v88, 0, 1.0, vcc
	v_cmp_eq_u32_e32 vcc, v190, v201
	s_nop 1
	v_cndmask_b32_e64 v89, 0, 1.0, vcc
	v_cmp_eq_u32_e32 vcc, v192, v201
	s_waitcnt lgkmcnt(0)
	v_pk_fma_f32 v[82:83], v[86:87], v[82:83], v[88:89] op_sel_hi:[0,1,1] neg_lo:[1,0,0] neg_hi:[1,0,0]
	v_cvt_pk_bf16_f32 v82, v82, v83
	v_cndmask_b32_e64 v89, 0, 1.0, vcc
	v_cmp_eq_u32_e32 vcc, v193, v201
	s_nop 1
	v_cndmask_b32_e64 v88, 0, 1.0, vcc
	v_pk_fma_f32 v[84:85], v[86:87], v[84:85], v[88:89] op_sel_hi:[0,1,1] neg_lo:[1,0,0] neg_hi:[1,0,0]
	v_cvt_pk_bf16_f32 v83, v84, v85
	ds_write_b64 v186, v[82:83] offset:3808
	ds_read_b128 v[82:85], v1
	ds_read_b128 v[86:89], v1 offset:64
	ds_read_b128 v[90:93], v1 offset:128
	ds_read_b128 v[94:97], v1 offset:192
	v_lshl_add_u64 v[98:99], v[150:151], 0, s[0:1]
	v_lshl_add_u64 v[192:193], v[164:165], 0, s[0:1]
	v_lshl_add_u64 v[196:197], v[166:167], 0, s[0:1]
	v_lshl_add_u64 v[100:101], v[152:153], 0, s[0:1]
	v_lshl_add_u64 v[106:107], v[156:157], 0, s[0:1]
	v_lshl_add_u64 v[108:109], v[158:159], 0, s[0:1]
	v_lshl_add_u64 v[110:111], v[160:161], 0, s[0:1]
	v_lshl_add_u64 v[112:113], v[162:163], 0, s[0:1]
	global_load_dwordx4 v[118:121], v[98:99], off sc0 sc1 nt
	global_load_dwordx4 v[134:137], v[100:101], off sc0 sc1 nt
	global_load_dwordx4 v[150:153], v[106:107], off sc0 sc1 nt
	global_load_dwordx4 v[156:159], v[108:109], off sc0 sc1 nt
	global_load_dwordx4 v[160:163], v[110:111], off sc0 sc1 nt
	global_load_dwordx4 v[164:167], v[112:113], off sc0 sc1 nt
	s_nop 0
	global_load_dwordx4 v[192:195], v[192:193], off sc0 sc1 nt
	s_nop 0
	global_load_dwordx4 v[196:199], v[196:197], off sc0 sc1 nt
	v_mov_b32_e32 v98, v188
	s_waitcnt vmcnt(15)
	s_waitcnt vmcnt(14)
	s_waitcnt vmcnt(13)
	s_waitcnt vmcnt(12)
	s_waitcnt vmcnt(11)
	s_waitcnt vmcnt(10)
	s_waitcnt vmcnt(9)
	s_waitcnt vmcnt(8)
	ds_read_b32 v98, v187
	s_waitcnt lgkmcnt(0)
	v_pk_fma_f32 v[100:101], v[98:99], v[146:147], 0 op_sel_hi:[0,1,0] neg_lo:[1,0,0] neg_hi:[1,0,0]
	v_pk_fma_f32 v[98:99], v[98:99], v[148:149], 0 op_sel_hi:[0,1,0] neg_lo:[1,0,0] neg_hi:[1,0,0]
	v_cvt_pk_bf16_f32 v100, v100, v101
	v_cvt_pk_bf16_f32 v101, v98, v99
	ds_write_b64 v186, v[100:101]
	ds_read_b32 v98, v187 offset:8
	s_waitcnt lgkmcnt(0)
	v_pk_fma_f32 v[100:101], v[98:99], v[142:143], 0 op_sel_hi:[0,1,0] neg_lo:[1,0,0] neg_hi:[1,0,0]
	v_pk_fma_f32 v[98:99], v[98:99], v[144:145], 0 op_sel_hi:[0,1,0] neg_lo:[1,0,0] neg_hi:[1,0,0]
	v_cvt_pk_bf16_f32 v100, v100, v101
	v_cvt_pk_bf16_f32 v101, v98, v99
	ds_write_b64 v186, v[100:101] offset:544
	ds_read_b32 v98, v187 offset:16
	s_waitcnt lgkmcnt(0)
	v_pk_fma_f32 v[100:101], v[98:99], v[138:139], 0 op_sel_hi:[0,1,0] neg_lo:[1,0,0] neg_hi:[1,0,0]
	v_pk_fma_f32 v[98:99], v[98:99], v[140:141], 0 op_sel_hi:[0,1,0] neg_lo:[1,0,0] neg_hi:[1,0,0]
	v_cvt_pk_bf16_f32 v100, v100, v101
	v_cvt_pk_bf16_f32 v101, v98, v99
	ds_write_b64 v186, v[100:101] offset:1088
	ds_read_b32 v98, v187 offset:24
	s_waitcnt lgkmcnt(0)
	v_pk_fma_f32 v[100:101], v[98:99], v[130:131], 0 op_sel_hi:[0,1,0] neg_lo:[1,0,0] neg_hi:[1,0,0]
	v_pk_fma_f32 v[98:99], v[98:99], v[132:133], 0 op_sel_hi:[0,1,0] neg_lo:[1,0,0] neg_hi:[1,0,0]
	v_cvt_pk_bf16_f32 v100, v100, v101
	v_cvt_pk_bf16_f32 v101, v98, v99
	ds_write_b64 v186, v[100:101] offset:1632
	ds_read_b32 v98, v187 offset:32
	s_waitcnt lgkmcnt(0)
	v_pk_fma_f32 v[100:101], v[98:99], v[126:127], 0 op_sel_hi:[0,1,0] neg_lo:[1,0,0] neg_hi:[1,0,0]
	v_pk_fma_f32 v[98:99], v[98:99], v[128:129], 0 op_sel_hi:[0,1,0] neg_lo:[1,0,0] neg_hi:[1,0,0]
	v_cvt_pk_bf16_f32 v100, v100, v101
	v_cvt_pk_bf16_f32 v101, v98, v99
	ds_write_b64 v186, v[100:101] offset:2176
	ds_read_b32 v98, v187 offset:40
	s_waitcnt lgkmcnt(0)
	v_pk_fma_f32 v[100:101], v[98:99], v[122:123], 0 op_sel_hi:[0,1,0] neg_lo:[1,0,0] neg_hi:[1,0,0]
	v_pk_fma_f32 v[98:99], v[98:99], v[124:125], 0 op_sel_hi:[0,1,0] neg_lo:[1,0,0] neg_hi:[1,0,0]
	v_cvt_pk_bf16_f32 v100, v100, v101
	v_cvt_pk_bf16_f32 v101, v98, v99
	ds_write_b64 v186, v[100:101] offset:2720
	ds_read_b32 v98, v187 offset:48
	s_waitcnt lgkmcnt(0)
	v_pk_fma_f32 v[100:101], v[98:99], v[114:115], 0 op_sel_hi:[0,1,0] neg_lo:[1,0,0] neg_hi:[1,0,0]
	v_pk_fma_f32 v[98:99], v[98:99], v[116:117], 0 op_sel_hi:[0,1,0] neg_lo:[1,0,0] neg_hi:[1,0,0]
	v_cvt_pk_bf16_f32 v100, v100, v101
	v_cvt_pk_bf16_f32 v101, v98, v99
	ds_write_b64 v186, v[100:101] offset:3264
	ds_read_b32 v98, v187 offset:56
	s_waitcnt lgkmcnt(0)
	v_pk_fma_f32 v[100:101], v[98:99], v[102:103], 0 op_sel_hi:[0,1,0] neg_lo:[1,0,0] neg_hi:[1,0,0]
	v_pk_fma_f32 v[98:99], v[98:99], v[104:105], 0 op_sel_hi:[0,1,0] neg_lo:[1,0,0] neg_hi:[1,0,0]
	v_cvt_pk_bf16_f32 v100, v100, v101
	v_cvt_pk_bf16_f32 v101, v98, v99
	ds_write_b64 v186, v[100:101] offset:3808
	ds_read_b128 v[98:101], v1
	ds_read_b128 v[102:105], v1 offset:64
	ds_read_b128 v[106:109], v1 offset:128
	ds_read_b128 v[110:113], v1 offset:192
	v_lshl_add_u64 v[114:115], v[168:169], 0, s[0:1]
	v_lshl_add_u64 v[126:127], v[176:177], 0, s[0:1]
	v_lshl_add_u64 v[176:177], v[180:181], 0, s[0:1]
	v_lshl_add_u64 v[180:181], v[182:183], 0, s[0:1]
	v_lshl_add_u64 v[116:117], v[170:171], 0, s[0:1]
	v_lshl_add_u64 v[122:123], v[172:173], 0, s[0:1]
	v_lshl_add_u64 v[124:125], v[174:175], 0, s[0:1]
	v_lshl_add_u64 v[128:129], v[178:179], 0, s[0:1]
	global_load_dwordx4 v[130:133], v[114:115], off sc0 sc1 nt
	global_load_dwordx4 v[138:141], v[116:117], off sc0 sc1 nt
	global_load_dwordx4 v[142:145], v[122:123], off sc0 sc1 nt
	global_load_dwordx4 v[146:149], v[124:125], off sc0 sc1 nt
	global_load_dwordx4 v[168:171], v[126:127], off sc0 sc1 nt
	global_load_dwordx4 v[172:175], v[128:129], off sc0 sc1 nt
	s_nop 0
	global_load_dwordx4 v[176:179], v[176:177], off sc0 sc1 nt
	s_nop 0
	global_load_dwordx4 v[180:183], v[180:181], off sc0 sc1 nt
	v_mov_b32_e32 v114, v188
	s_waitcnt vmcnt(15)
	s_waitcnt vmcnt(14)
	s_waitcnt vmcnt(13)
	s_waitcnt vmcnt(12)
	s_waitcnt vmcnt(11)
	s_waitcnt vmcnt(10)
	s_waitcnt vmcnt(9)
	s_waitcnt vmcnt(8)
	ds_read_b32 v114, v187 offset:64
	s_waitcnt lgkmcnt(0)
	v_pk_fma_f32 v[116:117], v[114:115], v[118:119], 0 op_sel_hi:[0,1,0] neg_lo:[1,0,0] neg_hi:[1,0,0]
	v_pk_fma_f32 v[114:115], v[114:115], v[120:121], 0 op_sel_hi:[0,1,0] neg_lo:[1,0,0] neg_hi:[1,0,0]
	v_cvt_pk_bf16_f32 v116, v116, v117
	v_cvt_pk_bf16_f32 v117, v114, v115
	ds_write_b64 v186, v[116:117]
	ds_read_b32 v114, v187 offset:72
	s_waitcnt lgkmcnt(0)
	v_pk_fma_f32 v[116:117], v[114:115], v[134:135], 0 op_sel_hi:[0,1,0] neg_lo:[1,0,0] neg_hi:[1,0,0]
	v_pk_fma_f32 v[114:115], v[114:115], v[136:137], 0 op_sel_hi:[0,1,0] neg_lo:[1,0,0] neg_hi:[1,0,0]
	v_cvt_pk_bf16_f32 v116, v116, v117
	v_cvt_pk_bf16_f32 v117, v114, v115
	ds_write_b64 v186, v[116:117] offset:544
	ds_read_b32 v114, v187 offset:80
	s_waitcnt lgkmcnt(0)
	v_pk_fma_f32 v[116:117], v[114:115], v[150:151], 0 op_sel_hi:[0,1,0] neg_lo:[1,0,0] neg_hi:[1,0,0]
	v_pk_fma_f32 v[114:115], v[114:115], v[152:153], 0 op_sel_hi:[0,1,0] neg_lo:[1,0,0] neg_hi:[1,0,0]
	v_cvt_pk_bf16_f32 v116, v116, v117
	v_cvt_pk_bf16_f32 v117, v114, v115
	ds_write_b64 v186, v[116:117] offset:1088
	ds_read_b32 v114, v187 offset:88
	s_waitcnt lgkmcnt(0)
	v_pk_fma_f32 v[116:117], v[114:115], v[156:157], 0 op_sel_hi:[0,1,0] neg_lo:[1,0,0] neg_hi:[1,0,0]
	v_pk_fma_f32 v[114:115], v[114:115], v[158:159], 0 op_sel_hi:[0,1,0] neg_lo:[1,0,0] neg_hi:[1,0,0]
	v_cvt_pk_bf16_f32 v116, v116, v117
	v_cvt_pk_bf16_f32 v117, v114, v115
	ds_write_b64 v186, v[116:117] offset:1632
	ds_read_b32 v114, v187 offset:96
	s_waitcnt lgkmcnt(0)
	v_pk_fma_f32 v[116:117], v[114:115], v[160:161], 0 op_sel_hi:[0,1,0] neg_lo:[1,0,0] neg_hi:[1,0,0]
	v_pk_fma_f32 v[114:115], v[114:115], v[162:163], 0 op_sel_hi:[0,1,0] neg_lo:[1,0,0] neg_hi:[1,0,0]
	v_cvt_pk_bf16_f32 v116, v116, v117
	v_cvt_pk_bf16_f32 v117, v114, v115
	ds_write_b64 v186, v[116:117] offset:2176
	ds_read_b32 v114, v187 offset:104
	s_waitcnt lgkmcnt(0)
	v_pk_fma_f32 v[116:117], v[114:115], v[164:165], 0 op_sel_hi:[0,1,0] neg_lo:[1,0,0] neg_hi:[1,0,0]
	v_pk_fma_f32 v[114:115], v[114:115], v[166:167], 0 op_sel_hi:[0,1,0] neg_lo:[1,0,0] neg_hi:[1,0,0]
	v_cvt_pk_bf16_f32 v116, v116, v117
	v_cvt_pk_bf16_f32 v117, v114, v115
	ds_write_b64 v186, v[116:117] offset:2720
	ds_read_b32 v114, v187 offset:112
	s_waitcnt lgkmcnt(0)
	v_pk_fma_f32 v[116:117], v[114:115], v[192:193], 0 op_sel_hi:[0,1,0] neg_lo:[1,0,0] neg_hi:[1,0,0]
	v_pk_fma_f32 v[114:115], v[114:115], v[194:195], 0 op_sel_hi:[0,1,0] neg_lo:[1,0,0] neg_hi:[1,0,0]
	v_cvt_pk_bf16_f32 v116, v116, v117
	v_cvt_pk_bf16_f32 v117, v114, v115
	ds_write_b64 v186, v[116:117] offset:3264
	ds_read_b32 v114, v187 offset:120
	s_waitcnt lgkmcnt(0)
	v_pk_fma_f32 v[116:117], v[114:115], v[196:197], 0 op_sel_hi:[0,1,0] neg_lo:[1,0,0] neg_hi:[1,0,0]
	v_pk_fma_f32 v[114:115], v[114:115], v[198:199], 0 op_sel_hi:[0,1,0] neg_lo:[1,0,0] neg_hi:[1,0,0]
	v_cvt_pk_bf16_f32 v116, v116, v117
	v_cvt_pk_bf16_f32 v117, v114, v115
	ds_write_b64 v186, v[116:117] offset:3808
	ds_read_b128 v[114:117], v1
	ds_read_b128 v[118:121], v1 offset:64
	ds_read_b128 v[122:125], v1 offset:128
	ds_read_b128 v[126:129], v1 offset:192
	s_waitcnt vmcnt(7)
	s_waitcnt vmcnt(6)
	s_waitcnt vmcnt(5)
	s_waitcnt vmcnt(4)
	s_waitcnt vmcnt(3)
	s_waitcnt vmcnt(2)
	s_waitcnt vmcnt(1)
	s_waitcnt vmcnt(0)
	ds_read_b32 v134, v187 offset:128
	s_waitcnt lgkmcnt(0)
	v_pk_fma_f32 v[130:131], v[134:135], v[130:131], 0 op_sel_hi:[0,1,0] neg_lo:[1,0,0] neg_hi:[1,0,0]
	v_pk_fma_f32 v[132:133], v[134:135], v[132:133], 0 op_sel_hi:[0,1,0] neg_lo:[1,0,0] neg_hi:[1,0,0]
	v_cvt_pk_bf16_f32 v130, v130, v131
	v_cvt_pk_bf16_f32 v131, v132, v133
	ds_write_b64 v186, v[130:131]
	ds_read_b32 v130, v187 offset:136
	s_waitcnt lgkmcnt(0)
	v_pk_fma_f32 v[132:133], v[130:131], v[138:139], 0 op_sel_hi:[0,1,0] neg_lo:[1,0,0] neg_hi:[1,0,0]
	v_pk_fma_f32 v[130:131], v[130:131], v[140:141], 0 op_sel_hi:[0,1,0] neg_lo:[1,0,0] neg_hi:[1,0,0]
	v_cvt_pk_bf16_f32 v132, v132, v133
	v_cvt_pk_bf16_f32 v133, v130, v131
	ds_write_b64 v186, v[132:133] offset:544
	ds_read_b32 v130, v187 offset:144
	s_waitcnt lgkmcnt(0)
	v_pk_fma_f32 v[132:133], v[130:131], v[142:143], 0 op_sel_hi:[0,1,0] neg_lo:[1,0,0] neg_hi:[1,0,0]
	v_pk_fma_f32 v[130:131], v[130:131], v[144:145], 0 op_sel_hi:[0,1,0] neg_lo:[1,0,0] neg_hi:[1,0,0]
	v_cvt_pk_bf16_f32 v132, v132, v133
	v_cvt_pk_bf16_f32 v133, v130, v131
	ds_write_b64 v186, v[132:133] offset:1088
	ds_read_b32 v130, v187 offset:152
	s_waitcnt lgkmcnt(0)
	v_pk_fma_f32 v[132:133], v[130:131], v[146:147], 0 op_sel_hi:[0,1,0] neg_lo:[1,0,0] neg_hi:[1,0,0]
	v_pk_fma_f32 v[130:131], v[130:131], v[148:149], 0 op_sel_hi:[0,1,0] neg_lo:[1,0,0] neg_hi:[1,0,0]
	v_cvt_pk_bf16_f32 v132, v132, v133
	v_cvt_pk_bf16_f32 v133, v130, v131
	ds_write_b64 v186, v[132:133] offset:1632
	ds_read_b32 v130, v187 offset:160
	s_waitcnt lgkmcnt(0)
	v_pk_fma_f32 v[132:133], v[130:131], v[168:169], 0 op_sel_hi:[0,1,0] neg_lo:[1,0,0] neg_hi:[1,0,0]
	v_pk_fma_f32 v[130:131], v[130:131], v[170:171], 0 op_sel_hi:[0,1,0] neg_lo:[1,0,0] neg_hi:[1,0,0]
	v_cvt_pk_bf16_f32 v132, v132, v133
	v_cvt_pk_bf16_f32 v133, v130, v131
	ds_write_b64 v186, v[132:133] offset:2176
	ds_read_b32 v130, v187 offset:168
	s_waitcnt lgkmcnt(0)
	v_pk_fma_f32 v[132:133], v[130:131], v[172:173], 0 op_sel_hi:[0,1,0] neg_lo:[1,0,0] neg_hi:[1,0,0]
	v_pk_fma_f32 v[130:131], v[130:131], v[174:175], 0 op_sel_hi:[0,1,0] neg_lo:[1,0,0] neg_hi:[1,0,0]
	v_cvt_pk_bf16_f32 v132, v132, v133
	v_cvt_pk_bf16_f32 v133, v130, v131
	ds_write_b64 v186, v[132:133] offset:2720
	ds_read_b32 v130, v187 offset:176
	s_waitcnt lgkmcnt(0)
	v_pk_fma_f32 v[132:133], v[130:131], v[176:177], 0 op_sel_hi:[0,1,0] neg_lo:[1,0,0] neg_hi:[1,0,0]
	v_pk_fma_f32 v[130:131], v[130:131], v[178:179], 0 op_sel_hi:[0,1,0] neg_lo:[1,0,0] neg_hi:[1,0,0]
	v_cvt_pk_bf16_f32 v132, v132, v133
	v_cvt_pk_bf16_f32 v133, v130, v131
	ds_write_b64 v186, v[132:133] offset:3264
	ds_read_b32 v130, v187 offset:184
	s_waitcnt lgkmcnt(0)
	v_pk_fma_f32 v[132:133], v[130:131], v[180:181], 0 op_sel_hi:[0,1,0] neg_lo:[1,0,0] neg_hi:[1,0,0]
	v_pk_fma_f32 v[130:131], v[130:131], v[182:183], 0 op_sel_hi:[0,1,0] neg_lo:[1,0,0] neg_hi:[1,0,0]
	v_cvt_pk_bf16_f32 v132, v132, v133
	v_cvt_pk_bf16_f32 v133, v130, v131
	ds_write_b64 v186, v[132:133] offset:3808
	ds_read_b128 v[130:133], v1
	ds_read_b128 v[134:137], v1 offset:64
	ds_read_b128 v[138:141], v1 offset:128
	ds_read_b128 v[142:145], v1 offset:192
	s_ashr_i32 s7, s6, 31
	s_lshl_b64 s[0:1], s[6:7], 2
	s_add_u32 s0, s4, s0
	s_addc_u32 s1, s5, s1
	v_lshlrev_b32_e32 v1, 4, v0
	s_add_i32 s20, s34, 1
	s_add_i32 s34, s34, -1
	v_or_b32_e32 v153, s10, v206
	s_xor_b32 s26, s3, 2
	s_lshl_b64 s[10:11], s[10:11], 3
	s_and_b32 s20, s20, 3
	s_and_b32 s27, s34, 3
	s_add_u32 s10, s14, s10
	s_addc_u32 s11, s15, s11
	s_lshl_b32 s42, s35, 2
	s_add_i32 s41, s42, 0x26a20
	s_add_i32 s42, s42, 0x26a00
	v_lshlrev_b32_e32 v190, 3, v206
	s_cmp_eq_u32 s35, 3
	v_lshlrev_b32_e32 v150, 3, v0
	v_and_b32_e32 v151, 1, v0
	v_lshl_add_u64 v[0:1], v[154:155], 3, s[14:15]
	v_lshl_add_u64 v[192:193], s[10:11], 0, v[190:191]
	s_cselect_b64 s[10:11], -1, 0
	s_lshl_b32 s14, s3, 2
	s_add_u32 s24, s16, s14
	v_or_b32_e32 v155, 0x20000, v150
	v_add_u32_e32 v156, 0x20880, v150
	v_lshlrev_b32_e32 v150, 1, v153
	s_addc_u32 s25, s17, 0
	s_lshl_b32 s43, s3, 9
	v_lshl_add_u32 v212, s26, 9, v150
	s_lshl_b32 s15, s26, 8
	s_add_i32 s26, s43, 0x200
	v_mov_b32_e32 v152, 0x880
	v_cmp_lt_u32_e64 s[0:1], 15, v206
	v_cmp_eq_u32_e32 vcc, 1, v151
	s_and_b32 s45, s26, 0x600
	s_add_i32 s26, s43, 0x500
	v_cndmask_b32_e32 v211, 0, v152, vcc
	s_and_b32 s56, s26, 0x700
	s_add_i32 s26, s43, 0x540
	v_lshl_add_u32 v213, s20, 9, v150
	v_lshl_add_u32 v214, s27, 9, v150
	s_and_b32 s57, s26, 0x740
	s_add_i32 s26, s43, 0x580
	s_and_b32 s58, s26, 0x780
	s_add_i32 s26, s43, 0x5c0
	s_and_b32 s59, s26, 0x7c0
	s_add_i32 s26, s43, 0x600
	s_and_b32 s60, s26, 0x600
	s_add_i32 s26, s43, 0x640
	s_and_b32 s61, s26, 0x640
	s_add_i32 s26, s43, 0x680
	s_and_b32 s62, s26, 0x680
	s_add_i32 s26, s43, 0x6c0
	s_and_b32 s63, s26, 0x6c0
	s_add_i32 s26, s43, 0x700
	s_and_b32 s64, s26, 0x700
	s_add_i32 s26, s43, 0x740
	s_and_b32 s65, s26, 0x740
	s_add_i32 s26, s43, 0x780
	s_lshl_b32 s14, s27, 8
	s_lshl_b32 s20, s20, 8
	s_add_i32 s27, s43, 0x240
	s_add_i32 s28, s43, 0x280
	s_add_i32 s29, s43, 0x2c0
	s_add_i32 s30, s43, 0x300
	s_add_i32 s31, s43, 0x340
	s_add_i32 s34, s43, 0x380
	s_add_i32 s35, s43, 0x3c0
	s_add_i32 s36, s43, 0x440
	s_add_i32 s37, s43, 0x480
	s_add_i32 s38, s43, 0x4c0
	s_and_b32 s66, s26, 0x780
	s_add_i32 s26, s43, 0x7c0
	s_mul_hi_i32 s23, s18, 0x65
	s_mul_i32 s22, s18, 0x65
	v_cmp_eq_u32_e64 s[4:5], 1, v185
	v_cmp_eq_u32_e64 s[6:7], 2, v185
	v_cmp_eq_u32_e64 s[8:9], 63, v206
	s_xor_b32 s44, s43, 0x400
	s_and_b32 s46, s27, 0x640
	s_and_b32 s47, s28, 0x680
	s_waitcnt lgkmcnt(0)
	v_mov_b32_e32 v146, 0x20000
	s_and_b32 s48, s29, 0x6c0
	s_and_b32 s49, s30, 0x700
	s_and_b32 s50, s31, 0x740
	s_and_b32 s51, s34, 0x780
	s_and_b32 s52, s35, 0x7c0
	s_and_b32 s53, s36, 0x640
	s_and_b32 s54, s37, 0x680
	s_and_b32 s55, s38, 0x6c0
	s_and_b32 s67, s26, 0x7c0
	s_and_b64 s[26:27], s[10:11], s[12:13]
	v_lshl_add_u32 v215, v154, 1, v146
	v_mov_b32_e32 v216, 1
	s_lshl_b32 s28, s14, 3
	s_lshl_b32 s30, s15, 3
	s_lshl_b32 s34, s20, 3
	s_movk_i32 s68, 0x7fff
	s_mov_b32 s69, 0
	v_and_b32_e32 v220, 24, v206
	v_lshlrev_b32_e32 v220, 2, v220
	v_and_b32_e32 v221, 2, v206
	v_lshl_or_b32 v220, v221, 3, v220
	v_and_b32_e32 v221, 32, v206
	v_lshrrev_b32_e32 v221, 2, v221
	v_or_b32_e32 v220, v220, v221
	v_and_b32_e32 v221, 4, v206
	v_or_b32_e32 v220, v220, v221
	v_and_b32_e32 v221, 1, v206
	v_lshl_or_b32 v220, v221, 1, v220
	v_mov_b32_e32 v220, v254
	s_lshr_b32 s76, s19, 8
	s_add_i32 s76, s76, 0x20000
	v_add_u32_e32 v220, s76, v220
	v_add_u32_e32 v225, s45, v220
	v_add_u32_e32 v226, s44, v220
	v_add_u32_e32 v227, s60, v220
	v_add_u32_e32 v228, s43, v220
	v_and_b32_e32 v221, 1, v206
	v_mul_u32_u24_e32 v221, 0x880, v221
	v_lshrrev_b32_e32 v220, 4, v206
	v_lshl_add_u32 v221, v220, 5, v221
	v_and_b32_e32 v220, 2, v206
	v_lshl_add_u32 v221, v220, 3, v221
	v_add_u32_e32 v222, 0x20000, v221
	v_cmp_ne_u32_e32 vcc, 0, v220
	v_mov_b32_e32 v220, 0x44444444
	v_mov_b32_e32 v221, 0xeeeeeeee
	s_nop 1
	v_cndmask_b32_e32 v223, v220, v221, vcc
	v_cmp_lt_u32_e64 s[74:75], 47, v206
	s_lshr_b32 s82, s19, 15
	s_mul_i32 s83, s82, 0x1100
	s_add_i32 s83, s83, 0x22200
	v_lshl_add_u32 v254, v206, 2, s83
	v_mov_b32_e32 v220, s41
	s_nop 1
	v_cndmask_b32_e64 v254, v254, v220, s[12:13]
	v_mov_b32_e32 v224, v184
	s_mov_b32 s86, 0x55555555
	s_mov_b32 s87, 0x55555555
	s_lshr_b32 s78, s19, 15
	s_lshl_b32 s79, s78, 11
	v_add_u32_e32 v255, s79, v224
	ds_read_b128 v[166:169], v224 offset:0
	ds_read_b128 v[170:173], v224 offset:1024
	ds_read_b128 v[174:177], v224 offset:2048
	ds_read_b128 v[178:181], v224 offset:3072
	ds_read_b128 v[182:185], v224 offset:4096
	ds_read_b128 v[186:189], v224 offset:5120
	s_mov_b32 s20, 0
